# one idle slot (s_nop 0) before the first MFMA of each block after the opening barrier, so the partner wave's trailing MFMA issues first
# speedup vs baseline: 1.0020x; 1.0020x over previous
.LBB0_575:
	s_add_i32 s28, s6, s77
	s_add_i32 s26, s28, 1
	s_cmp_ge_i32 s26, s52
	s_cselect_b32 s27, s52, 0
	s_sub_i32 s26, s26, s27
	s_ashr_i32 s27, s26, 31
	s_lshl_b64 s[78:79], s[26:27], s41
	s_add_i32 s28, s28, 2
	s_cmp_ge_i32 s28, s52
	s_cselect_b32 s26, s52, 0
	s_sub_i32 s26, s28, s26
	s_ashr_i32 s27, s26, 31
	s_lshl_b64 s[26:27], s[26:27], s41
	v_add_u32_e32 v148, s7, v155
	v_add_u32_e32 v152, s44, v155
	s_add_u32 s28, s22, s26
	ds_read_b128 v[136:139], v148
	ds_read_b128 v[140:143], v148 offset:1024
	ds_read_b128 v[144:147], v148 offset:2048
	ds_read_b128 v[148:151], v148 offset:3072
	ds_read_b128 v[158:161], v152
	ds_read_b128 v[172:175], v152 offset:1024
	ds_read_b128 v[176:179], v152 offset:2048
	ds_read_b128 v[180:183], v152 offset:3072
	s_addc_u32 s29, s23, s27
	s_add_u32 s26, s24, s26
	s_addc_u32 s27, s25, s27
	s_cmp_eq_u32 s53, s77
	s_cselect_b32 s30, s73, s28
	s_cselect_b32 s31, s74, s29
	s_cselect_b32 s29, s76, s27
	s_cselect_b32 s28, s75, s26
	s_add_u32 s26, s30, s54
	s_addc_u32 s27, s31, 0
	s_add_u32 s78, s71, s78
	s_addc_u32 s79, s72, s79
	s_add_i32 m0, s47, 0xc000
	ds_read_b128 v[184:187], v157
	ds_read_b128 v[188:191], v157 offset:1024
	ds_read_b128 v[192:195], v157 offset:2048
	ds_read_b128 v[196:199], v157 offset:3072
	ds_read_b128 v[212:215], v157 offset:4096
	ds_read_b128 v[216:219], v157 offset:5120
	ds_read_b128 v[220:223], v157 offset:6144
	ds_read_b128 v[224:227], v157 offset:7168
	global_load_lds_dwordx4 v130, s[78:79]
	s_add_i32 m0, s47, 0xe000
	s_nop 0
	global_load_lds_dwordx4 v132, s[78:79]
	s_waitcnt vmcnt(8)
	s_waitcnt lgkmcnt(0)
	s_barrier
	s_setprio 1
	s_waitcnt lgkmcnt(0)
	s_nop 0
	v_mfma_f32_16x16x32_bf16 v[126:129], v[136:139], v[184:187], v[126:129]
	v_mfma_f32_16x16x32_bf16 v[122:125], v[144:147], v[184:187], v[122:125]
	v_mfma_f32_16x16x32_bf16 v[110:113], v[136:139], v[192:195], v[110:113]
	v_mfma_f32_16x16x32_bf16 v[106:109], v[144:147], v[192:195], v[106:109]
	v_mfma_f32_16x16x32_bf16 v[94:97], v[136:139], v[212:215], v[94:97]
	v_mfma_f32_16x16x32_bf16 v[90:93], v[144:147], v[212:215], v[90:93]
	v_mfma_f32_16x16x32_bf16 v[78:81], v[136:139], v[220:223], v[78:81]
	v_mfma_f32_16x16x32_bf16 v[74:77], v[144:147], v[220:223], v[74:77]
	v_mfma_f32_16x16x32_bf16 v[126:129], v[140:143], v[188:191], v[126:129]
	v_mfma_f32_16x16x32_bf16 v[122:125], v[148:151], v[188:191], v[122:125]
	v_mfma_f32_16x16x32_bf16 v[110:113], v[140:143], v[196:199], v[110:113]
	v_mfma_f32_16x16x32_bf16 v[106:109], v[148:151], v[196:199], v[106:109]
	v_mfma_f32_16x16x32_bf16 v[94:97], v[140:143], v[216:219], v[94:97]
	v_mfma_f32_16x16x32_bf16 v[90:93], v[148:151], v[216:219], v[90:93]
	v_mfma_f32_16x16x32_bf16 v[78:81], v[140:143], v[224:227], v[78:81]
	v_mfma_f32_16x16x32_bf16 v[74:77], v[148:151], v[224:227], v[74:77]
	s_setprio 0
	s_setprio 1
	v_mfma_f32_16x16x32_bf16 v[118:121], v[158:161], v[184:187], v[118:121]
	v_mfma_f32_16x16x32_bf16 v[114:117], v[176:179], v[184:187], v[114:117]
	v_mfma_f32_16x16x32_bf16 v[102:105], v[158:161], v[192:195], v[102:105]
	v_mfma_f32_16x16x32_bf16 v[98:101], v[176:179], v[192:195], v[98:101]
	v_mfma_f32_16x16x32_bf16 v[86:89], v[158:161], v[212:215], v[86:89]
	v_mfma_f32_16x16x32_bf16 v[82:85], v[176:179], v[212:215], v[82:85]
	v_mfma_f32_16x16x32_bf16 v[70:73], v[158:161], v[220:223], v[70:73]
	v_mfma_f32_16x16x32_bf16 v[66:69], v[176:179], v[220:223], v[66:69]
	v_mfma_f32_16x16x32_bf16 v[118:121], v[172:175], v[188:191], v[118:121]
	v_mfma_f32_16x16x32_bf16 v[114:117], v[180:183], v[188:191], v[114:117]
	v_mfma_f32_16x16x32_bf16 v[102:105], v[172:175], v[196:199], v[102:105]
	v_mfma_f32_16x16x32_bf16 v[98:101], v[180:183], v[196:199], v[98:101]
	v_mfma_f32_16x16x32_bf16 v[86:89], v[172:175], v[216:219], v[86:89]
	v_mfma_f32_16x16x32_bf16 v[82:85], v[180:183], v[216:219], v[82:85]
	v_mfma_f32_16x16x32_bf16 v[70:73], v[172:175], v[224:227], v[70:73]
	s_barrier
	v_mfma_f32_16x16x32_bf16 v[66:69], v[180:183], v[224:227], v[66:69]
	s_setprio 0
	s_mov_b32 m0, s42
	s_add_u32 s78, s28, s40
	ds_read_b128 v[184:187], v157 offset:16384
	ds_read_b128 v[188:191], v157 offset:17408
	ds_read_b128 v[192:195], v157 offset:18432
	ds_read_b128 v[196:199], v157 offset:19456
	ds_read_b128 v[212:215], v157 offset:20480
	ds_read_b128 v[216:219], v157 offset:21504
	ds_read_b128 v[220:223], v157 offset:22528
	ds_read_b128 v[224:227], v157 offset:23552
	global_load_lds_dwordx4 v0, s[28:29]
	s_mov_b32 m0, s43
	s_addc_u32 s79, s29, 0
	global_load_lds_dwordx4 v134, s[28:29]
	s_mov_b32 m0, s45
	s_nop 0
	global_load_lds_dwordx4 v0, s[78:79]
	s_mov_b32 m0, s46
	s_nop 0
	global_load_lds_dwordx4 v134, s[78:79]
	s_mov_b32 m0, s47
	s_nop 0
	global_load_lds_dwordx4 v130, s[30:31]
	s_mov_b32 m0, s48
	s_nop 0
	global_load_lds_dwordx4 v132, s[30:31]
	s_waitcnt vmcnt(8)
	s_waitcnt lgkmcnt(0)
	s_barrier
	s_setprio 1
	s_waitcnt lgkmcnt(0)
	s_nop 0
	v_mfma_f32_16x16x32_bf16 v[62:65], v[136:139], v[184:187], v[62:65]
	v_mfma_f32_16x16x32_bf16 v[58:61], v[144:147], v[184:187], v[58:61]
	v_mfma_f32_16x16x32_bf16 v[46:49], v[136:139], v[192:195], v[46:49]
	v_mfma_f32_16x16x32_bf16 v[42:45], v[144:147], v[192:195], v[42:45]
	v_mfma_f32_16x16x32_bf16 v[30:33], v[136:139], v[212:215], v[30:33]
	v_mfma_f32_16x16x32_bf16 v[26:29], v[144:147], v[212:215], v[26:29]
	v_mfma_f32_16x16x32_bf16 v[14:17], v[136:139], v[220:223], v[14:17]
	v_mfma_f32_16x16x32_bf16 v[10:13], v[144:147], v[220:223], v[10:13]
	v_mfma_f32_16x16x32_bf16 v[62:65], v[140:143], v[188:191], v[62:65]
	v_mfma_f32_16x16x32_bf16 v[58:61], v[148:151], v[188:191], v[58:61]
	v_mfma_f32_16x16x32_bf16 v[46:49], v[140:143], v[196:199], v[46:49]
	v_mfma_f32_16x16x32_bf16 v[42:45], v[148:151], v[196:199], v[42:45]
	v_mfma_f32_16x16x32_bf16 v[30:33], v[140:143], v[216:219], v[30:33]
	v_mfma_f32_16x16x32_bf16 v[26:29], v[148:151], v[216:219], v[26:29]
	v_mfma_f32_16x16x32_bf16 v[14:17], v[140:143], v[224:227], v[14:17]
	v_mfma_f32_16x16x32_bf16 v[10:13], v[148:151], v[224:227], v[10:13]
	s_setprio 0
	s_setprio 1
	v_mfma_f32_16x16x32_bf16 v[54:57], v[158:161], v[184:187], v[54:57]
	v_mfma_f32_16x16x32_bf16 v[50:53], v[176:179], v[184:187], v[50:53]
	v_mfma_f32_16x16x32_bf16 v[38:41], v[158:161], v[192:195], v[38:41]
	v_mfma_f32_16x16x32_bf16 v[34:37], v[176:179], v[192:195], v[34:37]
	v_mfma_f32_16x16x32_bf16 v[22:25], v[158:161], v[212:215], v[22:25]
	v_mfma_f32_16x16x32_bf16 v[18:21], v[176:179], v[212:215], v[18:21]
	v_mfma_f32_16x16x32_bf16 v[6:9], v[158:161], v[220:223], v[6:9]
	v_mfma_f32_16x16x32_bf16 v[2:5], v[176:179], v[220:223], v[2:5]
	v_mfma_f32_16x16x32_bf16 v[54:57], v[172:175], v[188:191], v[54:57]
	v_mfma_f32_16x16x32_bf16 v[50:53], v[180:183], v[188:191], v[50:53]
	v_mfma_f32_16x16x32_bf16 v[38:41], v[172:175], v[196:199], v[38:41]
	v_mfma_f32_16x16x32_bf16 v[34:37], v[180:183], v[196:199], v[34:37]
	v_mfma_f32_16x16x32_bf16 v[22:25], v[172:175], v[216:219], v[22:25]
	v_mfma_f32_16x16x32_bf16 v[18:21], v[180:183], v[216:219], v[18:21]
	v_mfma_f32_16x16x32_bf16 v[6:9], v[172:175], v[224:227], v[6:9]
	s_barrier
	v_mfma_f32_16x16x32_bf16 v[2:5], v[180:183], v[224:227], v[2:5]
	s_setprio 0
	v_add_u32_e32 v148, s55, v155
	v_add_u32_e32 v152, s60, v155
	ds_read_b128 v[136:139], v148
	ds_read_b128 v[140:143], v148 offset:1024
	ds_read_b128 v[144:147], v148 offset:2048
	ds_read_b128 v[148:151], v148 offset:3072
	ds_read_b128 v[158:161], v152
	ds_read_b128 v[172:175], v152 offset:1024
	ds_read_b128 v[176:179], v152 offset:2048
	ds_read_b128 v[180:183], v152 offset:3072
	s_add_u32 s30, s30, s40
	s_addc_u32 s31, s31, 0
	s_mov_b32 m0, s49
	ds_read_b128 v[184:187], v157 offset:32768
	ds_read_b128 v[188:191], v157 offset:33792
	ds_read_b128 v[192:195], v157 offset:34816
	ds_read_b128 v[196:199], v157 offset:35840
	ds_read_b128 v[212:215], v157 offset:36864
	ds_read_b128 v[216:219], v157 offset:37888
	ds_read_b128 v[220:223], v157 offset:38912
	ds_read_b128 v[224:227], v157 offset:39936
	global_load_lds_dwordx4 v130, s[30:31]
	s_mov_b32 m0, s50
	s_nop 0
	global_load_lds_dwordx4 v132, s[30:31]
	s_waitcnt vmcnt(8)
	s_waitcnt lgkmcnt(0)
	s_barrier
	s_setprio 1
	s_waitcnt lgkmcnt(0)
	s_nop 0
	v_mfma_f32_16x16x32_bf16 v[126:129], v[136:139], v[184:187], v[126:129]
	v_mfma_f32_16x16x32_bf16 v[122:125], v[144:147], v[184:187], v[122:125]
	v_mfma_f32_16x16x32_bf16 v[110:113], v[136:139], v[192:195], v[110:113]
	v_mfma_f32_16x16x32_bf16 v[106:109], v[144:147], v[192:195], v[106:109]
	v_mfma_f32_16x16x32_bf16 v[94:97], v[136:139], v[212:215], v[94:97]
	v_mfma_f32_16x16x32_bf16 v[90:93], v[144:147], v[212:215], v[90:93]
	v_mfma_f32_16x16x32_bf16 v[78:81], v[136:139], v[220:223], v[78:81]
	v_mfma_f32_16x16x32_bf16 v[74:77], v[144:147], v[220:223], v[74:77]
	v_mfma_f32_16x16x32_bf16 v[126:129], v[140:143], v[188:191], v[126:129]
	v_mfma_f32_16x16x32_bf16 v[122:125], v[148:151], v[188:191], v[122:125]
	v_mfma_f32_16x16x32_bf16 v[110:113], v[140:143], v[196:199], v[110:113]
	v_mfma_f32_16x16x32_bf16 v[106:109], v[148:151], v[196:199], v[106:109]
	v_mfma_f32_16x16x32_bf16 v[94:97], v[140:143], v[216:219], v[94:97]
	v_mfma_f32_16x16x32_bf16 v[90:93], v[148:151], v[216:219], v[90:93]
	v_mfma_f32_16x16x32_bf16 v[78:81], v[140:143], v[224:227], v[78:81]
	v_mfma_f32_16x16x32_bf16 v[74:77], v[148:151], v[224:227], v[74:77]
	s_setprio 0
	s_setprio 1
	v_mfma_f32_16x16x32_bf16 v[118:121], v[158:161], v[184:187], v[118:121]
	v_mfma_f32_16x16x32_bf16 v[114:117], v[176:179], v[184:187], v[114:117]
	v_mfma_f32_16x16x32_bf16 v[102:105], v[158:161], v[192:195], v[102:105]
	v_mfma_f32_16x16x32_bf16 v[98:101], v[176:179], v[192:195], v[98:101]
	v_mfma_f32_16x16x32_bf16 v[86:89], v[158:161], v[212:215], v[86:89]
	v_mfma_f32_16x16x32_bf16 v[82:85], v[176:179], v[212:215], v[82:85]
	v_mfma_f32_16x16x32_bf16 v[70:73], v[158:161], v[220:223], v[70:73]
	v_mfma_f32_16x16x32_bf16 v[66:69], v[176:179], v[220:223], v[66:69]
	v_mfma_f32_16x16x32_bf16 v[118:121], v[172:175], v[188:191], v[118:121]
	v_mfma_f32_16x16x32_bf16 v[114:117], v[180:183], v[188:191], v[114:117]
	v_mfma_f32_16x16x32_bf16 v[102:105], v[172:175], v[196:199], v[102:105]
	v_mfma_f32_16x16x32_bf16 v[98:101], v[180:183], v[196:199], v[98:101]
	v_mfma_f32_16x16x32_bf16 v[86:89], v[172:175], v[216:219], v[86:89]
	v_mfma_f32_16x16x32_bf16 v[82:85], v[180:183], v[216:219], v[82:85]
	v_mfma_f32_16x16x32_bf16 v[70:73], v[172:175], v[224:227], v[70:73]
	s_barrier
	v_mfma_f32_16x16x32_bf16 v[66:69], v[180:183], v[224:227], v[66:69]
	s_setprio 0
	s_add_u32 s28, s28, s54
	s_addc_u32 s29, s29, 0
	s_mov_b32 m0, s56
	ds_read_b128 v[184:187], v157 offset:49152
	ds_read_b128 v[188:191], v157 offset:50176
	ds_read_b128 v[192:195], v157 offset:51200
	ds_read_b128 v[196:199], v157 offset:52224
	ds_read_b128 v[212:215], v157 offset:53248
	ds_read_b128 v[216:219], v157 offset:54272
	ds_read_b128 v[220:223], v157 offset:55296
	ds_read_b128 v[224:227], v157 offset:56320
	global_load_lds_dwordx4 v0, s[28:29]
	v_lshl_add_u64 v[152:153], s[28:29], 0, v[134:135]
	s_add_u32 s28, s28, s40
	s_mov_b32 m0, s57
	s_addc_u32 s29, s29, 0
	global_load_lds_dwordx4 v[152:153], off
	s_mov_b32 m0, s62
	s_nop 0
	global_load_lds_dwordx4 v0, s[28:29]
	s_mov_b32 m0, s63
	s_nop 0
	global_load_lds_dwordx4 v134, s[28:29]
	s_mov_b32 m0, s58
	s_nop 0
	global_load_lds_dwordx4 v130, s[26:27]
	s_mov_b32 m0, s59
	s_nop 0
	global_load_lds_dwordx4 v132, s[26:27]
	s_waitcnt vmcnt(8)
	s_waitcnt lgkmcnt(0)
	s_barrier
	s_setprio 1
	s_waitcnt lgkmcnt(0)
	s_nop 0
	v_mfma_f32_16x16x32_bf16 v[62:65], v[136:139], v[184:187], v[62:65]
	v_mfma_f32_16x16x32_bf16 v[58:61], v[144:147], v[184:187], v[58:61]
	v_mfma_f32_16x16x32_bf16 v[46:49], v[136:139], v[192:195], v[46:49]
	v_mfma_f32_16x16x32_bf16 v[42:45], v[144:147], v[192:195], v[42:45]
	v_mfma_f32_16x16x32_bf16 v[30:33], v[136:139], v[212:215], v[30:33]
	v_mfma_f32_16x16x32_bf16 v[26:29], v[144:147], v[212:215], v[26:29]
	v_mfma_f32_16x16x32_bf16 v[14:17], v[136:139], v[220:223], v[14:17]
	v_mfma_f32_16x16x32_bf16 v[10:13], v[144:147], v[220:223], v[10:13]
	v_mfma_f32_16x16x32_bf16 v[62:65], v[140:143], v[188:191], v[62:65]
	v_mfma_f32_16x16x32_bf16 v[58:61], v[148:151], v[188:191], v[58:61]
	v_mfma_f32_16x16x32_bf16 v[46:49], v[140:143], v[196:199], v[46:49]
	v_mfma_f32_16x16x32_bf16 v[42:45], v[148:151], v[196:199], v[42:45]
	v_mfma_f32_16x16x32_bf16 v[30:33], v[140:143], v[216:219], v[30:33]
	v_mfma_f32_16x16x32_bf16 v[26:29], v[148:151], v[216:219], v[26:29]
	v_mfma_f32_16x16x32_bf16 v[14:17], v[140:143], v[224:227], v[14:17]
	v_mfma_f32_16x16x32_bf16 v[10:13], v[148:151], v[224:227], v[10:13]
	s_setprio 0
	s_setprio 1
	v_mfma_f32_16x16x32_bf16 v[54:57], v[158:161], v[184:187], v[54:57]
	v_mfma_f32_16x16x32_bf16 v[50:53], v[176:179], v[184:187], v[50:53]
	v_mfma_f32_16x16x32_bf16 v[38:41], v[158:161], v[192:195], v[38:41]
	v_mfma_f32_16x16x32_bf16 v[34:37], v[176:179], v[192:195], v[34:37]
	v_mfma_f32_16x16x32_bf16 v[22:25], v[158:161], v[212:215], v[22:25]
	v_mfma_f32_16x16x32_bf16 v[18:21], v[176:179], v[212:215], v[18:21]
	v_mfma_f32_16x16x32_bf16 v[6:9], v[158:161], v[220:223], v[6:9]
	v_mfma_f32_16x16x32_bf16 v[2:5], v[176:179], v[220:223], v[2:5]
	v_mfma_f32_16x16x32_bf16 v[54:57], v[172:175], v[188:191], v[54:57]
	v_mfma_f32_16x16x32_bf16 v[50:53], v[180:183], v[188:191], v[50:53]
	v_mfma_f32_16x16x32_bf16 v[38:41], v[172:175], v[196:199], v[38:41]
	v_mfma_f32_16x16x32_bf16 v[34:37], v[180:183], v[196:199], v[34:37]
	v_mfma_f32_16x16x32_bf16 v[22:25], v[172:175], v[216:219], v[22:25]
	v_mfma_f32_16x16x32_bf16 v[18:21], v[180:183], v[216:219], v[18:21]
	v_mfma_f32_16x16x32_bf16 v[6:9], v[172:175], v[224:227], v[6:9]
	s_barrier
	v_mfma_f32_16x16x32_bf16 v[2:5], v[180:183], v[224:227], v[2:5]
	s_setprio 0
	s_add_i32 s77, s77, 2
	s_cmp_ge_i32 s77, s52
	s_cbranch_scc0 .LBB0_575

.LBB0_852:
	s_add_i32 s26, s0, s79
	s_add_i32 s24, s26, 1
	s_cmp_ge_i32 s24, s53
	s_cselect_b32 s25, s53, 0
	s_sub_i32 s24, s24, s25
	s_ashr_i32 s25, s24, 31
	s_lshl_b64 s[82:83], s[24:25], s39
	s_add_i32 s26, s26, 2
	s_cmp_ge_i32 s26, s53
	s_cselect_b32 s24, s53, 0
	s_sub_i32 s24, s26, s24
	s_ashr_i32 s25, s24, 31
	v_add_u32_e32 v137, s1, v134
	s_lshl_b64 s[24:25], s[24:25], s39
	ds_read_b128 v[138:141], v137
	ds_read_b128 v[142:145], v137 offset:1024
	ds_read_b128 v[146:149], v137 offset:2048
	ds_read_b128 v[150:153], v137 offset:3072
	v_add_u32_e32 v137, s46, v134
	s_add_u32 s26, s20, s24
	ds_read_b128 v[156:159], v137
	ds_read_b128 v[160:163], v137 offset:1024
	ds_read_b128 v[172:175], v137 offset:2048
	ds_read_b128 v[176:179], v137 offset:3072
	s_addc_u32 s27, s21, s25
	s_add_u32 s24, s22, s24
	s_addc_u32 s25, s23, s25
	s_cmp_eq_u32 s55, s79
	s_cselect_b32 s28, s75, s26
	s_cselect_b32 s29, s76, s27
	s_cselect_b32 s27, s78, s25
	s_cselect_b32 s26, s77, s24
	s_add_u32 s24, s28, s56
	s_addc_u32 s25, s29, 0
	s_add_u32 s82, s72, s82
	s_addc_u32 s83, s73, s83
	s_add_i32 m0, s49, 0xc000
	ds_read_b128 v[180:183], v136
	ds_read_b128 v[184:187], v136 offset:1024
	ds_read_b128 v[188:191], v136 offset:2048
	ds_read_b128 v[192:195], v136 offset:3072
	ds_read_b128 v[196:199], v136 offset:4096
	ds_read_b128 v[212:215], v136 offset:5120
	ds_read_b128 v[216:219], v136 offset:6144
	ds_read_b128 v[220:223], v136 offset:7168
	global_load_lds_dwordx4 v0, s[82:83]
	s_add_i32 m0, s49, 0xe000
	s_nop 0
	global_load_lds_dwordx4 v132, s[82:83]
	s_waitcnt vmcnt(8)
	s_waitcnt lgkmcnt(0)
	s_barrier
	s_setprio 1
	s_waitcnt lgkmcnt(0)
	s_nop 0
	v_mfma_f32_16x16x32_bf16 v[126:129], v[138:141], v[180:183], v[126:129]
	v_mfma_f32_16x16x32_bf16 v[122:125], v[146:149], v[180:183], v[122:125]
	v_mfma_f32_16x16x32_bf16 v[110:113], v[138:141], v[188:191], v[110:113]
	v_mfma_f32_16x16x32_bf16 v[106:109], v[146:149], v[188:191], v[106:109]
	v_mfma_f32_16x16x32_bf16 v[94:97], v[138:141], v[196:199], v[94:97]
	v_mfma_f32_16x16x32_bf16 v[90:93], v[146:149], v[196:199], v[90:93]
	v_mfma_f32_16x16x32_bf16 v[78:81], v[138:141], v[216:219], v[78:81]
	v_mfma_f32_16x16x32_bf16 v[74:77], v[146:149], v[216:219], v[74:77]
	v_mfma_f32_16x16x32_bf16 v[126:129], v[142:145], v[184:187], v[126:129]
	v_mfma_f32_16x16x32_bf16 v[122:125], v[150:153], v[184:187], v[122:125]
	v_mfma_f32_16x16x32_bf16 v[110:113], v[142:145], v[192:195], v[110:113]
	v_mfma_f32_16x16x32_bf16 v[106:109], v[150:153], v[192:195], v[106:109]
	v_mfma_f32_16x16x32_bf16 v[94:97], v[142:145], v[212:215], v[94:97]
	v_mfma_f32_16x16x32_bf16 v[90:93], v[150:153], v[212:215], v[90:93]
	v_mfma_f32_16x16x32_bf16 v[78:81], v[142:145], v[220:223], v[78:81]
	v_mfma_f32_16x16x32_bf16 v[74:77], v[150:153], v[220:223], v[74:77]
	s_setprio 0
	s_setprio 1
	v_mfma_f32_16x16x32_bf16 v[118:121], v[156:159], v[180:183], v[118:121]
	v_mfma_f32_16x16x32_bf16 v[114:117], v[172:175], v[180:183], v[114:117]
	v_mfma_f32_16x16x32_bf16 v[102:105], v[156:159], v[188:191], v[102:105]
	v_mfma_f32_16x16x32_bf16 v[98:101], v[172:175], v[188:191], v[98:101]
	v_mfma_f32_16x16x32_bf16 v[86:89], v[156:159], v[196:199], v[86:89]
	v_mfma_f32_16x16x32_bf16 v[82:85], v[172:175], v[196:199], v[82:85]
	v_mfma_f32_16x16x32_bf16 v[70:73], v[156:159], v[216:219], v[70:73]
	v_mfma_f32_16x16x32_bf16 v[66:69], v[172:175], v[216:219], v[66:69]
	v_mfma_f32_16x16x32_bf16 v[118:121], v[160:163], v[184:187], v[118:121]
	v_mfma_f32_16x16x32_bf16 v[114:117], v[176:179], v[184:187], v[114:117]
	v_mfma_f32_16x16x32_bf16 v[102:105], v[160:163], v[192:195], v[102:105]
	v_mfma_f32_16x16x32_bf16 v[98:101], v[176:179], v[192:195], v[98:101]
	v_mfma_f32_16x16x32_bf16 v[86:89], v[160:163], v[212:215], v[86:89]
	v_mfma_f32_16x16x32_bf16 v[82:85], v[176:179], v[212:215], v[82:85]
	v_mfma_f32_16x16x32_bf16 v[70:73], v[160:163], v[220:223], v[70:73]
	s_barrier
	v_mfma_f32_16x16x32_bf16 v[66:69], v[176:179], v[220:223], v[66:69]
	s_setprio 0
	s_mov_b32 m0, s40
	s_add_u32 s82, s26, s38
	ds_read_b128 v[180:183], v136 offset:16384
	ds_read_b128 v[184:187], v136 offset:17408
	ds_read_b128 v[188:191], v136 offset:18432
	ds_read_b128 v[192:195], v136 offset:19456
	ds_read_b128 v[196:199], v136 offset:20480
	ds_read_b128 v[212:215], v136 offset:21504
	ds_read_b128 v[216:219], v136 offset:22528
	ds_read_b128 v[220:223], v136 offset:23552
	global_load_lds_dwordx4 v0, s[26:27]
	s_mov_b32 m0, s41
	s_addc_u32 s83, s27, 0
	global_load_lds_dwordx4 v132, s[26:27]
	s_mov_b32 m0, s47
	s_nop 0
	global_load_lds_dwordx4 v0, s[82:83]
	s_mov_b32 m0, s48
	s_nop 0
	global_load_lds_dwordx4 v132, s[82:83]
	s_mov_b32 m0, s49
	s_nop 0
	global_load_lds_dwordx4 v0, s[28:29]
	s_mov_b32 m0, s50
	s_nop 0
	global_load_lds_dwordx4 v132, s[28:29]
	s_waitcnt vmcnt(8)
	s_waitcnt lgkmcnt(0)
	s_barrier
	s_setprio 1
	s_waitcnt lgkmcnt(0)
	s_nop 0
	v_mfma_f32_16x16x32_bf16 v[62:65], v[138:141], v[180:183], v[62:65]
	v_mfma_f32_16x16x32_bf16 v[58:61], v[146:149], v[180:183], v[58:61]
	v_mfma_f32_16x16x32_bf16 v[46:49], v[138:141], v[188:191], v[46:49]
	v_mfma_f32_16x16x32_bf16 v[42:45], v[146:149], v[188:191], v[42:45]
	v_mfma_f32_16x16x32_bf16 v[30:33], v[138:141], v[196:199], v[30:33]
	v_mfma_f32_16x16x32_bf16 v[26:29], v[146:149], v[196:199], v[26:29]
	v_mfma_f32_16x16x32_bf16 v[14:17], v[138:141], v[216:219], v[14:17]
	v_mfma_f32_16x16x32_bf16 v[10:13], v[146:149], v[216:219], v[10:13]
	v_mfma_f32_16x16x32_bf16 v[62:65], v[142:145], v[184:187], v[62:65]
	v_mfma_f32_16x16x32_bf16 v[58:61], v[150:153], v[184:187], v[58:61]
	v_mfma_f32_16x16x32_bf16 v[46:49], v[142:145], v[192:195], v[46:49]
	v_mfma_f32_16x16x32_bf16 v[42:45], v[150:153], v[192:195], v[42:45]
	v_mfma_f32_16x16x32_bf16 v[30:33], v[142:145], v[212:215], v[30:33]
	v_mfma_f32_16x16x32_bf16 v[26:29], v[150:153], v[212:215], v[26:29]
	v_mfma_f32_16x16x32_bf16 v[14:17], v[142:145], v[220:223], v[14:17]
	v_mfma_f32_16x16x32_bf16 v[10:13], v[150:153], v[220:223], v[10:13]
	s_setprio 0
	s_setprio 1
	v_mfma_f32_16x16x32_bf16 v[54:57], v[156:159], v[180:183], v[54:57]
	v_mfma_f32_16x16x32_bf16 v[50:53], v[172:175], v[180:183], v[50:53]
	v_mfma_f32_16x16x32_bf16 v[38:41], v[156:159], v[188:191], v[38:41]
	v_mfma_f32_16x16x32_bf16 v[34:37], v[172:175], v[188:191], v[34:37]
	v_mfma_f32_16x16x32_bf16 v[22:25], v[156:159], v[196:199], v[22:25]
	v_mfma_f32_16x16x32_bf16 v[18:21], v[172:175], v[196:199], v[18:21]
	v_mfma_f32_16x16x32_bf16 v[6:9], v[156:159], v[216:219], v[6:9]
	v_mfma_f32_16x16x32_bf16 v[2:5], v[172:175], v[216:219], v[2:5]
	v_mfma_f32_16x16x32_bf16 v[54:57], v[160:163], v[184:187], v[54:57]
	v_mfma_f32_16x16x32_bf16 v[50:53], v[176:179], v[184:187], v[50:53]
	v_mfma_f32_16x16x32_bf16 v[38:41], v[160:163], v[192:195], v[38:41]
	v_mfma_f32_16x16x32_bf16 v[34:37], v[176:179], v[192:195], v[34:37]
	v_mfma_f32_16x16x32_bf16 v[22:25], v[160:163], v[212:215], v[22:25]
	v_mfma_f32_16x16x32_bf16 v[18:21], v[176:179], v[212:215], v[18:21]
	v_mfma_f32_16x16x32_bf16 v[6:9], v[160:163], v[220:223], v[6:9]
	s_barrier
	v_mfma_f32_16x16x32_bf16 v[2:5], v[176:179], v[220:223], v[2:5]
	s_setprio 0
	v_add_u32_e32 v137, s57, v134
	ds_read_b128 v[138:141], v137
	ds_read_b128 v[142:145], v137 offset:1024
	ds_read_b128 v[146:149], v137 offset:2048
	ds_read_b128 v[150:153], v137 offset:3072
	v_add_u32_e32 v137, s63, v134
	ds_read_b128 v[156:159], v137
	ds_read_b128 v[160:163], v137 offset:1024
	ds_read_b128 v[172:175], v137 offset:2048
	ds_read_b128 v[176:179], v137 offset:3072
	s_add_u32 s28, s28, s38
	s_addc_u32 s29, s29, 0
	s_mov_b32 m0, s51
	ds_read_b128 v[180:183], v136 offset:32768
	ds_read_b128 v[184:187], v136 offset:33792
	ds_read_b128 v[188:191], v136 offset:34816
	ds_read_b128 v[192:195], v136 offset:35840
	ds_read_b128 v[196:199], v136 offset:36864
	ds_read_b128 v[212:215], v136 offset:37888
	ds_read_b128 v[216:219], v136 offset:38912
	ds_read_b128 v[220:223], v136 offset:39936
	global_load_lds_dwordx4 v0, s[28:29]
	s_mov_b32 m0, s52
	s_nop 0
	global_load_lds_dwordx4 v132, s[28:29]
	s_waitcnt vmcnt(8)
	s_waitcnt lgkmcnt(0)
	s_barrier
	s_setprio 1
	s_waitcnt lgkmcnt(0)
	s_nop 0
	v_mfma_f32_16x16x32_bf16 v[126:129], v[138:141], v[180:183], v[126:129]
	v_mfma_f32_16x16x32_bf16 v[122:125], v[146:149], v[180:183], v[122:125]
	v_mfma_f32_16x16x32_bf16 v[110:113], v[138:141], v[188:191], v[110:113]
	v_mfma_f32_16x16x32_bf16 v[106:109], v[146:149], v[188:191], v[106:109]
	v_mfma_f32_16x16x32_bf16 v[94:97], v[138:141], v[196:199], v[94:97]
	v_mfma_f32_16x16x32_bf16 v[90:93], v[146:149], v[196:199], v[90:93]
	v_mfma_f32_16x16x32_bf16 v[78:81], v[138:141], v[216:219], v[78:81]
	v_mfma_f32_16x16x32_bf16 v[74:77], v[146:149], v[216:219], v[74:77]
	v_mfma_f32_16x16x32_bf16 v[126:129], v[142:145], v[184:187], v[126:129]
	v_mfma_f32_16x16x32_bf16 v[122:125], v[150:153], v[184:187], v[122:125]
	v_mfma_f32_16x16x32_bf16 v[110:113], v[142:145], v[192:195], v[110:113]
	v_mfma_f32_16x16x32_bf16 v[106:109], v[150:153], v[192:195], v[106:109]
	v_mfma_f32_16x16x32_bf16 v[94:97], v[142:145], v[212:215], v[94:97]
	v_mfma_f32_16x16x32_bf16 v[90:93], v[150:153], v[212:215], v[90:93]
	v_mfma_f32_16x16x32_bf16 v[78:81], v[142:145], v[220:223], v[78:81]
	v_mfma_f32_16x16x32_bf16 v[74:77], v[150:153], v[220:223], v[74:77]
	s_setprio 0
	s_setprio 1
	v_mfma_f32_16x16x32_bf16 v[118:121], v[156:159], v[180:183], v[118:121]
	v_mfma_f32_16x16x32_bf16 v[114:117], v[172:175], v[180:183], v[114:117]
	v_mfma_f32_16x16x32_bf16 v[102:105], v[156:159], v[188:191], v[102:105]
	v_mfma_f32_16x16x32_bf16 v[98:101], v[172:175], v[188:191], v[98:101]
	v_mfma_f32_16x16x32_bf16 v[86:89], v[156:159], v[196:199], v[86:89]
	v_mfma_f32_16x16x32_bf16 v[82:85], v[172:175], v[196:199], v[82:85]
	v_mfma_f32_16x16x32_bf16 v[70:73], v[156:159], v[216:219], v[70:73]
	v_mfma_f32_16x16x32_bf16 v[66:69], v[172:175], v[216:219], v[66:69]
	v_mfma_f32_16x16x32_bf16 v[118:121], v[160:163], v[184:187], v[118:121]
	v_mfma_f32_16x16x32_bf16 v[114:117], v[176:179], v[184:187], v[114:117]
	v_mfma_f32_16x16x32_bf16 v[102:105], v[160:163], v[192:195], v[102:105]
	v_mfma_f32_16x16x32_bf16 v[98:101], v[176:179], v[192:195], v[98:101]
	v_mfma_f32_16x16x32_bf16 v[86:89], v[160:163], v[212:215], v[86:89]
	v_mfma_f32_16x16x32_bf16 v[82:85], v[176:179], v[212:215], v[82:85]
	v_mfma_f32_16x16x32_bf16 v[70:73], v[160:163], v[220:223], v[70:73]
	s_barrier
	v_mfma_f32_16x16x32_bf16 v[66:69], v[176:179], v[220:223], v[66:69]
	s_setprio 0
	s_add_u32 s26, s26, s56
	s_addc_u32 s27, s27, 0
	s_mov_b32 m0, s58
	ds_read_b128 v[180:183], v136 offset:49152
	ds_read_b128 v[184:187], v136 offset:50176
	ds_read_b128 v[188:191], v136 offset:51200
	ds_read_b128 v[192:195], v136 offset:52224
	ds_read_b128 v[196:199], v136 offset:53248
	ds_read_b128 v[212:215], v136 offset:54272
	ds_read_b128 v[216:219], v136 offset:55296
	ds_read_b128 v[220:223], v136 offset:56320
	global_load_lds_dwordx4 v0, s[26:27]
	v_lshl_add_u64 v[168:169], s[26:27], 0, v[132:133]
	s_add_u32 s26, s26, s38
	s_mov_b32 m0, s59
	s_addc_u32 s27, s27, 0
	global_load_lds_dwordx4 v[168:169], off
	s_mov_b32 m0, s64
	s_nop 0
	global_load_lds_dwordx4 v0, s[26:27]
	s_mov_b32 m0, s65
	s_nop 0
	global_load_lds_dwordx4 v132, s[26:27]
	s_mov_b32 m0, s60
	s_nop 0
	global_load_lds_dwordx4 v0, s[24:25]
	s_mov_b32 m0, s62
	s_nop 0
	global_load_lds_dwordx4 v132, s[24:25]
	s_waitcnt vmcnt(8)
	s_waitcnt lgkmcnt(0)
	s_barrier
	s_setprio 1
	s_waitcnt lgkmcnt(0)
	s_nop 0
	v_mfma_f32_16x16x32_bf16 v[62:65], v[138:141], v[180:183], v[62:65]
	v_mfma_f32_16x16x32_bf16 v[58:61], v[146:149], v[180:183], v[58:61]
	v_mfma_f32_16x16x32_bf16 v[46:49], v[138:141], v[188:191], v[46:49]
	v_mfma_f32_16x16x32_bf16 v[42:45], v[146:149], v[188:191], v[42:45]
	v_mfma_f32_16x16x32_bf16 v[30:33], v[138:141], v[196:199], v[30:33]
	v_mfma_f32_16x16x32_bf16 v[26:29], v[146:149], v[196:199], v[26:29]
	v_mfma_f32_16x16x32_bf16 v[14:17], v[138:141], v[216:219], v[14:17]
	v_mfma_f32_16x16x32_bf16 v[10:13], v[146:149], v[216:219], v[10:13]
	v_mfma_f32_16x16x32_bf16 v[62:65], v[142:145], v[184:187], v[62:65]
	v_mfma_f32_16x16x32_bf16 v[58:61], v[150:153], v[184:187], v[58:61]
	v_mfma_f32_16x16x32_bf16 v[46:49], v[142:145], v[192:195], v[46:49]
	v_mfma_f32_16x16x32_bf16 v[42:45], v[150:153], v[192:195], v[42:45]
	v_mfma_f32_16x16x32_bf16 v[30:33], v[142:145], v[212:215], v[30:33]
	v_mfma_f32_16x16x32_bf16 v[26:29], v[150:153], v[212:215], v[26:29]
	v_mfma_f32_16x16x32_bf16 v[14:17], v[142:145], v[220:223], v[14:17]
	v_mfma_f32_16x16x32_bf16 v[10:13], v[150:153], v[220:223], v[10:13]
	s_setprio 0
	s_setprio 1
	v_mfma_f32_16x16x32_bf16 v[54:57], v[156:159], v[180:183], v[54:57]
	v_mfma_f32_16x16x32_bf16 v[50:53], v[172:175], v[180:183], v[50:53]
	v_mfma_f32_16x16x32_bf16 v[38:41], v[156:159], v[188:191], v[38:41]
	v_mfma_f32_16x16x32_bf16 v[34:37], v[172:175], v[188:191], v[34:37]
	v_mfma_f32_16x16x32_bf16 v[22:25], v[156:159], v[196:199], v[22:25]
	v_mfma_f32_16x16x32_bf16 v[18:21], v[172:175], v[196:199], v[18:21]
	v_mfma_f32_16x16x32_bf16 v[6:9], v[156:159], v[216:219], v[6:9]
	v_mfma_f32_16x16x32_bf16 v[2:5], v[172:175], v[216:219], v[2:5]
	v_mfma_f32_16x16x32_bf16 v[54:57], v[160:163], v[184:187], v[54:57]
	v_mfma_f32_16x16x32_bf16 v[50:53], v[176:179], v[184:187], v[50:53]
	v_mfma_f32_16x16x32_bf16 v[38:41], v[160:163], v[192:195], v[38:41]
	v_mfma_f32_16x16x32_bf16 v[34:37], v[176:179], v[192:195], v[34:37]
	v_mfma_f32_16x16x32_bf16 v[22:25], v[160:163], v[212:215], v[22:25]
	v_mfma_f32_16x16x32_bf16 v[18:21], v[176:179], v[212:215], v[18:21]
	v_mfma_f32_16x16x32_bf16 v[6:9], v[160:163], v[220:223], v[6:9]
	s_barrier
	v_mfma_f32_16x16x32_bf16 v[2:5], v[176:179], v[220:223], v[2:5]
	s_setprio 0
	s_add_i32 s79, s79, 2
	s_cmp_ge_i32 s79, s53
	s_cbranch_scc0 .LBB0_852

.LBB0_1216:
	s_add_i32 s28, s0, s74
	s_add_i32 s4, s28, 1
	s_cmp_ge_i32 s4, s50
	s_cselect_b32 s5, s50, 0
	s_sub_i32 s4, s4, s5
	s_ashr_i32 s5, s4, 31
	s_lshl_b64 s[76:77], s[4:5], s39
	s_add_i32 s28, s28, 2
	s_cmp_ge_i32 s28, s50
	s_cselect_b32 s4, s50, 0
	s_sub_i32 s4, s28, s4
	s_ashr_i32 s5, s4, 31
	v_add_u32_e32 v0, s1, v188
	s_lshl_b64 s[4:5], s[4:5], s39
	ds_read_b128 v[132:135], v0
	ds_read_b128 v[136:139], v0 offset:1024
	ds_read_b128 v[140:143], v0 offset:2048
	ds_read_b128 v[144:147], v0 offset:3072
	v_add_u32_e32 v0, s42, v188
	s_add_u32 s28, s6, s4
	ds_read_b128 v[148:151], v0
	ds_read_b128 v[152:155], v0 offset:1024
	ds_read_b128 v[156:159], v0 offset:2048
	ds_read_b128 v[160:163], v0 offset:3072
	s_addc_u32 s29, s7, s5
	s_add_u32 s4, s26, s4
	s_addc_u32 s5, s27, s5
	s_cmp_eq_u32 s51, s74
	s_cselect_b32 s30, s70, s28
	s_cselect_b32 s31, s71, s29
	s_cselect_b32 s29, s73, s5
	s_cselect_b32 s28, s72, s4
	s_add_u32 s4, s30, s52
	s_addc_u32 s5, s31, 0
	s_add_u32 s76, s68, s76
	s_addc_u32 s77, s69, s77
	s_add_i32 m0, s45, 0xc000
	ds_read_b128 v[180:183], v190
	ds_read_b128 v[184:187], v190 offset:1024
	ds_read_b128 v[192:195], v190 offset:2048
	ds_read_b128 v[196:199], v190 offset:3072
	ds_read_b128 v[212:215], v190 offset:4096
	ds_read_b128 v[216:219], v190 offset:5120
	ds_read_b128 v[220:223], v190 offset:6144
	ds_read_b128 v[224:227], v190 offset:7168
	global_load_lds_dwordx4 v172, s[76:77]
	s_add_i32 m0, s45, 0xe000
	s_nop 0
	global_load_lds_dwordx4 v176, s[76:77]
	s_waitcnt vmcnt(8)
	s_waitcnt lgkmcnt(0)
	s_barrier
	s_setprio 1
	s_waitcnt lgkmcnt(0)
	s_nop 0
	v_mfma_f32_16x16x32_bf16 v[112:115], v[132:135], v[180:183], v[112:115]
	v_mfma_f32_16x16x32_bf16 v[108:111], v[140:143], v[180:183], v[108:111]
	v_mfma_f32_16x16x32_bf16 v[104:107], v[132:135], v[192:195], v[104:107]
	v_mfma_f32_16x16x32_bf16 v[100:103], v[140:143], v[192:195], v[100:103]
	v_mfma_f32_16x16x32_bf16 v[96:99], v[132:135], v[212:215], v[96:99]
	v_mfma_f32_16x16x32_bf16 v[92:95], v[140:143], v[212:215], v[92:95]
	v_mfma_f32_16x16x32_bf16 v[88:91], v[132:135], v[220:223], v[88:91]
	v_mfma_f32_16x16x32_bf16 v[84:87], v[140:143], v[220:223], v[84:87]
	v_mfma_f32_16x16x32_bf16 v[112:115], v[136:139], v[184:187], v[112:115]
	v_mfma_f32_16x16x32_bf16 v[108:111], v[144:147], v[184:187], v[108:111]
	v_mfma_f32_16x16x32_bf16 v[104:107], v[136:139], v[196:199], v[104:107]
	v_mfma_f32_16x16x32_bf16 v[100:103], v[144:147], v[196:199], v[100:103]
	v_mfma_f32_16x16x32_bf16 v[96:99], v[136:139], v[216:219], v[96:99]
	v_mfma_f32_16x16x32_bf16 v[92:95], v[144:147], v[216:219], v[92:95]
	v_mfma_f32_16x16x32_bf16 v[88:91], v[136:139], v[224:227], v[88:91]
	v_mfma_f32_16x16x32_bf16 v[84:87], v[144:147], v[224:227], v[84:87]
	s_setprio 0
	s_setprio 1
	v_mfma_f32_16x16x32_bf16 v[80:83], v[148:151], v[180:183], v[80:83]
	v_mfma_f32_16x16x32_bf16 v[76:79], v[156:159], v[180:183], v[76:79]
	v_mfma_f32_16x16x32_bf16 v[72:75], v[148:151], v[192:195], v[72:75]
	v_mfma_f32_16x16x32_bf16 v[68:71], v[156:159], v[192:195], v[68:71]
	v_mfma_f32_16x16x32_bf16 v[64:67], v[148:151], v[212:215], v[64:67]
	v_mfma_f32_16x16x32_bf16 v[60:63], v[156:159], v[212:215], v[60:63]
	v_mfma_f32_16x16x32_bf16 v[56:59], v[148:151], v[220:223], v[56:59]
	v_mfma_f32_16x16x32_bf16 v[48:51], v[156:159], v[220:223], v[48:51]
	v_mfma_f32_16x16x32_bf16 v[80:83], v[152:155], v[184:187], v[80:83]
	v_mfma_f32_16x16x32_bf16 v[76:79], v[160:163], v[184:187], v[76:79]
	v_mfma_f32_16x16x32_bf16 v[72:75], v[152:155], v[196:199], v[72:75]
	v_mfma_f32_16x16x32_bf16 v[68:71], v[160:163], v[196:199], v[68:71]
	v_mfma_f32_16x16x32_bf16 v[64:67], v[152:155], v[216:219], v[64:67]
	v_mfma_f32_16x16x32_bf16 v[60:63], v[160:163], v[216:219], v[60:63]
	v_mfma_f32_16x16x32_bf16 v[56:59], v[152:155], v[224:227], v[56:59]
	s_barrier
	v_mfma_f32_16x16x32_bf16 v[48:51], v[160:163], v[224:227], v[48:51]
	s_setprio 0
	s_mov_b32 m0, s40
	s_add_u32 s76, s28, s38
	ds_read_b128 v[180:183], v190 offset:16384
	ds_read_b128 v[184:187], v190 offset:17408
	ds_read_b128 v[192:195], v190 offset:18432
	ds_read_b128 v[196:199], v190 offset:19456
	ds_read_b128 v[212:215], v190 offset:20480
	ds_read_b128 v[216:219], v190 offset:21504
	ds_read_b128 v[220:223], v190 offset:22528
	ds_read_b128 v[224:227], v190 offset:23552
	global_load_lds_dwordx4 v174, s[28:29]
	s_mov_b32 m0, s41
	s_addc_u32 s77, s29, 0
	global_load_lds_dwordx4 v178, s[28:29]
	s_mov_b32 m0, s43
	s_nop 0
	global_load_lds_dwordx4 v174, s[76:77]
	s_mov_b32 m0, s44
	s_nop 0
	global_load_lds_dwordx4 v178, s[76:77]
	s_mov_b32 m0, s45
	s_nop 0
	global_load_lds_dwordx4 v172, s[30:31]
	s_mov_b32 m0, s46
	s_nop 0
	global_load_lds_dwordx4 v176, s[30:31]
	s_waitcnt vmcnt(8)
	s_waitcnt lgkmcnt(0)
	s_barrier
	s_setprio 1
	s_waitcnt lgkmcnt(0)
	s_nop 0
	v_mfma_f32_16x16x32_bf16 v[52:55], v[132:135], v[180:183], v[52:55]
	v_mfma_f32_16x16x32_bf16 v[44:47], v[140:143], v[180:183], v[44:47]
	v_mfma_f32_16x16x32_bf16 v[40:43], v[132:135], v[192:195], v[40:43]
	v_mfma_f32_16x16x32_bf16 v[36:39], v[140:143], v[192:195], v[36:39]
	v_mfma_f32_16x16x32_bf16 v[32:35], v[132:135], v[212:215], v[32:35]
	v_mfma_f32_16x16x32_bf16 v[28:31], v[140:143], v[212:215], v[28:31]
	v_mfma_f32_16x16x32_bf16 v[24:27], v[132:135], v[220:223], v[24:27]
	v_mfma_f32_16x16x32_bf16 v[20:23], v[140:143], v[220:223], v[20:23]
	v_mfma_f32_16x16x32_bf16 v[52:55], v[136:139], v[184:187], v[52:55]
	v_mfma_f32_16x16x32_bf16 v[44:47], v[144:147], v[184:187], v[44:47]
	v_mfma_f32_16x16x32_bf16 v[40:43], v[136:139], v[196:199], v[40:43]
	v_mfma_f32_16x16x32_bf16 v[36:39], v[144:147], v[196:199], v[36:39]
	v_mfma_f32_16x16x32_bf16 v[32:35], v[136:139], v[216:219], v[32:35]
	v_mfma_f32_16x16x32_bf16 v[28:31], v[144:147], v[216:219], v[28:31]
	v_mfma_f32_16x16x32_bf16 v[24:27], v[136:139], v[224:227], v[24:27]
	v_mfma_f32_16x16x32_bf16 v[20:23], v[144:147], v[224:227], v[20:23]
	s_setprio 0
	s_setprio 1
	v_mfma_f32_16x16x32_bf16 v[16:19], v[148:151], v[180:183], v[16:19]
	v_mfma_f32_16x16x32_bf16 v[12:15], v[156:159], v[180:183], v[12:15]
	v_mfma_f32_16x16x32_bf16 v[8:11], v[148:151], v[192:195], v[8:11]
	v_mfma_f32_16x16x32_bf16 v[2:5], v[156:159], v[192:195], v[4:7]
	v_mfma_f32_16x16x32_bf16 v[116:119], v[148:151], v[212:215], v[116:119]
	v_mfma_f32_16x16x32_bf16 v[120:123], v[156:159], v[212:215], v[120:123]
	v_mfma_f32_16x16x32_bf16 v[124:127], v[148:151], v[220:223], v[124:127]
	v_mfma_f32_16x16x32_bf16 v[128:131], v[156:159], v[220:223], v[128:131]
	v_mfma_f32_16x16x32_bf16 v[16:19], v[152:155], v[184:187], v[16:19]
	v_mfma_f32_16x16x32_bf16 v[12:15], v[160:163], v[184:187], v[12:15]
	v_mfma_f32_16x16x32_bf16 v[8:11], v[152:155], v[196:199], v[8:11]
	v_mfma_f32_16x16x32_bf16 v[2:5], v[160:163], v[196:199], v[2:5]
	v_mfma_f32_16x16x32_bf16 v[116:119], v[152:155], v[216:219], v[116:119]
	v_mfma_f32_16x16x32_bf16 v[120:123], v[160:163], v[216:219], v[120:123]
	v_mfma_f32_16x16x32_bf16 v[124:127], v[152:155], v[224:227], v[124:127]
	s_barrier
	v_mfma_f32_16x16x32_bf16 v[128:131], v[160:163], v[224:227], v[128:131]
	s_setprio 0
	v_add_u32_e32 v0, s54, v188
	ds_read_b128 v[132:135], v0
	ds_read_b128 v[136:139], v0 offset:1024
	ds_read_b128 v[140:143], v0 offset:2048
	ds_read_b128 v[144:147], v0 offset:3072
	v_add_u32_e32 v0, s59, v188
	ds_read_b128 v[148:151], v0
	ds_read_b128 v[152:155], v0 offset:1024
	ds_read_b128 v[156:159], v0 offset:2048
	ds_read_b128 v[160:163], v0 offset:3072
	s_add_u32 s30, s30, s38
	s_addc_u32 s31, s31, 0
	s_mov_b32 m0, s47
	ds_read_b128 v[180:183], v190 offset:32768
	ds_read_b128 v[184:187], v190 offset:33792
	ds_read_b128 v[192:195], v190 offset:34816
	ds_read_b128 v[196:199], v190 offset:35840
	ds_read_b128 v[212:215], v190 offset:36864
	ds_read_b128 v[216:219], v190 offset:37888
	ds_read_b128 v[220:223], v190 offset:38912
	ds_read_b128 v[224:227], v190 offset:39936
	global_load_lds_dwordx4 v172, s[30:31]
	s_mov_b32 m0, s48
	s_nop 0
	global_load_lds_dwordx4 v176, s[30:31]
	s_waitcnt vmcnt(8)
	s_waitcnt lgkmcnt(0)
	s_barrier
	s_setprio 1
	s_waitcnt lgkmcnt(0)
	s_nop 0
	v_mfma_f32_16x16x32_bf16 v[112:115], v[132:135], v[180:183], v[112:115]
	v_mfma_f32_16x16x32_bf16 v[108:111], v[140:143], v[180:183], v[108:111]
	v_mfma_f32_16x16x32_bf16 v[104:107], v[132:135], v[192:195], v[104:107]
	v_mfma_f32_16x16x32_bf16 v[100:103], v[140:143], v[192:195], v[100:103]
	v_mfma_f32_16x16x32_bf16 v[96:99], v[132:135], v[212:215], v[96:99]
	v_mfma_f32_16x16x32_bf16 v[92:95], v[140:143], v[212:215], v[92:95]
	v_mfma_f32_16x16x32_bf16 v[88:91], v[132:135], v[220:223], v[88:91]
	v_mfma_f32_16x16x32_bf16 v[84:87], v[140:143], v[220:223], v[84:87]
	v_mfma_f32_16x16x32_bf16 v[112:115], v[136:139], v[184:187], v[112:115]
	v_mfma_f32_16x16x32_bf16 v[108:111], v[144:147], v[184:187], v[108:111]
	v_mfma_f32_16x16x32_bf16 v[104:107], v[136:139], v[196:199], v[104:107]
	v_mfma_f32_16x16x32_bf16 v[100:103], v[144:147], v[196:199], v[100:103]
	v_mfma_f32_16x16x32_bf16 v[96:99], v[136:139], v[216:219], v[96:99]
	v_mfma_f32_16x16x32_bf16 v[92:95], v[144:147], v[216:219], v[92:95]
	v_mfma_f32_16x16x32_bf16 v[88:91], v[136:139], v[224:227], v[88:91]
	v_mfma_f32_16x16x32_bf16 v[84:87], v[144:147], v[224:227], v[84:87]
	s_setprio 0
	s_setprio 1
	v_mfma_f32_16x16x32_bf16 v[80:83], v[148:151], v[180:183], v[80:83]
	v_mfma_f32_16x16x32_bf16 v[76:79], v[156:159], v[180:183], v[76:79]
	v_mfma_f32_16x16x32_bf16 v[72:75], v[148:151], v[192:195], v[72:75]
	v_mfma_f32_16x16x32_bf16 v[68:71], v[156:159], v[192:195], v[68:71]
	v_mfma_f32_16x16x32_bf16 v[64:67], v[148:151], v[212:215], v[64:67]
	v_mfma_f32_16x16x32_bf16 v[60:63], v[156:159], v[212:215], v[60:63]
	v_mfma_f32_16x16x32_bf16 v[56:59], v[148:151], v[220:223], v[56:59]
	v_mfma_f32_16x16x32_bf16 v[48:51], v[156:159], v[220:223], v[48:51]
	v_mfma_f32_16x16x32_bf16 v[80:83], v[152:155], v[184:187], v[80:83]
	v_mfma_f32_16x16x32_bf16 v[76:79], v[160:163], v[184:187], v[76:79]
	v_mfma_f32_16x16x32_bf16 v[72:75], v[152:155], v[196:199], v[72:75]
	v_mfma_f32_16x16x32_bf16 v[68:71], v[160:163], v[196:199], v[68:71]
	v_mfma_f32_16x16x32_bf16 v[64:67], v[152:155], v[216:219], v[64:67]
	v_mfma_f32_16x16x32_bf16 v[60:63], v[160:163], v[216:219], v[60:63]
	v_mfma_f32_16x16x32_bf16 v[56:59], v[152:155], v[224:227], v[56:59]
	s_barrier
	v_mfma_f32_16x16x32_bf16 v[48:51], v[160:163], v[224:227], v[48:51]
	s_setprio 0
	s_add_u32 s28, s28, s52
	s_addc_u32 s29, s29, 0
	s_mov_b32 m0, s55
	ds_read_b128 v[180:183], v190 offset:49152
	ds_read_b128 v[184:187], v190 offset:50176
	ds_read_b128 v[192:195], v190 offset:51200
	ds_read_b128 v[196:199], v190 offset:52224
	ds_read_b128 v[212:215], v190 offset:53248
	ds_read_b128 v[216:219], v190 offset:54272
	ds_read_b128 v[220:223], v190 offset:55296
	ds_read_b128 v[224:227], v190 offset:56320
	global_load_lds_dwordx4 v174, s[28:29]
	v_lshl_add_u64 v[6:7], s[28:29], 0, v[178:179]
	s_add_u32 s28, s28, s38
	s_mov_b32 m0, s56
	s_addc_u32 s29, s29, 0
	global_load_lds_dwordx4 v[6:7], off
	s_mov_b32 m0, s60
	s_nop 0
	global_load_lds_dwordx4 v174, s[28:29]
	s_mov_b32 m0, s62
	s_nop 0
	global_load_lds_dwordx4 v178, s[28:29]
	s_mov_b32 m0, s57
	s_nop 0
	global_load_lds_dwordx4 v172, s[4:5]
	s_mov_b32 m0, s58
	s_nop 0
	global_load_lds_dwordx4 v176, s[4:5]
	s_waitcnt vmcnt(8)
	s_waitcnt lgkmcnt(0)
	s_barrier
	s_setprio 1
	s_waitcnt lgkmcnt(0)
	s_nop 0
	v_mfma_f32_16x16x32_bf16 v[52:55], v[132:135], v[180:183], v[52:55]
	v_mfma_f32_16x16x32_bf16 v[44:47], v[140:143], v[180:183], v[44:47]
	v_mfma_f32_16x16x32_bf16 v[40:43], v[132:135], v[192:195], v[40:43]
	v_mfma_f32_16x16x32_bf16 v[36:39], v[140:143], v[192:195], v[36:39]
	v_mfma_f32_16x16x32_bf16 v[32:35], v[132:135], v[212:215], v[32:35]
	v_mfma_f32_16x16x32_bf16 v[28:31], v[140:143], v[212:215], v[28:31]
	v_mfma_f32_16x16x32_bf16 v[24:27], v[132:135], v[220:223], v[24:27]
	v_mfma_f32_16x16x32_bf16 v[20:23], v[140:143], v[220:223], v[20:23]
	v_mfma_f32_16x16x32_bf16 v[52:55], v[136:139], v[184:187], v[52:55]
	v_mfma_f32_16x16x32_bf16 v[44:47], v[144:147], v[184:187], v[44:47]
	v_mfma_f32_16x16x32_bf16 v[40:43], v[136:139], v[196:199], v[40:43]
	v_mfma_f32_16x16x32_bf16 v[36:39], v[144:147], v[196:199], v[36:39]
	v_mfma_f32_16x16x32_bf16 v[32:35], v[136:139], v[216:219], v[32:35]
	v_mfma_f32_16x16x32_bf16 v[28:31], v[144:147], v[216:219], v[28:31]
	v_mfma_f32_16x16x32_bf16 v[24:27], v[136:139], v[224:227], v[24:27]
	v_mfma_f32_16x16x32_bf16 v[20:23], v[144:147], v[224:227], v[20:23]
	s_setprio 0
	s_setprio 1
	v_mfma_f32_16x16x32_bf16 v[16:19], v[148:151], v[180:183], v[16:19]
	v_mfma_f32_16x16x32_bf16 v[12:15], v[156:159], v[180:183], v[12:15]
	v_mfma_f32_16x16x32_bf16 v[6:9], v[148:151], v[192:195], v[8:11]
	v_mfma_f32_16x16x32_bf16 v[2:5], v[156:159], v[192:195], v[2:5]
	v_mfma_f32_16x16x32_bf16 v[116:119], v[148:151], v[212:215], v[116:119]
	v_mfma_f32_16x16x32_bf16 v[120:123], v[156:159], v[212:215], v[120:123]
	v_mfma_f32_16x16x32_bf16 v[124:127], v[148:151], v[220:223], v[124:127]
	v_mfma_f32_16x16x32_bf16 v[128:131], v[156:159], v[220:223], v[128:131]
	v_mfma_f32_16x16x32_bf16 v[16:19], v[152:155], v[184:187], v[16:19]
	v_mfma_f32_16x16x32_bf16 v[12:15], v[160:163], v[184:187], v[12:15]
	v_mfma_f32_16x16x32_bf16 v[8:11], v[152:155], v[196:199], v[6:9]
	v_mfma_f32_16x16x32_bf16 v[4:7], v[160:163], v[196:199], v[2:5]
	v_mfma_f32_16x16x32_bf16 v[116:119], v[152:155], v[216:219], v[116:119]
	v_mfma_f32_16x16x32_bf16 v[120:123], v[160:163], v[216:219], v[120:123]
	v_mfma_f32_16x16x32_bf16 v[124:127], v[152:155], v[224:227], v[124:127]
	s_barrier
	v_mfma_f32_16x16x32_bf16 v[128:131], v[160:163], v[224:227], v[128:131]
	s_setprio 0
	s_add_i32 s74, s74, 2
	s_cmp_ge_i32 s74, s50
	s_cbranch_scc0 .LBB0_1216

.LBB0_1464:
	s_add_i32 s30, s6, s78
	s_add_i32 s28, s30, 1
	s_cmp_ge_i32 s28, s52
	s_cselect_b32 s29, s52, 0
	s_sub_i32 s28, s28, s29
	s_ashr_i32 s29, s28, 31
	s_lshl_b64 s[80:81], s[28:29], s42
	s_add_i32 s30, s30, 2
	s_cmp_ge_i32 s30, s52
	s_cselect_b32 s28, s52, 0
	s_sub_i32 s28, s30, s28
	s_ashr_i32 s29, s28, 31
	s_lshl_b64 s[28:29], s[28:29], s42
	v_add_u32_e32 v142, s7, v187
	v_add_u32_e32 v158, s45, v187
	s_add_u32 s30, s4, s28
	ds_read_b128 v[130:133], v142
	ds_read_b128 v[134:137], v142 offset:1024
	ds_read_b128 v[138:141], v142 offset:2048
	ds_read_b128 v[142:145], v142 offset:3072
	ds_read_b128 v[146:149], v158
	ds_read_b128 v[150:153], v158 offset:1024
	ds_read_b128 v[154:157], v158 offset:2048
	ds_read_b128 v[158:161], v158 offset:3072
	s_addc_u32 s31, s5, s29
	s_add_u32 s28, s26, s28
	s_addc_u32 s29, s27, s29
	s_cmp_eq_u32 s53, s78
	s_cselect_b32 s34, s74, s30
	s_cselect_b32 s35, s75, s31
	s_cselect_b32 s31, s77, s29
	s_cselect_b32 s30, s76, s28
	s_add_u32 s28, s34, s54
	s_addc_u32 s29, s35, 0
	s_add_u32 s80, s72, s80
	s_addc_u32 s81, s73, s81
	s_add_i32 m0, s48, 0xc000
	ds_read_b128 v[172:175], v189
	ds_read_b128 v[176:179], v189 offset:1024
	ds_read_b128 v[180:183], v189 offset:2048
	ds_read_b128 v[190:193], v189 offset:3072
	ds_read_b128 v[194:197], v189 offset:4096
	ds_read_b128 v[212:215], v189 offset:5120
	ds_read_b128 v[216:219], v189 offset:6144
	ds_read_b128 v[220:223], v189 offset:7168
	global_load_lds_dwordx4 v0, s[80:81]
	s_add_i32 m0, s48, 0xe000
	s_nop 0
	global_load_lds_dwordx4 v162, s[80:81]
	s_waitcnt vmcnt(8)
	s_waitcnt lgkmcnt(0)
	s_barrier
	s_setprio 1
	s_waitcnt lgkmcnt(0)
	s_nop 0
	v_mfma_f32_16x16x32_bf16 v[126:129], v[130:133], v[172:175], v[126:129]
	v_mfma_f32_16x16x32_bf16 v[122:125], v[138:141], v[172:175], v[122:125]
	v_mfma_f32_16x16x32_bf16 v[110:113], v[130:133], v[180:183], v[110:113]
	v_mfma_f32_16x16x32_bf16 v[106:109], v[138:141], v[180:183], v[106:109]
	v_mfma_f32_16x16x32_bf16 v[94:97], v[130:133], v[194:197], v[94:97]
	v_mfma_f32_16x16x32_bf16 v[90:93], v[138:141], v[194:197], v[90:93]
	v_mfma_f32_16x16x32_bf16 v[78:81], v[130:133], v[216:219], v[78:81]
	v_mfma_f32_16x16x32_bf16 v[74:77], v[138:141], v[216:219], v[74:77]
	v_mfma_f32_16x16x32_bf16 v[126:129], v[134:137], v[176:179], v[126:129]
	v_mfma_f32_16x16x32_bf16 v[122:125], v[142:145], v[176:179], v[122:125]
	v_mfma_f32_16x16x32_bf16 v[110:113], v[134:137], v[190:193], v[110:113]
	v_mfma_f32_16x16x32_bf16 v[106:109], v[142:145], v[190:193], v[106:109]
	v_mfma_f32_16x16x32_bf16 v[94:97], v[134:137], v[212:215], v[94:97]
	v_mfma_f32_16x16x32_bf16 v[90:93], v[142:145], v[212:215], v[90:93]
	v_mfma_f32_16x16x32_bf16 v[78:81], v[134:137], v[220:223], v[78:81]
	v_mfma_f32_16x16x32_bf16 v[74:77], v[142:145], v[220:223], v[74:77]
	s_setprio 0
	s_setprio 1
	v_mfma_f32_16x16x32_bf16 v[118:121], v[146:149], v[172:175], v[118:121]
	v_mfma_f32_16x16x32_bf16 v[114:117], v[154:157], v[172:175], v[114:117]
	v_mfma_f32_16x16x32_bf16 v[102:105], v[146:149], v[180:183], v[102:105]
	v_mfma_f32_16x16x32_bf16 v[98:101], v[154:157], v[180:183], v[98:101]
	v_mfma_f32_16x16x32_bf16 v[86:89], v[146:149], v[194:197], v[86:89]
	v_mfma_f32_16x16x32_bf16 v[82:85], v[154:157], v[194:197], v[82:85]
	v_mfma_f32_16x16x32_bf16 v[70:73], v[146:149], v[216:219], v[70:73]
	v_mfma_f32_16x16x32_bf16 v[66:69], v[154:157], v[216:219], v[66:69]
	v_mfma_f32_16x16x32_bf16 v[118:121], v[150:153], v[176:179], v[118:121]
	v_mfma_f32_16x16x32_bf16 v[114:117], v[158:161], v[176:179], v[114:117]
	v_mfma_f32_16x16x32_bf16 v[102:105], v[150:153], v[190:193], v[102:105]
	v_mfma_f32_16x16x32_bf16 v[98:101], v[158:161], v[190:193], v[98:101]
	v_mfma_f32_16x16x32_bf16 v[86:89], v[150:153], v[212:215], v[86:89]
	v_mfma_f32_16x16x32_bf16 v[82:85], v[158:161], v[212:215], v[82:85]
	v_mfma_f32_16x16x32_bf16 v[70:73], v[150:153], v[220:223], v[70:73]
	s_barrier
	v_mfma_f32_16x16x32_bf16 v[66:69], v[158:161], v[220:223], v[66:69]
	s_setprio 0
	s_mov_b32 m0, s43
	s_add_u32 s80, s30, s41
	ds_read_b128 v[172:175], v189 offset:16384
	ds_read_b128 v[176:179], v189 offset:17408
	ds_read_b128 v[180:183], v189 offset:18432
	ds_read_b128 v[190:193], v189 offset:19456
	ds_read_b128 v[194:197], v189 offset:20480
	ds_read_b128 v[212:215], v189 offset:21504
	ds_read_b128 v[216:219], v189 offset:22528
	ds_read_b128 v[220:223], v189 offset:23552
	global_load_lds_dwordx4 v0, s[30:31]
	s_mov_b32 m0, s44
	s_addc_u32 s81, s31, 0
	global_load_lds_dwordx4 v162, s[30:31]
	s_mov_b32 m0, s46
	s_nop 0
	global_load_lds_dwordx4 v0, s[80:81]
	s_mov_b32 m0, s47
	s_nop 0
	global_load_lds_dwordx4 v162, s[80:81]
	s_mov_b32 m0, s48
	s_nop 0
	global_load_lds_dwordx4 v0, s[34:35]
	s_mov_b32 m0, s49
	s_nop 0
	global_load_lds_dwordx4 v162, s[34:35]
	s_waitcnt vmcnt(8)
	s_waitcnt lgkmcnt(0)
	s_barrier
	s_setprio 1
	s_waitcnt lgkmcnt(0)
	s_nop 0
	v_mfma_f32_16x16x32_bf16 v[62:65], v[130:133], v[172:175], v[62:65]
	v_mfma_f32_16x16x32_bf16 v[58:61], v[138:141], v[172:175], v[58:61]
	v_mfma_f32_16x16x32_bf16 v[46:49], v[130:133], v[180:183], v[46:49]
	v_mfma_f32_16x16x32_bf16 v[42:45], v[138:141], v[180:183], v[42:45]
	v_mfma_f32_16x16x32_bf16 v[30:33], v[130:133], v[194:197], v[30:33]
	v_mfma_f32_16x16x32_bf16 v[26:29], v[138:141], v[194:197], v[26:29]
	v_mfma_f32_16x16x32_bf16 v[14:17], v[130:133], v[216:219], v[14:17]
	v_mfma_f32_16x16x32_bf16 v[10:13], v[138:141], v[216:219], v[10:13]
	v_mfma_f32_16x16x32_bf16 v[62:65], v[134:137], v[176:179], v[62:65]
	v_mfma_f32_16x16x32_bf16 v[58:61], v[142:145], v[176:179], v[58:61]
	v_mfma_f32_16x16x32_bf16 v[46:49], v[134:137], v[190:193], v[46:49]
	v_mfma_f32_16x16x32_bf16 v[42:45], v[142:145], v[190:193], v[42:45]
	v_mfma_f32_16x16x32_bf16 v[30:33], v[134:137], v[212:215], v[30:33]
	v_mfma_f32_16x16x32_bf16 v[26:29], v[142:145], v[212:215], v[26:29]
	v_mfma_f32_16x16x32_bf16 v[14:17], v[134:137], v[220:223], v[14:17]
	v_mfma_f32_16x16x32_bf16 v[10:13], v[142:145], v[220:223], v[10:13]
	s_setprio 0
	s_setprio 1
	v_mfma_f32_16x16x32_bf16 v[54:57], v[146:149], v[172:175], v[54:57]
	v_mfma_f32_16x16x32_bf16 v[50:53], v[154:157], v[172:175], v[50:53]
	v_mfma_f32_16x16x32_bf16 v[38:41], v[146:149], v[180:183], v[38:41]
	v_mfma_f32_16x16x32_bf16 v[34:37], v[154:157], v[180:183], v[34:37]
	v_mfma_f32_16x16x32_bf16 v[22:25], v[146:149], v[194:197], v[22:25]
	v_mfma_f32_16x16x32_bf16 v[18:21], v[154:157], v[194:197], v[18:21]
	v_mfma_f32_16x16x32_bf16 v[6:9], v[146:149], v[216:219], v[6:9]
	v_mfma_f32_16x16x32_bf16 v[2:5], v[154:157], v[216:219], v[2:5]
	v_mfma_f32_16x16x32_bf16 v[54:57], v[150:153], v[176:179], v[54:57]
	v_mfma_f32_16x16x32_bf16 v[50:53], v[158:161], v[176:179], v[50:53]
	v_mfma_f32_16x16x32_bf16 v[38:41], v[150:153], v[190:193], v[38:41]
	v_mfma_f32_16x16x32_bf16 v[34:37], v[158:161], v[190:193], v[34:37]
	v_mfma_f32_16x16x32_bf16 v[22:25], v[150:153], v[212:215], v[22:25]
	v_mfma_f32_16x16x32_bf16 v[18:21], v[158:161], v[212:215], v[18:21]
	v_mfma_f32_16x16x32_bf16 v[6:9], v[150:153], v[220:223], v[6:9]
	s_barrier
	v_mfma_f32_16x16x32_bf16 v[2:5], v[158:161], v[220:223], v[2:5]
	s_setprio 0
	v_add_u32_e32 v142, s56, v187
	v_add_u32_e32 v158, s62, v187
	ds_read_b128 v[130:133], v142
	ds_read_b128 v[134:137], v142 offset:1024
	ds_read_b128 v[138:141], v142 offset:2048
	ds_read_b128 v[142:145], v142 offset:3072
	ds_read_b128 v[146:149], v158
	ds_read_b128 v[150:153], v158 offset:1024
	ds_read_b128 v[154:157], v158 offset:2048
	ds_read_b128 v[158:161], v158 offset:3072
	s_add_u32 s34, s34, s41
	s_addc_u32 s35, s35, 0
	s_mov_b32 m0, s50
	ds_read_b128 v[172:175], v189 offset:32768
	ds_read_b128 v[176:179], v189 offset:33792
	ds_read_b128 v[180:183], v189 offset:34816
	ds_read_b128 v[190:193], v189 offset:35840
	ds_read_b128 v[194:197], v189 offset:36864
	ds_read_b128 v[212:215], v189 offset:37888
	ds_read_b128 v[216:219], v189 offset:38912
	ds_read_b128 v[220:223], v189 offset:39936
	global_load_lds_dwordx4 v0, s[34:35]
	s_mov_b32 m0, s51
	s_nop 0
	global_load_lds_dwordx4 v162, s[34:35]
	s_waitcnt vmcnt(8)
	s_waitcnt lgkmcnt(0)
	s_barrier
	s_setprio 1
	s_waitcnt lgkmcnt(0)
	s_nop 0
	v_mfma_f32_16x16x32_bf16 v[126:129], v[130:133], v[172:175], v[126:129]
	v_mfma_f32_16x16x32_bf16 v[122:125], v[138:141], v[172:175], v[122:125]
	v_mfma_f32_16x16x32_bf16 v[110:113], v[130:133], v[180:183], v[110:113]
	v_mfma_f32_16x16x32_bf16 v[106:109], v[138:141], v[180:183], v[106:109]
	v_mfma_f32_16x16x32_bf16 v[94:97], v[130:133], v[194:197], v[94:97]
	v_mfma_f32_16x16x32_bf16 v[90:93], v[138:141], v[194:197], v[90:93]
	v_mfma_f32_16x16x32_bf16 v[78:81], v[130:133], v[216:219], v[78:81]
	v_mfma_f32_16x16x32_bf16 v[74:77], v[138:141], v[216:219], v[74:77]
	v_mfma_f32_16x16x32_bf16 v[126:129], v[134:137], v[176:179], v[126:129]
	v_mfma_f32_16x16x32_bf16 v[122:125], v[142:145], v[176:179], v[122:125]
	v_mfma_f32_16x16x32_bf16 v[110:113], v[134:137], v[190:193], v[110:113]
	v_mfma_f32_16x16x32_bf16 v[106:109], v[142:145], v[190:193], v[106:109]
	v_mfma_f32_16x16x32_bf16 v[94:97], v[134:137], v[212:215], v[94:97]
	v_mfma_f32_16x16x32_bf16 v[90:93], v[142:145], v[212:215], v[90:93]
	v_mfma_f32_16x16x32_bf16 v[78:81], v[134:137], v[220:223], v[78:81]
	v_mfma_f32_16x16x32_bf16 v[74:77], v[142:145], v[220:223], v[74:77]
	s_setprio 0
	s_setprio 1
	v_mfma_f32_16x16x32_bf16 v[118:121], v[146:149], v[172:175], v[118:121]
	v_mfma_f32_16x16x32_bf16 v[114:117], v[154:157], v[172:175], v[114:117]
	v_mfma_f32_16x16x32_bf16 v[102:105], v[146:149], v[180:183], v[102:105]
	v_mfma_f32_16x16x32_bf16 v[98:101], v[154:157], v[180:183], v[98:101]
	v_mfma_f32_16x16x32_bf16 v[86:89], v[146:149], v[194:197], v[86:89]
	v_mfma_f32_16x16x32_bf16 v[82:85], v[154:157], v[194:197], v[82:85]
	v_mfma_f32_16x16x32_bf16 v[70:73], v[146:149], v[216:219], v[70:73]
	v_mfma_f32_16x16x32_bf16 v[66:69], v[154:157], v[216:219], v[66:69]
	v_mfma_f32_16x16x32_bf16 v[118:121], v[150:153], v[176:179], v[118:121]
	v_mfma_f32_16x16x32_bf16 v[114:117], v[158:161], v[176:179], v[114:117]
	v_mfma_f32_16x16x32_bf16 v[102:105], v[150:153], v[190:193], v[102:105]
	v_mfma_f32_16x16x32_bf16 v[98:101], v[158:161], v[190:193], v[98:101]
	v_mfma_f32_16x16x32_bf16 v[86:89], v[150:153], v[212:215], v[86:89]
	v_mfma_f32_16x16x32_bf16 v[82:85], v[158:161], v[212:215], v[82:85]
	v_mfma_f32_16x16x32_bf16 v[70:73], v[150:153], v[220:223], v[70:73]
	s_barrier
	v_mfma_f32_16x16x32_bf16 v[66:69], v[158:161], v[220:223], v[66:69]
	s_setprio 0
	s_add_u32 s30, s30, s54
	s_addc_u32 s31, s31, 0
	s_mov_b32 m0, s57
	ds_read_b128 v[172:175], v189 offset:49152
	ds_read_b128 v[176:179], v189 offset:50176
	ds_read_b128 v[180:183], v189 offset:51200
	ds_read_b128 v[190:193], v189 offset:52224
	ds_read_b128 v[194:197], v189 offset:53248
	ds_read_b128 v[212:215], v189 offset:54272
	ds_read_b128 v[216:219], v189 offset:55296
	ds_read_b128 v[220:223], v189 offset:56320
	global_load_lds_dwordx4 v0, s[30:31]
	v_lshl_add_u64 v[168:169], s[30:31], 0, v[162:163]
	s_add_u32 s30, s30, s41
	s_mov_b32 m0, s58
	s_addc_u32 s31, s31, 0
	global_load_lds_dwordx4 v[168:169], off
	s_mov_b32 m0, s63
	s_nop 0
	global_load_lds_dwordx4 v0, s[30:31]
	s_mov_b32 m0, s64
	s_nop 0
	global_load_lds_dwordx4 v162, s[30:31]
	s_mov_b32 m0, s59
	s_nop 0
	global_load_lds_dwordx4 v0, s[28:29]
	s_mov_b32 m0, s60
	s_nop 0
	global_load_lds_dwordx4 v162, s[28:29]
	s_waitcnt vmcnt(8)
	s_waitcnt lgkmcnt(0)
	s_barrier
	s_setprio 1
	s_waitcnt lgkmcnt(0)
	s_nop 0
	v_mfma_f32_16x16x32_bf16 v[62:65], v[130:133], v[172:175], v[62:65]
	v_mfma_f32_16x16x32_bf16 v[58:61], v[138:141], v[172:175], v[58:61]
	v_mfma_f32_16x16x32_bf16 v[46:49], v[130:133], v[180:183], v[46:49]
	v_mfma_f32_16x16x32_bf16 v[42:45], v[138:141], v[180:183], v[42:45]
	v_mfma_f32_16x16x32_bf16 v[30:33], v[130:133], v[194:197], v[30:33]
	v_mfma_f32_16x16x32_bf16 v[26:29], v[138:141], v[194:197], v[26:29]
	v_mfma_f32_16x16x32_bf16 v[14:17], v[130:133], v[216:219], v[14:17]
	v_mfma_f32_16x16x32_bf16 v[10:13], v[138:141], v[216:219], v[10:13]
	v_mfma_f32_16x16x32_bf16 v[62:65], v[134:137], v[176:179], v[62:65]
	v_mfma_f32_16x16x32_bf16 v[58:61], v[142:145], v[176:179], v[58:61]
	v_mfma_f32_16x16x32_bf16 v[46:49], v[134:137], v[190:193], v[46:49]
	v_mfma_f32_16x16x32_bf16 v[42:45], v[142:145], v[190:193], v[42:45]
	v_mfma_f32_16x16x32_bf16 v[30:33], v[134:137], v[212:215], v[30:33]
	v_mfma_f32_16x16x32_bf16 v[26:29], v[142:145], v[212:215], v[26:29]
	v_mfma_f32_16x16x32_bf16 v[14:17], v[134:137], v[220:223], v[14:17]
	v_mfma_f32_16x16x32_bf16 v[10:13], v[142:145], v[220:223], v[10:13]
	s_setprio 0
	s_setprio 1
	v_mfma_f32_16x16x32_bf16 v[54:57], v[146:149], v[172:175], v[54:57]
	v_mfma_f32_16x16x32_bf16 v[50:53], v[154:157], v[172:175], v[50:53]
	v_mfma_f32_16x16x32_bf16 v[38:41], v[146:149], v[180:183], v[38:41]
	v_mfma_f32_16x16x32_bf16 v[34:37], v[154:157], v[180:183], v[34:37]
	v_mfma_f32_16x16x32_bf16 v[22:25], v[146:149], v[194:197], v[22:25]
	v_mfma_f32_16x16x32_bf16 v[18:21], v[154:157], v[194:197], v[18:21]
	v_mfma_f32_16x16x32_bf16 v[6:9], v[146:149], v[216:219], v[6:9]
	v_mfma_f32_16x16x32_bf16 v[2:5], v[154:157], v[216:219], v[2:5]
	v_mfma_f32_16x16x32_bf16 v[54:57], v[150:153], v[176:179], v[54:57]
	v_mfma_f32_16x16x32_bf16 v[50:53], v[158:161], v[176:179], v[50:53]
	v_mfma_f32_16x16x32_bf16 v[38:41], v[150:153], v[190:193], v[38:41]
	v_mfma_f32_16x16x32_bf16 v[34:37], v[158:161], v[190:193], v[34:37]
	v_mfma_f32_16x16x32_bf16 v[22:25], v[150:153], v[212:215], v[22:25]
	v_mfma_f32_16x16x32_bf16 v[18:21], v[158:161], v[212:215], v[18:21]
	v_mfma_f32_16x16x32_bf16 v[6:9], v[150:153], v[220:223], v[6:9]
	s_barrier
	v_mfma_f32_16x16x32_bf16 v[2:5], v[158:161], v[220:223], v[2:5]
	s_setprio 0
	s_add_i32 s78, s78, 2
	s_cmp_ge_i32 s78, s52
	s_cbranch_scc0 .LBB0_1464

.LBB0_1983:
	s_add_i32 s3, s3, 1
	s_cmp_ge_i32 s3, s71
	s_cselect_b32 vcc_lo, s71, 0
	s_sub_i32 vcc_lo, s3, vcc_lo
	s_ashr_i32 vcc_hi, vcc_lo, 31
	v_add_u32_e32 v154, s1, v190
	s_lshl_b64 vcc, vcc, s75
	ds_read_b128 v[160:163], v154
	ds_read_b128 v[172:175], v154 offset:1024
	ds_read_b128 v[176:179], v154 offset:2048
	ds_read_b128 v[180:183], v154 offset:3072
	v_add_u32_e32 v154, s93, v190
	s_add_u32 vcc_lo, s65, vcc_lo
	ds_read_b128 v[196:199], v154
	ds_read_b128 v[212:215], v154 offset:1024
	ds_read_b128 v[216:219], v154 offset:2048
	ds_read_b128 v[220:223], v154 offset:3072
	s_addc_u32 vcc_hi, s66, vcc_hi
	s_and_b64 s[52:53], exec, s[52:53]
	s_cselect_b32 s52, s16, s54
	s_cselect_b32 s3, s17, s55
	s_add_u32 s54, s65, s52
	s_addc_u32 s55, s66, s3
	s_add_u32 s52, s54, s73
	s_addc_u32 s53, s55, 0
	s_add_i32 m0, s78, 0xc000
	ds_read_b128 v[224:227], v192
	ds_read_b128 v[228:231], v192 offset:1024
	ds_read_b128 v[232:235], v192 offset:2048
	ds_read_b128 v[236:239], v192 offset:3072
	ds_read_b128 v[240:243], v192 offset:4096
	ds_read_b128 v[244:247], v192 offset:5120
	ds_read_b128 v[248:251], v192 offset:6144
	ds_read_b128 v[168:171], v192 offset:7168
	global_load_lds_dwordx4 v0, vcc
	s_add_i32 m0, s78, 0xe000
	s_nop 0
	global_load_lds_dwordx4 v144, vcc
	s_waitcnt vmcnt(8)
	s_waitcnt lgkmcnt(0)
	s_barrier
	s_setprio 1
	s_waitcnt lgkmcnt(0)
	s_nop 0
	v_mfma_f32_16x16x32_bf16 v[122:125], v[160:163], v[224:227], v[122:125]
	v_mfma_f32_16x16x32_bf16 v[114:117], v[176:179], v[224:227], v[114:117]
	v_mfma_f32_16x16x32_bf16 v[106:109], v[160:163], v[232:235], v[106:109]
	v_mfma_f32_16x16x32_bf16 v[98:101], v[176:179], v[232:235], v[98:101]
	v_mfma_f32_16x16x32_bf16 v[90:93], v[160:163], v[240:243], v[90:93]
	v_mfma_f32_16x16x32_bf16 v[82:85], v[176:179], v[240:243], v[82:85]
	v_mfma_f32_16x16x32_bf16 v[74:77], v[160:163], v[248:251], v[74:77]
	v_mfma_f32_16x16x32_bf16 v[66:69], v[176:179], v[248:251], v[66:69]
	v_mfma_f32_16x16x32_bf16 v[122:125], v[172:175], v[228:231], v[122:125]
	v_mfma_f32_16x16x32_bf16 v[114:117], v[180:183], v[228:231], v[114:117]
	v_mfma_f32_16x16x32_bf16 v[106:109], v[172:175], v[236:239], v[106:109]
	v_mfma_f32_16x16x32_bf16 v[98:101], v[180:183], v[236:239], v[98:101]
	v_mfma_f32_16x16x32_bf16 v[90:93], v[172:175], v[244:247], v[90:93]
	v_mfma_f32_16x16x32_bf16 v[82:85], v[180:183], v[244:247], v[82:85]
	v_mfma_f32_16x16x32_bf16 v[74:77], v[172:175], v[168:171], v[74:77]
	v_mfma_f32_16x16x32_bf16 v[66:69], v[180:183], v[168:171], v[66:69]
	s_setprio 0
	s_setprio 1
	v_mfma_f32_16x16x32_bf16 v[126:129], v[196:199], v[224:227], v[126:129]
	v_mfma_f32_16x16x32_bf16 v[118:121], v[216:219], v[224:227], v[118:121]
	v_mfma_f32_16x16x32_bf16 v[110:113], v[196:199], v[232:235], v[110:113]
	v_mfma_f32_16x16x32_bf16 v[102:105], v[216:219], v[232:235], v[102:105]
	v_mfma_f32_16x16x32_bf16 v[94:97], v[196:199], v[240:243], v[94:97]
	v_mfma_f32_16x16x32_bf16 v[86:89], v[216:219], v[240:243], v[86:89]
	v_mfma_f32_16x16x32_bf16 v[78:81], v[196:199], v[248:251], v[78:81]
	v_mfma_f32_16x16x32_bf16 v[70:73], v[216:219], v[248:251], v[70:73]
	v_mfma_f32_16x16x32_bf16 v[126:129], v[212:215], v[228:231], v[126:129]
	v_mfma_f32_16x16x32_bf16 v[118:121], v[220:223], v[228:231], v[118:121]
	v_mfma_f32_16x16x32_bf16 v[110:113], v[212:215], v[236:239], v[110:113]
	v_mfma_f32_16x16x32_bf16 v[102:105], v[220:223], v[236:239], v[102:105]
	v_mfma_f32_16x16x32_bf16 v[94:97], v[212:215], v[244:247], v[94:97]
	v_mfma_f32_16x16x32_bf16 v[86:89], v[220:223], v[244:247], v[86:89]
	v_mfma_f32_16x16x32_bf16 v[78:81], v[212:215], v[168:171], v[78:81]
	s_barrier
	v_mfma_f32_16x16x32_bf16 v[70:73], v[220:223], v[168:171], v[70:73]
	s_setprio 0
	s_mov_b32 m0, s13
	s_add_u32 vcc_lo, s50, s74
	ds_read_b128 v[168:171], v192 offset:16384
	ds_read_b128 v[224:227], v192 offset:17408
	ds_read_b128 v[228:231], v192 offset:18432
	ds_read_b128 v[232:235], v192 offset:19456
	ds_read_b128 v[236:239], v192 offset:20480
	ds_read_b128 v[240:243], v192 offset:21504
	ds_read_b128 v[244:247], v192 offset:22528
	ds_read_b128 v[248:251], v192 offset:23552
	global_load_lds_dwordx4 v130, s[50:51]
	s_mov_b32 m0, s76
	s_addc_u32 vcc_hi, s51, 0
	global_load_lds_dwordx4 v132, s[50:51]
	s_mov_b32 m0, s79
	s_nop 0
	global_load_lds_dwordx4 v130, vcc
	s_mov_b32 m0, s77
	s_nop 0
	global_load_lds_dwordx4 v132, vcc
	s_mov_b32 m0, s78
	s_nop 0
	global_load_lds_dwordx4 v149, s[54:55]
	s_mov_b32 m0, s80
	s_nop 0
	global_load_lds_dwordx4 v147, s[54:55]
	s_waitcnt vmcnt(8)
	s_waitcnt lgkmcnt(0)
	s_barrier
	s_setprio 1
	s_waitcnt lgkmcnt(0)
	s_nop 0
	v_mfma_f32_16x16x32_bf16 v[58:61], v[160:163], v[168:171], v[58:61]
	v_mfma_f32_16x16x32_bf16 v[50:53], v[176:179], v[168:171], v[50:53]
	v_mfma_f32_16x16x32_bf16 v[42:45], v[160:163], v[228:231], v[42:45]
	v_mfma_f32_16x16x32_bf16 v[38:41], v[176:179], v[228:231], v[38:41]
	v_mfma_f32_16x16x32_bf16 v[26:29], v[160:163], v[236:239], v[26:29]
	v_mfma_f32_16x16x32_bf16 v[18:21], v[176:179], v[236:239], v[18:21]
	v_mfma_f32_16x16x32_bf16 v[10:13], v[160:163], v[244:247], v[10:13]
	v_mfma_f32_16x16x32_bf16 v[6:9], v[176:179], v[244:247], v[6:9]
	v_mfma_f32_16x16x32_bf16 v[58:61], v[172:175], v[224:227], v[58:61]
	v_mfma_f32_16x16x32_bf16 v[50:53], v[180:183], v[224:227], v[50:53]
	v_mfma_f32_16x16x32_bf16 v[42:45], v[172:175], v[232:235], v[42:45]
	v_mfma_f32_16x16x32_bf16 v[38:41], v[180:183], v[232:235], v[38:41]
	v_mfma_f32_16x16x32_bf16 v[26:29], v[172:175], v[240:243], v[26:29]
	v_mfma_f32_16x16x32_bf16 v[18:21], v[180:183], v[240:243], v[18:21]
	v_mfma_f32_16x16x32_bf16 v[10:13], v[172:175], v[248:251], v[10:13]
	v_mfma_f32_16x16x32_bf16 v[6:9], v[180:183], v[248:251], v[6:9]
	s_setprio 0
	s_setprio 1
	v_mfma_f32_16x16x32_bf16 v[62:65], v[196:199], v[168:171], v[62:65]
	v_mfma_f32_16x16x32_bf16 v[54:57], v[216:219], v[168:171], v[54:57]
	v_mfma_f32_16x16x32_bf16 v[46:49], v[196:199], v[228:231], v[46:49]
	v_mfma_f32_16x16x32_bf16 v[34:37], v[216:219], v[228:231], v[34:37]
	v_mfma_f32_16x16x32_bf16 v[30:33], v[196:199], v[236:239], v[30:33]
	v_mfma_f32_16x16x32_bf16 v[22:25], v[216:219], v[236:239], v[22:25]
	v_mfma_f32_16x16x32_bf16 v[14:17], v[196:199], v[244:247], v[14:17]
	v_mfma_f32_16x16x32_bf16 v[2:5], v[216:219], v[244:247], v[2:5]
	v_mfma_f32_16x16x32_bf16 v[62:65], v[212:215], v[224:227], v[62:65]
	v_mfma_f32_16x16x32_bf16 v[54:57], v[220:223], v[224:227], v[54:57]
	v_mfma_f32_16x16x32_bf16 v[46:49], v[212:215], v[232:235], v[46:49]
	v_mfma_f32_16x16x32_bf16 v[34:37], v[220:223], v[232:235], v[34:37]
	v_mfma_f32_16x16x32_bf16 v[30:33], v[212:215], v[240:243], v[30:33]
	v_mfma_f32_16x16x32_bf16 v[22:25], v[220:223], v[240:243], v[22:25]
	v_mfma_f32_16x16x32_bf16 v[14:17], v[212:215], v[248:251], v[14:17]
	s_barrier
	v_mfma_f32_16x16x32_bf16 v[2:5], v[220:223], v[248:251], v[2:5]
	s_setprio 0
	v_add_u32_e32 v154, s94, v190
	ds_read_b128 v[160:163], v154
	ds_read_b128 v[168:171], v154 offset:1024
	ds_read_b128 v[172:175], v154 offset:2048
	ds_read_b128 v[176:179], v154 offset:3072
	v_add_u32_e32 v154, s95, v190
	ds_read_b128 v[180:183], v154
	ds_read_b128 v[196:199], v154 offset:1024
	ds_read_b128 v[212:215], v154 offset:2048
	ds_read_b128 v[216:219], v154 offset:3072
	s_mov_b32 m0, s81
	ds_read_b128 v[220:223], v192 offset:32768
	ds_read_b128 v[224:227], v192 offset:33792
	ds_read_b128 v[228:231], v192 offset:34816
	ds_read_b128 v[232:235], v192 offset:35840
	ds_read_b128 v[236:239], v192 offset:36864
	ds_read_b128 v[240:243], v192 offset:37888
	ds_read_b128 v[244:247], v192 offset:38912
	ds_read_b128 v[248:251], v192 offset:39936
	global_load_lds_dwordx4 v152, s[54:55]
	s_mov_b32 m0, s82
	s_nop 0
	global_load_lds_dwordx4 v150, s[54:55]
	s_waitcnt vmcnt(8)
	s_waitcnt lgkmcnt(0)
	s_barrier
	s_setprio 1
	s_waitcnt lgkmcnt(0)
	s_nop 0
	v_mfma_f32_16x16x32_bf16 v[122:125], v[160:163], v[220:223], v[122:125]
	v_mfma_f32_16x16x32_bf16 v[114:117], v[172:175], v[220:223], v[114:117]
	v_mfma_f32_16x16x32_bf16 v[106:109], v[160:163], v[228:231], v[106:109]
	v_mfma_f32_16x16x32_bf16 v[98:101], v[172:175], v[228:231], v[98:101]
	v_mfma_f32_16x16x32_bf16 v[90:93], v[160:163], v[236:239], v[90:93]
	v_mfma_f32_16x16x32_bf16 v[82:85], v[172:175], v[236:239], v[82:85]
	v_mfma_f32_16x16x32_bf16 v[74:77], v[160:163], v[244:247], v[74:77]
	v_mfma_f32_16x16x32_bf16 v[66:69], v[172:175], v[244:247], v[66:69]
	v_mfma_f32_16x16x32_bf16 v[122:125], v[168:171], v[224:227], v[122:125]
	v_mfma_f32_16x16x32_bf16 v[114:117], v[176:179], v[224:227], v[114:117]
	v_mfma_f32_16x16x32_bf16 v[106:109], v[168:171], v[232:235], v[106:109]
	v_mfma_f32_16x16x32_bf16 v[98:101], v[176:179], v[232:235], v[98:101]
	v_mfma_f32_16x16x32_bf16 v[90:93], v[168:171], v[240:243], v[90:93]
	v_mfma_f32_16x16x32_bf16 v[82:85], v[176:179], v[240:243], v[82:85]
	v_mfma_f32_16x16x32_bf16 v[74:77], v[168:171], v[248:251], v[74:77]
	v_mfma_f32_16x16x32_bf16 v[66:69], v[176:179], v[248:251], v[66:69]
	s_setprio 0
	s_setprio 1
	v_mfma_f32_16x16x32_bf16 v[126:129], v[180:183], v[220:223], v[126:129]
	v_mfma_f32_16x16x32_bf16 v[118:121], v[212:215], v[220:223], v[118:121]
	v_mfma_f32_16x16x32_bf16 v[110:113], v[180:183], v[228:231], v[110:113]
	v_mfma_f32_16x16x32_bf16 v[102:105], v[212:215], v[228:231], v[102:105]
	v_mfma_f32_16x16x32_bf16 v[94:97], v[180:183], v[236:239], v[94:97]
	v_mfma_f32_16x16x32_bf16 v[86:89], v[212:215], v[236:239], v[86:89]
	v_mfma_f32_16x16x32_bf16 v[78:81], v[180:183], v[244:247], v[78:81]
	v_mfma_f32_16x16x32_bf16 v[70:73], v[212:215], v[244:247], v[70:73]
	v_mfma_f32_16x16x32_bf16 v[126:129], v[196:199], v[224:227], v[126:129]
	v_mfma_f32_16x16x32_bf16 v[118:121], v[216:219], v[224:227], v[118:121]
	v_mfma_f32_16x16x32_bf16 v[110:113], v[196:199], v[232:235], v[110:113]
	v_mfma_f32_16x16x32_bf16 v[102:105], v[216:219], v[232:235], v[102:105]
	v_mfma_f32_16x16x32_bf16 v[94:97], v[196:199], v[240:243], v[94:97]
	v_mfma_f32_16x16x32_bf16 v[86:89], v[216:219], v[240:243], v[86:89]
	v_mfma_f32_16x16x32_bf16 v[78:81], v[196:199], v[248:251], v[78:81]
	s_barrier
	v_mfma_f32_16x16x32_bf16 v[70:73], v[216:219], v[248:251], v[70:73]
	s_setprio 0
	s_add_u32 s50, s50, s73
	s_addc_u32 s51, s51, 0
	s_mov_b32 m0, s60
	ds_read_b128 v[150:153], v192 offset:49152
	ds_read_b128 v[220:223], v192 offset:50176
	ds_read_b128 v[224:227], v192 offset:51200
	ds_read_b128 v[228:231], v192 offset:52224
	ds_read_b128 v[232:235], v192 offset:53248
	ds_read_b128 v[236:239], v192 offset:54272
	ds_read_b128 v[240:243], v192 offset:55296
	ds_read_b128 v[244:247], v192 offset:56320
	global_load_lds_dwordx4 v130, s[50:51]
	v_lshl_add_u64 v[156:157], s[50:51], 0, v[132:133]
	s_add_u32 s50, s50, s74
	s_mov_b32 m0, s83
	s_addc_u32 s51, s51, 0
	global_load_lds_dwordx4 v[156:157], off
	s_mov_b32 m0, s88
	s_nop 0
	global_load_lds_dwordx4 v130, s[50:51]
	s_mov_b32 m0, s89
	s_nop 0
	global_load_lds_dwordx4 v132, s[50:51]
	s_mov_b32 m0, s84
	s_nop 0
	global_load_lds_dwordx4 v149, s[52:53]
	s_mov_b32 m0, s87
	s_nop 0
	global_load_lds_dwordx4 v147, s[52:53]
	s_waitcnt vmcnt(8)
	s_waitcnt lgkmcnt(0)
	s_barrier
	s_setprio 1
	s_waitcnt lgkmcnt(0)
	s_nop 0
	v_mfma_f32_16x16x32_bf16 v[58:61], v[160:163], v[150:153], v[58:61]
	v_mfma_f32_16x16x32_bf16 v[50:53], v[172:175], v[150:153], v[50:53]
	v_mfma_f32_16x16x32_bf16 v[42:45], v[160:163], v[224:227], v[42:45]
	v_mfma_f32_16x16x32_bf16 v[38:41], v[172:175], v[224:227], v[38:41]
	v_mfma_f32_16x16x32_bf16 v[26:29], v[160:163], v[232:235], v[26:29]
	v_mfma_f32_16x16x32_bf16 v[18:21], v[172:175], v[232:235], v[18:21]
	v_mfma_f32_16x16x32_bf16 v[10:13], v[160:163], v[240:243], v[10:13]
	v_mfma_f32_16x16x32_bf16 v[6:9], v[172:175], v[240:243], v[6:9]
	v_mfma_f32_16x16x32_bf16 v[58:61], v[168:171], v[220:223], v[58:61]
	v_mfma_f32_16x16x32_bf16 v[50:53], v[176:179], v[220:223], v[50:53]
	v_mfma_f32_16x16x32_bf16 v[42:45], v[168:171], v[228:231], v[42:45]
	v_mfma_f32_16x16x32_bf16 v[38:41], v[176:179], v[228:231], v[38:41]
	v_mfma_f32_16x16x32_bf16 v[26:29], v[168:171], v[236:239], v[26:29]
	v_mfma_f32_16x16x32_bf16 v[18:21], v[176:179], v[236:239], v[18:21]
	v_mfma_f32_16x16x32_bf16 v[10:13], v[168:171], v[244:247], v[10:13]
	v_mfma_f32_16x16x32_bf16 v[6:9], v[176:179], v[244:247], v[6:9]
	s_setprio 0
	s_setprio 1
	v_mfma_f32_16x16x32_bf16 v[62:65], v[180:183], v[150:153], v[62:65]
	v_mfma_f32_16x16x32_bf16 v[54:57], v[212:215], v[150:153], v[54:57]
	v_mfma_f32_16x16x32_bf16 v[46:49], v[180:183], v[224:227], v[46:49]
	v_mfma_f32_16x16x32_bf16 v[34:37], v[212:215], v[224:227], v[34:37]
	v_mfma_f32_16x16x32_bf16 v[30:33], v[180:183], v[232:235], v[30:33]
	v_mfma_f32_16x16x32_bf16 v[22:25], v[212:215], v[232:235], v[22:25]
	v_mfma_f32_16x16x32_bf16 v[14:17], v[180:183], v[240:243], v[14:17]
	v_mfma_f32_16x16x32_bf16 v[2:5], v[212:215], v[240:243], v[2:5]
	v_mfma_f32_16x16x32_bf16 v[62:65], v[196:199], v[220:223], v[62:65]
	v_mfma_f32_16x16x32_bf16 v[54:57], v[216:219], v[220:223], v[54:57]
	v_mfma_f32_16x16x32_bf16 v[46:49], v[196:199], v[228:231], v[46:49]
	v_mfma_f32_16x16x32_bf16 v[34:37], v[216:219], v[228:231], v[34:37]
	v_mfma_f32_16x16x32_bf16 v[30:33], v[196:199], v[236:239], v[30:33]
	v_mfma_f32_16x16x32_bf16 v[22:25], v[216:219], v[236:239], v[22:25]
	v_mfma_f32_16x16x32_bf16 v[14:17], v[196:199], v[244:247], v[14:17]
	s_barrier
	v_mfma_f32_16x16x32_bf16 v[2:5], v[216:219], v[244:247], v[2:5]
	s_setprio 0
	s_add_i32 s2, s2, 2
	s_cmp_ge_i32 s2, s71
	s_cbranch_scc1 .LBB0_1986

.LBB0_2148:
	s_add_i32 s9, s10, s8
	s_add_i32 s28, s9, 1
	s_cmp_ge_i32 s28, s75
	s_cselect_b32 s29, s75, 0
	s_sub_i32 s28, s28, s29
	s_ashr_i32 s29, s28, 31
	s_lshl_b64 s[40:41], s[28:29], s36
	s_add_i32 s9, s9, 2
	s_cmp_ge_i32 s9, s75
	s_cselect_b32 s28, s75, 0
	s_sub_i32 s28, s9, s28
	s_ashr_i32 s29, s28, 31
	v_add_u32_e32 v0, s11, v180
	s_lshl_b64 s[28:29], s[28:29], s36
	ds_read_b128 v[140:143], v0
	ds_read_b128 v[144:147], v0 offset:1024
	ds_read_b128 v[148:151], v0 offset:2048
	ds_read_b128 v[152:155], v0 offset:3072
	v_add_u32_e32 v0, s66, v180
	s_add_u32 s9, s24, s28
	ds_read_b128 v[156:159], v0
	ds_read_b128 v[160:163], v0 offset:1024
	ds_read_b128 v[168:171], v0 offset:2048
	ds_read_b128 v[172:175], v0 offset:3072
	s_addc_u32 s30, s25, s29
	s_add_u32 s28, s26, s28
	s_addc_u32 s29, s27, s29
	s_cmp_eq_u32 s76, s8
	s_cselect_b32 s34, s91, s9
	s_cselect_b32 s35, s97, s30
	s_cselect_b32 s31, vcc_hi, s29
	s_cselect_b32 s30, vcc_lo, s28
	s_add_u32 s28, s34, s47
	s_addc_u32 s29, s35, 0
	s_add_u32 s40, s85, s40
	s_addc_u32 s41, s86, s41
	s_add_i32 m0, s71, 0xc000
	ds_read_b128 v[184:187], v182
	ds_read_b128 v[188:191], v182 offset:1024
	ds_read_b128 v[192:195], v182 offset:2048
	ds_read_b128 v[196:199], v182 offset:3072
	ds_read_b128 v[212:215], v182 offset:4096
	ds_read_b128 v[216:219], v182 offset:5120
	ds_read_b128 v[220:223], v182 offset:6144
	ds_read_b128 v[224:227], v182 offset:7168
	global_load_lds_dwordx4 v134, s[40:41]
	s_add_i32 m0, s71, 0xe000
	s_nop 0
	global_load_lds_dwordx4 v136, s[40:41]
	s_waitcnt vmcnt(8)
	s_waitcnt lgkmcnt(0)
	s_barrier
	s_setprio 1
	s_waitcnt lgkmcnt(0)
	s_nop 0
	v_mfma_f32_16x16x32_bf16 v[126:129], v[140:143], v[184:187], v[126:129]
	v_mfma_f32_16x16x32_bf16 v[122:125], v[148:151], v[184:187], v[122:125]
	v_mfma_f32_16x16x32_bf16 v[110:113], v[140:143], v[192:195], v[110:113]
	v_mfma_f32_16x16x32_bf16 v[106:109], v[148:151], v[192:195], v[106:109]
	v_mfma_f32_16x16x32_bf16 v[94:97], v[140:143], v[212:215], v[94:97]
	v_mfma_f32_16x16x32_bf16 v[90:93], v[148:151], v[212:215], v[90:93]
	v_mfma_f32_16x16x32_bf16 v[78:81], v[140:143], v[220:223], v[78:81]
	v_mfma_f32_16x16x32_bf16 v[74:77], v[148:151], v[220:223], v[74:77]
	v_mfma_f32_16x16x32_bf16 v[126:129], v[144:147], v[188:191], v[126:129]
	v_mfma_f32_16x16x32_bf16 v[122:125], v[152:155], v[188:191], v[122:125]
	v_mfma_f32_16x16x32_bf16 v[110:113], v[144:147], v[196:199], v[110:113]
	v_mfma_f32_16x16x32_bf16 v[106:109], v[152:155], v[196:199], v[106:109]
	v_mfma_f32_16x16x32_bf16 v[94:97], v[144:147], v[216:219], v[94:97]
	v_mfma_f32_16x16x32_bf16 v[90:93], v[152:155], v[216:219], v[90:93]
	v_mfma_f32_16x16x32_bf16 v[78:81], v[144:147], v[224:227], v[78:81]
	v_mfma_f32_16x16x32_bf16 v[74:77], v[152:155], v[224:227], v[74:77]
	s_setprio 0
	s_setprio 1
	v_mfma_f32_16x16x32_bf16 v[118:121], v[156:159], v[184:187], v[118:121]
	v_mfma_f32_16x16x32_bf16 v[114:117], v[168:171], v[184:187], v[114:117]
	v_mfma_f32_16x16x32_bf16 v[102:105], v[156:159], v[192:195], v[102:105]
	v_mfma_f32_16x16x32_bf16 v[98:101], v[168:171], v[192:195], v[98:101]
	v_mfma_f32_16x16x32_bf16 v[86:89], v[156:159], v[212:215], v[86:89]
	v_mfma_f32_16x16x32_bf16 v[82:85], v[168:171], v[212:215], v[82:85]
	v_mfma_f32_16x16x32_bf16 v[70:73], v[156:159], v[220:223], v[70:73]
	v_mfma_f32_16x16x32_bf16 v[66:69], v[168:171], v[220:223], v[66:69]
	v_mfma_f32_16x16x32_bf16 v[118:121], v[160:163], v[188:191], v[118:121]
	v_mfma_f32_16x16x32_bf16 v[114:117], v[172:175], v[188:191], v[114:117]
	v_mfma_f32_16x16x32_bf16 v[102:105], v[160:163], v[196:199], v[102:105]
	v_mfma_f32_16x16x32_bf16 v[98:101], v[172:175], v[196:199], v[98:101]
	v_mfma_f32_16x16x32_bf16 v[86:89], v[160:163], v[216:219], v[86:89]
	v_mfma_f32_16x16x32_bf16 v[82:85], v[172:175], v[216:219], v[82:85]
	v_mfma_f32_16x16x32_bf16 v[70:73], v[160:163], v[224:227], v[70:73]
	s_barrier
	v_mfma_f32_16x16x32_bf16 v[66:69], v[172:175], v[224:227], v[66:69]
	s_setprio 0
	s_mov_b32 m0, s37
	s_add_u32 s40, s30, s33
	ds_read_b128 v[184:187], v182 offset:16384
	ds_read_b128 v[188:191], v182 offset:17408
	ds_read_b128 v[192:195], v182 offset:18432
	ds_read_b128 v[196:199], v182 offset:19456
	ds_read_b128 v[212:215], v182 offset:20480
	ds_read_b128 v[216:219], v182 offset:21504
	ds_read_b128 v[220:223], v182 offset:22528
	ds_read_b128 v[224:227], v182 offset:23552
	global_load_lds_dwordx4 v134, s[30:31]
	s_mov_b32 m0, s60
	s_addc_u32 s41, s31, 0
	global_load_lds_dwordx4 v136, s[30:31]
	s_mov_b32 m0, s67
	s_nop 0
	global_load_lds_dwordx4 v134, s[40:41]
	s_mov_b32 m0, s70
	s_nop 0
	global_load_lds_dwordx4 v136, s[40:41]
	s_mov_b32 m0, s71
	s_nop 0
	global_load_lds_dwordx4 v134, s[34:35]
	s_mov_b32 m0, s72
	s_nop 0
	global_load_lds_dwordx4 v136, s[34:35]
	s_waitcnt vmcnt(8)
	s_waitcnt lgkmcnt(0)
	s_barrier
	s_setprio 1
	s_waitcnt lgkmcnt(0)
	s_nop 0
	v_mfma_f32_16x16x32_bf16 v[62:65], v[140:143], v[184:187], v[62:65]
	v_mfma_f32_16x16x32_bf16 v[58:61], v[148:151], v[184:187], v[58:61]
	v_mfma_f32_16x16x32_bf16 v[46:49], v[140:143], v[192:195], v[46:49]
	v_mfma_f32_16x16x32_bf16 v[42:45], v[148:151], v[192:195], v[42:45]
	v_mfma_f32_16x16x32_bf16 v[30:33], v[140:143], v[212:215], v[30:33]
	v_mfma_f32_16x16x32_bf16 v[26:29], v[148:151], v[212:215], v[26:29]
	v_mfma_f32_16x16x32_bf16 v[14:17], v[140:143], v[220:223], v[14:17]
	v_mfma_f32_16x16x32_bf16 v[10:13], v[148:151], v[220:223], v[10:13]
	v_mfma_f32_16x16x32_bf16 v[62:65], v[144:147], v[188:191], v[62:65]
	v_mfma_f32_16x16x32_bf16 v[58:61], v[152:155], v[188:191], v[58:61]
	v_mfma_f32_16x16x32_bf16 v[46:49], v[144:147], v[196:199], v[46:49]
	v_mfma_f32_16x16x32_bf16 v[42:45], v[152:155], v[196:199], v[42:45]
	v_mfma_f32_16x16x32_bf16 v[30:33], v[144:147], v[216:219], v[30:33]
	v_mfma_f32_16x16x32_bf16 v[26:29], v[152:155], v[216:219], v[26:29]
	v_mfma_f32_16x16x32_bf16 v[14:17], v[144:147], v[224:227], v[14:17]
	v_mfma_f32_16x16x32_bf16 v[10:13], v[152:155], v[224:227], v[10:13]
	s_setprio 0
	s_setprio 1
	v_mfma_f32_16x16x32_bf16 v[54:57], v[156:159], v[184:187], v[54:57]
	v_mfma_f32_16x16x32_bf16 v[50:53], v[168:171], v[184:187], v[50:53]
	v_mfma_f32_16x16x32_bf16 v[38:41], v[156:159], v[192:195], v[38:41]
	v_mfma_f32_16x16x32_bf16 v[34:37], v[168:171], v[192:195], v[34:37]
	v_mfma_f32_16x16x32_bf16 v[22:25], v[156:159], v[212:215], v[22:25]
	v_mfma_f32_16x16x32_bf16 v[18:21], v[168:171], v[212:215], v[18:21]
	v_mfma_f32_16x16x32_bf16 v[6:9], v[156:159], v[220:223], v[6:9]
	v_mfma_f32_16x16x32_bf16 v[2:5], v[168:171], v[220:223], v[2:5]
	v_mfma_f32_16x16x32_bf16 v[54:57], v[160:163], v[188:191], v[54:57]
	v_mfma_f32_16x16x32_bf16 v[50:53], v[172:175], v[188:191], v[50:53]
	v_mfma_f32_16x16x32_bf16 v[38:41], v[160:163], v[196:199], v[38:41]
	v_mfma_f32_16x16x32_bf16 v[34:37], v[172:175], v[196:199], v[34:37]
	v_mfma_f32_16x16x32_bf16 v[22:25], v[160:163], v[216:219], v[22:25]
	v_mfma_f32_16x16x32_bf16 v[18:21], v[172:175], v[216:219], v[18:21]
	v_mfma_f32_16x16x32_bf16 v[6:9], v[160:163], v[224:227], v[6:9]
	s_barrier
	v_mfma_f32_16x16x32_bf16 v[2:5], v[172:175], v[224:227], v[2:5]
	s_setprio 0
	v_add_u32_e32 v0, s77, v180
	ds_read_b128 v[140:143], v0
	ds_read_b128 v[144:147], v0 offset:1024
	ds_read_b128 v[148:151], v0 offset:2048
	ds_read_b128 v[152:155], v0 offset:3072
	v_add_u32_e32 v0, s82, v180
	ds_read_b128 v[156:159], v0
	ds_read_b128 v[160:163], v0 offset:1024
	ds_read_b128 v[168:171], v0 offset:2048
	ds_read_b128 v[172:175], v0 offset:3072
	s_add_u32 s34, s34, s33
	s_addc_u32 s35, s35, 0
	s_mov_b32 m0, s73
	ds_read_b128 v[184:187], v182 offset:32768
	ds_read_b128 v[188:191], v182 offset:33792
	ds_read_b128 v[192:195], v182 offset:34816
	ds_read_b128 v[196:199], v182 offset:35840
	ds_read_b128 v[212:215], v182 offset:36864
	ds_read_b128 v[216:219], v182 offset:37888
	ds_read_b128 v[220:223], v182 offset:38912
	ds_read_b128 v[224:227], v182 offset:39936
	global_load_lds_dwordx4 v134, s[34:35]
	s_mov_b32 m0, s74
	s_nop 0
	global_load_lds_dwordx4 v136, s[34:35]
	s_waitcnt vmcnt(8)
	s_waitcnt lgkmcnt(0)
	s_barrier
	s_setprio 1
	s_waitcnt lgkmcnt(0)
	s_nop 0
	v_mfma_f32_16x16x32_bf16 v[126:129], v[140:143], v[184:187], v[126:129]
	v_mfma_f32_16x16x32_bf16 v[122:125], v[148:151], v[184:187], v[122:125]
	v_mfma_f32_16x16x32_bf16 v[110:113], v[140:143], v[192:195], v[110:113]
	v_mfma_f32_16x16x32_bf16 v[106:109], v[148:151], v[192:195], v[106:109]
	v_mfma_f32_16x16x32_bf16 v[94:97], v[140:143], v[212:215], v[94:97]
	v_mfma_f32_16x16x32_bf16 v[90:93], v[148:151], v[212:215], v[90:93]
	v_mfma_f32_16x16x32_bf16 v[78:81], v[140:143], v[220:223], v[78:81]
	v_mfma_f32_16x16x32_bf16 v[74:77], v[148:151], v[220:223], v[74:77]
	v_mfma_f32_16x16x32_bf16 v[126:129], v[144:147], v[188:191], v[126:129]
	v_mfma_f32_16x16x32_bf16 v[122:125], v[152:155], v[188:191], v[122:125]
	v_mfma_f32_16x16x32_bf16 v[110:113], v[144:147], v[196:199], v[110:113]
	v_mfma_f32_16x16x32_bf16 v[106:109], v[152:155], v[196:199], v[106:109]
	v_mfma_f32_16x16x32_bf16 v[94:97], v[144:147], v[216:219], v[94:97]
	v_mfma_f32_16x16x32_bf16 v[90:93], v[152:155], v[216:219], v[90:93]
	v_mfma_f32_16x16x32_bf16 v[78:81], v[144:147], v[224:227], v[78:81]
	v_mfma_f32_16x16x32_bf16 v[74:77], v[152:155], v[224:227], v[74:77]
	s_setprio 0
	s_setprio 1
	v_mfma_f32_16x16x32_bf16 v[118:121], v[156:159], v[184:187], v[118:121]
	v_mfma_f32_16x16x32_bf16 v[114:117], v[168:171], v[184:187], v[114:117]
	v_mfma_f32_16x16x32_bf16 v[102:105], v[156:159], v[192:195], v[102:105]
	v_mfma_f32_16x16x32_bf16 v[98:101], v[168:171], v[192:195], v[98:101]
	v_mfma_f32_16x16x32_bf16 v[86:89], v[156:159], v[212:215], v[86:89]
	v_mfma_f32_16x16x32_bf16 v[82:85], v[168:171], v[212:215], v[82:85]
	v_mfma_f32_16x16x32_bf16 v[70:73], v[156:159], v[220:223], v[70:73]
	v_mfma_f32_16x16x32_bf16 v[66:69], v[168:171], v[220:223], v[66:69]
	v_mfma_f32_16x16x32_bf16 v[118:121], v[160:163], v[188:191], v[118:121]
	v_mfma_f32_16x16x32_bf16 v[114:117], v[172:175], v[188:191], v[114:117]
	v_mfma_f32_16x16x32_bf16 v[102:105], v[160:163], v[196:199], v[102:105]
	v_mfma_f32_16x16x32_bf16 v[98:101], v[172:175], v[196:199], v[98:101]
	v_mfma_f32_16x16x32_bf16 v[86:89], v[160:163], v[216:219], v[86:89]
	v_mfma_f32_16x16x32_bf16 v[82:85], v[172:175], v[216:219], v[82:85]
	v_mfma_f32_16x16x32_bf16 v[70:73], v[160:163], v[224:227], v[70:73]
	s_barrier
	v_mfma_f32_16x16x32_bf16 v[66:69], v[172:175], v[224:227], v[66:69]
	s_setprio 0
	s_add_u32 s30, s30, s47
	s_addc_u32 s31, s31, 0
	s_mov_b32 m0, s78
	ds_read_b128 v[184:187], v182 offset:49152
	ds_read_b128 v[188:191], v182 offset:50176
	ds_read_b128 v[192:195], v182 offset:51200
	ds_read_b128 v[196:199], v182 offset:52224
	ds_read_b128 v[212:215], v182 offset:53248
	ds_read_b128 v[216:219], v182 offset:54272
	ds_read_b128 v[220:223], v182 offset:55296
	ds_read_b128 v[224:227], v182 offset:56320
	global_load_lds_dwordx4 v134, s[30:31]
	v_lshl_add_u64 v[228:229], s[30:31], 0, v[136:137]
	s_add_u32 s30, s30, s33
	s_mov_b32 m0, s79
	s_addc_u32 s31, s31, 0
	global_load_lds_dwordx4 v[228:229], off
	s_mov_b32 m0, s83
	s_nop 0
	global_load_lds_dwordx4 v134, s[30:31]
	s_mov_b32 m0, s92
	s_nop 0
	global_load_lds_dwordx4 v136, s[30:31]
	s_mov_b32 m0, s80
	s_nop 0
	global_load_lds_dwordx4 v134, s[28:29]
	s_mov_b32 m0, s81
	s_nop 0
	global_load_lds_dwordx4 v136, s[28:29]
	s_waitcnt vmcnt(8)
	s_waitcnt lgkmcnt(0)
	s_barrier
	s_setprio 1
	s_waitcnt lgkmcnt(0)
	s_nop 0
	v_mfma_f32_16x16x32_bf16 v[62:65], v[140:143], v[184:187], v[62:65]
	v_mfma_f32_16x16x32_bf16 v[58:61], v[148:151], v[184:187], v[58:61]
	v_mfma_f32_16x16x32_bf16 v[46:49], v[140:143], v[192:195], v[46:49]
	v_mfma_f32_16x16x32_bf16 v[42:45], v[148:151], v[192:195], v[42:45]
	v_mfma_f32_16x16x32_bf16 v[30:33], v[140:143], v[212:215], v[30:33]
	v_mfma_f32_16x16x32_bf16 v[26:29], v[148:151], v[212:215], v[26:29]
	v_mfma_f32_16x16x32_bf16 v[14:17], v[140:143], v[220:223], v[14:17]
	v_mfma_f32_16x16x32_bf16 v[10:13], v[148:151], v[220:223], v[10:13]
	v_mfma_f32_16x16x32_bf16 v[62:65], v[144:147], v[188:191], v[62:65]
	v_mfma_f32_16x16x32_bf16 v[58:61], v[152:155], v[188:191], v[58:61]
	v_mfma_f32_16x16x32_bf16 v[46:49], v[144:147], v[196:199], v[46:49]
	v_mfma_f32_16x16x32_bf16 v[42:45], v[152:155], v[196:199], v[42:45]
	v_mfma_f32_16x16x32_bf16 v[30:33], v[144:147], v[216:219], v[30:33]
	v_mfma_f32_16x16x32_bf16 v[26:29], v[152:155], v[216:219], v[26:29]
	v_mfma_f32_16x16x32_bf16 v[14:17], v[144:147], v[224:227], v[14:17]
	v_mfma_f32_16x16x32_bf16 v[10:13], v[152:155], v[224:227], v[10:13]
	s_setprio 0
	s_setprio 1
	v_mfma_f32_16x16x32_bf16 v[54:57], v[156:159], v[184:187], v[54:57]
	v_mfma_f32_16x16x32_bf16 v[50:53], v[168:171], v[184:187], v[50:53]
	v_mfma_f32_16x16x32_bf16 v[38:41], v[156:159], v[192:195], v[38:41]
	v_mfma_f32_16x16x32_bf16 v[34:37], v[168:171], v[192:195], v[34:37]
	v_mfma_f32_16x16x32_bf16 v[22:25], v[156:159], v[212:215], v[22:25]
	v_mfma_f32_16x16x32_bf16 v[18:21], v[168:171], v[212:215], v[18:21]
	v_mfma_f32_16x16x32_bf16 v[6:9], v[156:159], v[220:223], v[6:9]
	v_mfma_f32_16x16x32_bf16 v[2:5], v[168:171], v[220:223], v[2:5]
	v_mfma_f32_16x16x32_bf16 v[54:57], v[160:163], v[188:191], v[54:57]
	v_mfma_f32_16x16x32_bf16 v[50:53], v[172:175], v[188:191], v[50:53]
	v_mfma_f32_16x16x32_bf16 v[38:41], v[160:163], v[196:199], v[38:41]
	v_mfma_f32_16x16x32_bf16 v[34:37], v[172:175], v[196:199], v[34:37]
	v_mfma_f32_16x16x32_bf16 v[22:25], v[160:163], v[216:219], v[22:25]
	v_mfma_f32_16x16x32_bf16 v[18:21], v[172:175], v[216:219], v[18:21]
	v_mfma_f32_16x16x32_bf16 v[6:9], v[160:163], v[224:227], v[6:9]
	s_barrier
	v_mfma_f32_16x16x32_bf16 v[2:5], v[172:175], v[224:227], v[2:5]
	s_setprio 0
	s_add_i32 s8, s8, 2
	s_cmp_ge_i32 s8, s75
	s_cbranch_scc0 .LBB0_2148

.LBB0_2381:
	s_add_i32 s8, s52, s66
	s_add_i32 s6, s8, -1
	s_cmp_ge_i32 s6, s67
	s_cselect_b32 s7, s67, 0
	s_sub_i32 s6, s6, s7
	s_ashr_i32 s7, s6, 31
	s_lshl_b64 s[40:41], s[6:7], s21
	s_cmp_ge_i32 s8, s67
	s_cselect_b32 s6, s67, 0
	s_sub_i32 s6, s8, s6
	s_ashr_i32 s7, s6, 31
	v_add_u32_e32 v141, s24, v0
	s_lshl_b64 s[6:7], s[6:7], s21
	ds_read_b128 v[142:145], v141
	ds_read_b128 v[146:149], v141 offset:1024
	ds_read_b128 v[150:153], v141 offset:2048
	ds_read_b128 v[154:157], v141 offset:3072
	v_add_u32_e32 v141, s27, v0
	s_add_u32 s8, s19, s6
	ds_read_b128 v[158:161], v141
	ds_read_b128 v[168:171], v141 offset:1024
	ds_read_b128 v[172:175], v141 offset:2048
	ds_read_b128 v[180:183], v141 offset:3072
	s_addc_u32 s9, s20, s7
	s_add_u32 s6, s22, s6
	s_addc_u32 s7, s23, s7
	s_cmp_eq_u32 s67, s66
	s_cselect_b32 s10, s2, s8
	s_cselect_b32 s11, s3, s9
	s_cselect_b32 s9, s5, s7
	s_cselect_b32 s8, s4, s6
	s_add_u32 s6, s10, s47
	s_addc_u32 s7, s11, 0
	s_add_u32 s40, s64, s40
	s_addc_u32 s41, s65, s41
	s_add_i32 m0, s30, 0xc000
	ds_read_b128 v[184:187], v139
	ds_read_b128 v[188:191], v139 offset:1024
	ds_read_b128 v[192:195], v139 offset:2048
	ds_read_b128 v[196:199], v139 offset:3072
	ds_read_b128 v[212:215], v139 offset:4096
	ds_read_b128 v[216:219], v139 offset:5120
	ds_read_b128 v[220:223], v139 offset:6144
	ds_read_b128 v[224:227], v139 offset:7168
	global_load_lds_dwordx4 v134, s[40:41]
	s_add_i32 m0, s30, 0xe000
	s_nop 0
	global_load_lds_dwordx4 v136, s[40:41]
	s_waitcnt vmcnt(8)
	s_waitcnt lgkmcnt(0)
	s_barrier
	s_setprio 1
	s_waitcnt lgkmcnt(0)
	s_nop 0
	v_mfma_f32_16x16x32_bf16 v[126:129], v[142:145], v[184:187], v[126:129]
	v_mfma_f32_16x16x32_bf16 v[122:125], v[150:153], v[184:187], v[122:125]
	v_mfma_f32_16x16x32_bf16 v[110:113], v[142:145], v[192:195], v[110:113]
	v_mfma_f32_16x16x32_bf16 v[106:109], v[150:153], v[192:195], v[106:109]
	v_mfma_f32_16x16x32_bf16 v[94:97], v[142:145], v[212:215], v[94:97]
	v_mfma_f32_16x16x32_bf16 v[90:93], v[150:153], v[212:215], v[90:93]
	v_mfma_f32_16x16x32_bf16 v[78:81], v[142:145], v[220:223], v[78:81]
	v_mfma_f32_16x16x32_bf16 v[74:77], v[150:153], v[220:223], v[74:77]
	v_mfma_f32_16x16x32_bf16 v[126:129], v[146:149], v[188:191], v[126:129]
	v_mfma_f32_16x16x32_bf16 v[122:125], v[154:157], v[188:191], v[122:125]
	v_mfma_f32_16x16x32_bf16 v[110:113], v[146:149], v[196:199], v[110:113]
	v_mfma_f32_16x16x32_bf16 v[106:109], v[154:157], v[196:199], v[106:109]
	v_mfma_f32_16x16x32_bf16 v[94:97], v[146:149], v[216:219], v[94:97]
	v_mfma_f32_16x16x32_bf16 v[90:93], v[154:157], v[216:219], v[90:93]
	v_mfma_f32_16x16x32_bf16 v[78:81], v[146:149], v[224:227], v[78:81]
	v_mfma_f32_16x16x32_bf16 v[74:77], v[154:157], v[224:227], v[74:77]
	s_setprio 0
	s_setprio 1
	v_mfma_f32_16x16x32_bf16 v[118:121], v[158:161], v[184:187], v[118:121]
	v_mfma_f32_16x16x32_bf16 v[114:117], v[172:175], v[184:187], v[114:117]
	v_mfma_f32_16x16x32_bf16 v[102:105], v[158:161], v[192:195], v[102:105]
	v_mfma_f32_16x16x32_bf16 v[98:101], v[172:175], v[192:195], v[98:101]
	v_mfma_f32_16x16x32_bf16 v[86:89], v[158:161], v[212:215], v[86:89]
	v_mfma_f32_16x16x32_bf16 v[82:85], v[172:175], v[212:215], v[82:85]
	v_mfma_f32_16x16x32_bf16 v[70:73], v[158:161], v[220:223], v[70:73]
	v_mfma_f32_16x16x32_bf16 v[66:69], v[172:175], v[220:223], v[66:69]
	v_mfma_f32_16x16x32_bf16 v[118:121], v[168:171], v[188:191], v[118:121]
	v_mfma_f32_16x16x32_bf16 v[114:117], v[180:183], v[188:191], v[114:117]
	v_mfma_f32_16x16x32_bf16 v[102:105], v[168:171], v[196:199], v[102:105]
	v_mfma_f32_16x16x32_bf16 v[98:101], v[180:183], v[196:199], v[98:101]
	v_mfma_f32_16x16x32_bf16 v[86:89], v[168:171], v[216:219], v[86:89]
	v_mfma_f32_16x16x32_bf16 v[82:85], v[180:183], v[216:219], v[82:85]
	v_mfma_f32_16x16x32_bf16 v[70:73], v[168:171], v[224:227], v[70:73]
	s_barrier
	v_mfma_f32_16x16x32_bf16 v[66:69], v[180:183], v[224:227], v[66:69]
	s_setprio 0
	s_mov_b32 m0, s25
	s_add_u32 s40, s8, s18
	ds_read_b128 v[184:187], v139 offset:16384
	ds_read_b128 v[188:191], v139 offset:17408
	ds_read_b128 v[192:195], v139 offset:18432
	ds_read_b128 v[196:199], v139 offset:19456
	ds_read_b128 v[212:215], v139 offset:20480
	ds_read_b128 v[216:219], v139 offset:21504
	ds_read_b128 v[220:223], v139 offset:22528
	ds_read_b128 v[224:227], v139 offset:23552
	global_load_lds_dwordx4 v134, s[8:9]
	s_mov_b32 m0, s26
	s_addc_u32 s41, s9, s17
	global_load_lds_dwordx4 v136, s[8:9]
	s_mov_b32 m0, s28
	s_nop 0
	global_load_lds_dwordx4 v134, s[40:41]
	s_mov_b32 m0, s29
	s_nop 0
	global_load_lds_dwordx4 v136, s[40:41]
	s_mov_b32 m0, s30
	s_nop 0
	global_load_lds_dwordx4 v134, s[10:11]
	s_mov_b32 m0, s31
	s_nop 0
	global_load_lds_dwordx4 v136, s[10:11]
	s_waitcnt vmcnt(8)
	s_waitcnt lgkmcnt(0)
	s_barrier
	s_setprio 1
	s_waitcnt lgkmcnt(0)
	s_nop 0
	v_mfma_f32_16x16x32_bf16 v[62:65], v[142:145], v[184:187], v[62:65]
	v_mfma_f32_16x16x32_bf16 v[58:61], v[150:153], v[184:187], v[58:61]
	v_mfma_f32_16x16x32_bf16 v[46:49], v[142:145], v[192:195], v[46:49]
	v_mfma_f32_16x16x32_bf16 v[42:45], v[150:153], v[192:195], v[42:45]
	v_mfma_f32_16x16x32_bf16 v[30:33], v[142:145], v[212:215], v[30:33]
	v_mfma_f32_16x16x32_bf16 v[26:29], v[150:153], v[212:215], v[26:29]
	v_mfma_f32_16x16x32_bf16 v[14:17], v[142:145], v[220:223], v[14:17]
	v_mfma_f32_16x16x32_bf16 v[10:13], v[150:153], v[220:223], v[10:13]
	v_mfma_f32_16x16x32_bf16 v[62:65], v[146:149], v[188:191], v[62:65]
	v_mfma_f32_16x16x32_bf16 v[58:61], v[154:157], v[188:191], v[58:61]
	v_mfma_f32_16x16x32_bf16 v[46:49], v[146:149], v[196:199], v[46:49]
	v_mfma_f32_16x16x32_bf16 v[42:45], v[154:157], v[196:199], v[42:45]
	v_mfma_f32_16x16x32_bf16 v[30:33], v[146:149], v[216:219], v[30:33]
	v_mfma_f32_16x16x32_bf16 v[26:29], v[154:157], v[216:219], v[26:29]
	v_mfma_f32_16x16x32_bf16 v[14:17], v[146:149], v[224:227], v[14:17]
	v_mfma_f32_16x16x32_bf16 v[10:13], v[154:157], v[224:227], v[10:13]
	s_setprio 0
	s_setprio 1
	v_mfma_f32_16x16x32_bf16 v[54:57], v[158:161], v[184:187], v[54:57]
	v_mfma_f32_16x16x32_bf16 v[50:53], v[172:175], v[184:187], v[50:53]
	v_mfma_f32_16x16x32_bf16 v[38:41], v[158:161], v[192:195], v[38:41]
	v_mfma_f32_16x16x32_bf16 v[34:37], v[172:175], v[192:195], v[34:37]
	v_mfma_f32_16x16x32_bf16 v[22:25], v[158:161], v[212:215], v[22:25]
	v_mfma_f32_16x16x32_bf16 v[18:21], v[172:175], v[212:215], v[18:21]
	v_mfma_f32_16x16x32_bf16 v[6:9], v[158:161], v[220:223], v[6:9]
	v_mfma_f32_16x16x32_bf16 v[2:5], v[172:175], v[220:223], v[2:5]
	v_mfma_f32_16x16x32_bf16 v[54:57], v[168:171], v[188:191], v[54:57]
	v_mfma_f32_16x16x32_bf16 v[50:53], v[180:183], v[188:191], v[50:53]
	v_mfma_f32_16x16x32_bf16 v[38:41], v[168:171], v[196:199], v[38:41]
	v_mfma_f32_16x16x32_bf16 v[34:37], v[180:183], v[196:199], v[34:37]
	v_mfma_f32_16x16x32_bf16 v[22:25], v[168:171], v[216:219], v[22:25]
	v_mfma_f32_16x16x32_bf16 v[18:21], v[180:183], v[216:219], v[18:21]
	v_mfma_f32_16x16x32_bf16 v[6:9], v[168:171], v[224:227], v[6:9]
	s_barrier
	v_mfma_f32_16x16x32_bf16 v[2:5], v[180:183], v[224:227], v[2:5]
	s_setprio 0
	v_add_u32_e32 v141, s35, v0
	ds_read_b128 v[142:145], v141
	ds_read_b128 v[146:149], v141 offset:1024
	ds_read_b128 v[150:153], v141 offset:2048
	ds_read_b128 v[154:157], v141 offset:3072
	v_add_u32_e32 v141, s51, v0
	ds_read_b128 v[158:161], v141
	ds_read_b128 v[168:171], v141 offset:1024
	ds_read_b128 v[172:175], v141 offset:2048
	ds_read_b128 v[180:183], v141 offset:3072
	s_add_u32 s10, s10, s18
	s_addc_u32 s11, s11, s17
	s_mov_b32 m0, s33
	ds_read_b128 v[184:187], v139 offset:32768
	ds_read_b128 v[188:191], v139 offset:33792
	ds_read_b128 v[192:195], v139 offset:34816
	ds_read_b128 v[196:199], v139 offset:35840
	ds_read_b128 v[212:215], v139 offset:36864
	ds_read_b128 v[216:219], v139 offset:37888
	ds_read_b128 v[220:223], v139 offset:38912
	ds_read_b128 v[224:227], v139 offset:39936
	global_load_lds_dwordx4 v134, s[10:11]
	s_mov_b32 m0, s34
	s_nop 0
	global_load_lds_dwordx4 v136, s[10:11]
	s_waitcnt vmcnt(8)
	s_waitcnt lgkmcnt(0)
	s_barrier
	s_setprio 1
	s_waitcnt lgkmcnt(0)
	s_nop 0
	v_mfma_f32_16x16x32_bf16 v[126:129], v[142:145], v[184:187], v[126:129]
	v_mfma_f32_16x16x32_bf16 v[122:125], v[150:153], v[184:187], v[122:125]
	v_mfma_f32_16x16x32_bf16 v[110:113], v[142:145], v[192:195], v[110:113]
	v_mfma_f32_16x16x32_bf16 v[106:109], v[150:153], v[192:195], v[106:109]
	v_mfma_f32_16x16x32_bf16 v[94:97], v[142:145], v[212:215], v[94:97]
	v_mfma_f32_16x16x32_bf16 v[90:93], v[150:153], v[212:215], v[90:93]
	v_mfma_f32_16x16x32_bf16 v[78:81], v[142:145], v[220:223], v[78:81]
	v_mfma_f32_16x16x32_bf16 v[74:77], v[150:153], v[220:223], v[74:77]
	v_mfma_f32_16x16x32_bf16 v[126:129], v[146:149], v[188:191], v[126:129]
	v_mfma_f32_16x16x32_bf16 v[122:125], v[154:157], v[188:191], v[122:125]
	v_mfma_f32_16x16x32_bf16 v[110:113], v[146:149], v[196:199], v[110:113]
	v_mfma_f32_16x16x32_bf16 v[106:109], v[154:157], v[196:199], v[106:109]
	v_mfma_f32_16x16x32_bf16 v[94:97], v[146:149], v[216:219], v[94:97]
	v_mfma_f32_16x16x32_bf16 v[90:93], v[154:157], v[216:219], v[90:93]
	v_mfma_f32_16x16x32_bf16 v[78:81], v[146:149], v[224:227], v[78:81]
	v_mfma_f32_16x16x32_bf16 v[74:77], v[154:157], v[224:227], v[74:77]
	s_setprio 0
	s_setprio 1
	v_mfma_f32_16x16x32_bf16 v[118:121], v[158:161], v[184:187], v[118:121]
	v_mfma_f32_16x16x32_bf16 v[114:117], v[172:175], v[184:187], v[114:117]
	v_mfma_f32_16x16x32_bf16 v[102:105], v[158:161], v[192:195], v[102:105]
	v_mfma_f32_16x16x32_bf16 v[98:101], v[172:175], v[192:195], v[98:101]
	v_mfma_f32_16x16x32_bf16 v[86:89], v[158:161], v[212:215], v[86:89]
	v_mfma_f32_16x16x32_bf16 v[82:85], v[172:175], v[212:215], v[82:85]
	v_mfma_f32_16x16x32_bf16 v[70:73], v[158:161], v[220:223], v[70:73]
	v_mfma_f32_16x16x32_bf16 v[66:69], v[172:175], v[220:223], v[66:69]
	v_mfma_f32_16x16x32_bf16 v[118:121], v[168:171], v[188:191], v[118:121]
	v_mfma_f32_16x16x32_bf16 v[114:117], v[180:183], v[188:191], v[114:117]
	v_mfma_f32_16x16x32_bf16 v[102:105], v[168:171], v[196:199], v[102:105]
	v_mfma_f32_16x16x32_bf16 v[98:101], v[180:183], v[196:199], v[98:101]
	v_mfma_f32_16x16x32_bf16 v[86:89], v[168:171], v[216:219], v[86:89]
	v_mfma_f32_16x16x32_bf16 v[82:85], v[180:183], v[216:219], v[82:85]
	v_mfma_f32_16x16x32_bf16 v[70:73], v[168:171], v[224:227], v[70:73]
	s_barrier
	v_mfma_f32_16x16x32_bf16 v[66:69], v[180:183], v[224:227], v[66:69]
	s_setprio 0
	s_add_u32 s8, s8, s47
	s_addc_u32 s9, s9, 0
	s_mov_b32 m0, s36
	ds_read_b128 v[184:187], v139 offset:49152
	ds_read_b128 v[188:191], v139 offset:50176
	ds_read_b128 v[192:195], v139 offset:51200
	ds_read_b128 v[196:199], v139 offset:52224
	ds_read_b128 v[212:215], v139 offset:53248
	ds_read_b128 v[216:219], v139 offset:54272
	ds_read_b128 v[220:223], v139 offset:55296
	ds_read_b128 v[224:227], v139 offset:56320
	global_load_lds_dwordx4 v134, s[8:9]
	v_lshl_add_u64 v[162:163], s[8:9], 0, v[136:137]
	s_add_u32 s8, s8, s18
	s_mov_b32 m0, s37
	s_addc_u32 s9, s9, s17
	global_load_lds_dwordx4 v[162:163], off
	s_mov_b32 m0, s55
	s_nop 0
	global_load_lds_dwordx4 v134, s[8:9]
	s_mov_b32 m0, s60
	s_nop 0
	global_load_lds_dwordx4 v136, s[8:9]
	s_mov_b32 m0, s48
	s_nop 0
	global_load_lds_dwordx4 v134, s[6:7]
	s_mov_b32 m0, s50
	s_nop 0
	global_load_lds_dwordx4 v136, s[6:7]
	s_waitcnt vmcnt(8)
	s_waitcnt lgkmcnt(0)
	s_barrier
	s_setprio 1
	s_waitcnt lgkmcnt(0)
	s_nop 0
	v_mfma_f32_16x16x32_bf16 v[62:65], v[142:145], v[184:187], v[62:65]
	v_mfma_f32_16x16x32_bf16 v[58:61], v[150:153], v[184:187], v[58:61]
	v_mfma_f32_16x16x32_bf16 v[46:49], v[142:145], v[192:195], v[46:49]
	v_mfma_f32_16x16x32_bf16 v[42:45], v[150:153], v[192:195], v[42:45]
	v_mfma_f32_16x16x32_bf16 v[30:33], v[142:145], v[212:215], v[30:33]
	v_mfma_f32_16x16x32_bf16 v[26:29], v[150:153], v[212:215], v[26:29]
	v_mfma_f32_16x16x32_bf16 v[14:17], v[142:145], v[220:223], v[14:17]
	v_mfma_f32_16x16x32_bf16 v[10:13], v[150:153], v[220:223], v[10:13]
	v_mfma_f32_16x16x32_bf16 v[62:65], v[146:149], v[188:191], v[62:65]
	v_mfma_f32_16x16x32_bf16 v[58:61], v[154:157], v[188:191], v[58:61]
	v_mfma_f32_16x16x32_bf16 v[46:49], v[146:149], v[196:199], v[46:49]
	v_mfma_f32_16x16x32_bf16 v[42:45], v[154:157], v[196:199], v[42:45]
	v_mfma_f32_16x16x32_bf16 v[30:33], v[146:149], v[216:219], v[30:33]
	v_mfma_f32_16x16x32_bf16 v[26:29], v[154:157], v[216:219], v[26:29]
	v_mfma_f32_16x16x32_bf16 v[14:17], v[146:149], v[224:227], v[14:17]
	v_mfma_f32_16x16x32_bf16 v[10:13], v[154:157], v[224:227], v[10:13]
	s_setprio 0
	s_setprio 1
	v_mfma_f32_16x16x32_bf16 v[54:57], v[158:161], v[184:187], v[54:57]
	v_mfma_f32_16x16x32_bf16 v[50:53], v[172:175], v[184:187], v[50:53]
	v_mfma_f32_16x16x32_bf16 v[38:41], v[158:161], v[192:195], v[38:41]
	v_mfma_f32_16x16x32_bf16 v[34:37], v[172:175], v[192:195], v[34:37]
	v_mfma_f32_16x16x32_bf16 v[22:25], v[158:161], v[212:215], v[22:25]
	v_mfma_f32_16x16x32_bf16 v[18:21], v[172:175], v[212:215], v[18:21]
	v_mfma_f32_16x16x32_bf16 v[6:9], v[158:161], v[220:223], v[6:9]
	v_mfma_f32_16x16x32_bf16 v[2:5], v[172:175], v[220:223], v[2:5]
	v_mfma_f32_16x16x32_bf16 v[54:57], v[168:171], v[188:191], v[54:57]
	v_mfma_f32_16x16x32_bf16 v[50:53], v[180:183], v[188:191], v[50:53]
	v_mfma_f32_16x16x32_bf16 v[38:41], v[168:171], v[196:199], v[38:41]
	v_mfma_f32_16x16x32_bf16 v[34:37], v[180:183], v[196:199], v[34:37]
	v_mfma_f32_16x16x32_bf16 v[22:25], v[168:171], v[216:219], v[22:25]
	v_mfma_f32_16x16x32_bf16 v[18:21], v[180:183], v[216:219], v[18:21]
	v_mfma_f32_16x16x32_bf16 v[6:9], v[168:171], v[224:227], v[6:9]
	s_barrier
	v_mfma_f32_16x16x32_bf16 v[2:5], v[180:183], v[224:227], v[2:5]
	s_setprio 0
	s_add_i32 s6, s66, 2
	s_cmp_ge_i32 s66, s67
	s_mov_b32 s66, s6
	s_cbranch_scc0 .LBB0_2381

.LBB0_2391:
	s_add_i32 s8, s52, s60
	s_add_i32 s6, s8, -1
	s_cmp_ge_i32 s6, s64
	s_cselect_b32 s7, s64, 0
	s_sub_i32 s6, s6, s7
	s_ashr_i32 s7, s6, 31
	s_lshl_b64 s[40:41], s[6:7], s19
	s_cmp_ge_i32 s8, s64
	s_cselect_b32 s6, s64, 0
	s_sub_i32 s6, s8, s6
	s_ashr_i32 s7, s6, 31
	s_lshl_b64 s[6:7], s[6:7], s19
	v_add_u32_e32 v152, s22, v138
	v_add_u32_e32 v165, s25, v138
	s_add_u32 s8, s17, s6
	ds_read_b128 v[140:143], v152
	ds_read_b128 v[144:147], v152 offset:1024
	ds_read_b128 v[148:151], v152 offset:2048
	ds_read_b128 v[152:155], v152 offset:3072
	ds_read_b128 v[156:159], v165
	ds_read_b128 v[160:163], v165 offset:1024
	ds_read_b128 v[168:171], v165 offset:2048
	ds_read_b128 v[172:175], v165 offset:3072
	s_addc_u32 s9, s18, s7
	s_add_u32 s6, s20, s6
	s_addc_u32 s7, s21, s7
	s_cmp_eq_u32 s64, s60
	s_cselect_b32 s10, s2, s8
	s_cselect_b32 s11, s3, s9
	s_cselect_b32 s9, s5, s7
	s_cselect_b32 s8, s4, s6
	s_add_u32 s6, s10, s47
	s_addc_u32 s7, s11, 0
	s_add_u32 s40, s51, s40
	s_addc_u32 s41, s55, s41
	s_add_i32 m0, s28, 0xc000
	ds_read_b128 v[180:183], v139
	ds_read_b128 v[184:187], v139 offset:1024
	ds_read_b128 v[188:191], v139 offset:2048
	ds_read_b128 v[192:195], v139 offset:3072
	ds_read_b128 v[196:199], v139 offset:4096
	ds_read_b128 v[212:215], v139 offset:5120
	ds_read_b128 v[216:219], v139 offset:6144
	ds_read_b128 v[220:223], v139 offset:7168
	global_load_lds_dwordx4 v134, s[40:41]
	s_add_i32 m0, s28, 0xe000
	s_nop 0
	global_load_lds_dwordx4 v136, s[40:41]
	s_waitcnt vmcnt(8)
	s_waitcnt lgkmcnt(0)
	s_barrier
	s_setprio 1
	s_waitcnt lgkmcnt(0)
	s_nop 0
	v_mfma_f32_16x16x32_bf16 v[126:129], v[140:143], v[180:183], v[126:129]
	v_mfma_f32_16x16x32_bf16 v[122:125], v[148:151], v[180:183], v[122:125]
	v_mfma_f32_16x16x32_bf16 v[110:113], v[140:143], v[188:191], v[110:113]
	v_mfma_f32_16x16x32_bf16 v[106:109], v[148:151], v[188:191], v[106:109]
	v_mfma_f32_16x16x32_bf16 v[94:97], v[140:143], v[196:199], v[94:97]
	v_mfma_f32_16x16x32_bf16 v[90:93], v[148:151], v[196:199], v[90:93]
	v_mfma_f32_16x16x32_bf16 v[78:81], v[140:143], v[216:219], v[78:81]
	v_mfma_f32_16x16x32_bf16 v[74:77], v[148:151], v[216:219], v[74:77]
	v_mfma_f32_16x16x32_bf16 v[126:129], v[144:147], v[184:187], v[126:129]
	v_mfma_f32_16x16x32_bf16 v[122:125], v[152:155], v[184:187], v[122:125]
	v_mfma_f32_16x16x32_bf16 v[110:113], v[144:147], v[192:195], v[110:113]
	v_mfma_f32_16x16x32_bf16 v[106:109], v[152:155], v[192:195], v[106:109]
	v_mfma_f32_16x16x32_bf16 v[94:97], v[144:147], v[212:215], v[94:97]
	v_mfma_f32_16x16x32_bf16 v[90:93], v[152:155], v[212:215], v[90:93]
	v_mfma_f32_16x16x32_bf16 v[78:81], v[144:147], v[220:223], v[78:81]
	v_mfma_f32_16x16x32_bf16 v[74:77], v[152:155], v[220:223], v[74:77]
	s_setprio 0
	s_setprio 1
	v_mfma_f32_16x16x32_bf16 v[118:121], v[156:159], v[180:183], v[118:121]
	v_mfma_f32_16x16x32_bf16 v[114:117], v[168:171], v[180:183], v[114:117]
	v_mfma_f32_16x16x32_bf16 v[102:105], v[156:159], v[188:191], v[102:105]
	v_mfma_f32_16x16x32_bf16 v[98:101], v[168:171], v[188:191], v[98:101]
	v_mfma_f32_16x16x32_bf16 v[86:89], v[156:159], v[196:199], v[86:89]
	v_mfma_f32_16x16x32_bf16 v[82:85], v[168:171], v[196:199], v[82:85]
	v_mfma_f32_16x16x32_bf16 v[70:73], v[156:159], v[216:219], v[70:73]
	v_mfma_f32_16x16x32_bf16 v[66:69], v[168:171], v[216:219], v[66:69]
	v_mfma_f32_16x16x32_bf16 v[118:121], v[160:163], v[184:187], v[118:121]
	v_mfma_f32_16x16x32_bf16 v[114:117], v[172:175], v[184:187], v[114:117]
	v_mfma_f32_16x16x32_bf16 v[102:105], v[160:163], v[192:195], v[102:105]
	v_mfma_f32_16x16x32_bf16 v[98:101], v[172:175], v[192:195], v[98:101]
	v_mfma_f32_16x16x32_bf16 v[86:89], v[160:163], v[212:215], v[86:89]
	v_mfma_f32_16x16x32_bf16 v[82:85], v[172:175], v[212:215], v[82:85]
	v_mfma_f32_16x16x32_bf16 v[70:73], v[160:163], v[220:223], v[70:73]
	s_barrier
	v_mfma_f32_16x16x32_bf16 v[66:69], v[172:175], v[220:223], v[66:69]
	s_setprio 0
	s_mov_b32 m0, s23
	s_add_u32 s40, s8, s16
	ds_read_b128 v[180:183], v139 offset:16384
	ds_read_b128 v[184:187], v139 offset:17408
	ds_read_b128 v[188:191], v139 offset:18432
	ds_read_b128 v[192:195], v139 offset:19456
	ds_read_b128 v[196:199], v139 offset:20480
	ds_read_b128 v[212:215], v139 offset:21504
	ds_read_b128 v[216:219], v139 offset:22528
	ds_read_b128 v[220:223], v139 offset:23552
	global_load_lds_dwordx4 v134, s[8:9]
	s_mov_b32 m0, s24
	s_addc_u32 s41, s9, s15
	global_load_lds_dwordx4 v136, s[8:9]
	s_mov_b32 m0, s26
	s_nop 0
	global_load_lds_dwordx4 v134, s[40:41]
	s_mov_b32 m0, s27
	s_nop 0
	global_load_lds_dwordx4 v136, s[40:41]
	s_mov_b32 m0, s28
	s_nop 0
	global_load_lds_dwordx4 v134, s[10:11]
	s_mov_b32 m0, s29
	s_nop 0
	global_load_lds_dwordx4 v136, s[10:11]
	s_waitcnt vmcnt(8)
	s_waitcnt lgkmcnt(0)
	s_barrier
	s_setprio 1
	s_waitcnt lgkmcnt(0)
	s_nop 0
	v_mfma_f32_16x16x32_bf16 v[62:65], v[140:143], v[180:183], v[62:65]
	v_mfma_f32_16x16x32_bf16 v[58:61], v[148:151], v[180:183], v[58:61]
	v_mfma_f32_16x16x32_bf16 v[46:49], v[140:143], v[188:191], v[46:49]
	v_mfma_f32_16x16x32_bf16 v[42:45], v[148:151], v[188:191], v[42:45]
	v_mfma_f32_16x16x32_bf16 v[30:33], v[140:143], v[196:199], v[30:33]
	v_mfma_f32_16x16x32_bf16 v[26:29], v[148:151], v[196:199], v[26:29]
	v_mfma_f32_16x16x32_bf16 v[14:17], v[140:143], v[216:219], v[14:17]
	v_mfma_f32_16x16x32_bf16 v[10:13], v[148:151], v[216:219], v[10:13]
	v_mfma_f32_16x16x32_bf16 v[62:65], v[144:147], v[184:187], v[62:65]
	v_mfma_f32_16x16x32_bf16 v[58:61], v[152:155], v[184:187], v[58:61]
	v_mfma_f32_16x16x32_bf16 v[46:49], v[144:147], v[192:195], v[46:49]
	v_mfma_f32_16x16x32_bf16 v[42:45], v[152:155], v[192:195], v[42:45]
	v_mfma_f32_16x16x32_bf16 v[30:33], v[144:147], v[212:215], v[30:33]
	v_mfma_f32_16x16x32_bf16 v[26:29], v[152:155], v[212:215], v[26:29]
	v_mfma_f32_16x16x32_bf16 v[14:17], v[144:147], v[220:223], v[14:17]
	v_mfma_f32_16x16x32_bf16 v[10:13], v[152:155], v[220:223], v[10:13]
	s_setprio 0
	s_setprio 1
	v_mfma_f32_16x16x32_bf16 v[54:57], v[156:159], v[180:183], v[54:57]
	v_mfma_f32_16x16x32_bf16 v[50:53], v[168:171], v[180:183], v[50:53]
	v_mfma_f32_16x16x32_bf16 v[38:41], v[156:159], v[188:191], v[38:41]
	v_mfma_f32_16x16x32_bf16 v[34:37], v[168:171], v[188:191], v[34:37]
	v_mfma_f32_16x16x32_bf16 v[22:25], v[156:159], v[196:199], v[22:25]
	v_mfma_f32_16x16x32_bf16 v[18:21], v[168:171], v[196:199], v[18:21]
	v_mfma_f32_16x16x32_bf16 v[6:9], v[156:159], v[216:219], v[6:9]
	v_mfma_f32_16x16x32_bf16 v[2:5], v[168:171], v[216:219], v[2:5]
	v_mfma_f32_16x16x32_bf16 v[54:57], v[160:163], v[184:187], v[54:57]
	v_mfma_f32_16x16x32_bf16 v[50:53], v[172:175], v[184:187], v[50:53]
	v_mfma_f32_16x16x32_bf16 v[38:41], v[160:163], v[192:195], v[38:41]
	v_mfma_f32_16x16x32_bf16 v[34:37], v[172:175], v[192:195], v[34:37]
	v_mfma_f32_16x16x32_bf16 v[22:25], v[160:163], v[212:215], v[22:25]
	v_mfma_f32_16x16x32_bf16 v[18:21], v[172:175], v[212:215], v[18:21]
	v_mfma_f32_16x16x32_bf16 v[6:9], v[160:163], v[220:223], v[6:9]
	s_barrier
	v_mfma_f32_16x16x32_bf16 v[2:5], v[172:175], v[220:223], v[2:5]
	s_setprio 0
	v_add_u32_e32 v152, s33, v138
	v_add_u32_e32 v165, s38, v138
	ds_read_b128 v[140:143], v152
	ds_read_b128 v[144:147], v152 offset:1024
	ds_read_b128 v[148:151], v152 offset:2048
	ds_read_b128 v[152:155], v152 offset:3072
	ds_read_b128 v[156:159], v165
	ds_read_b128 v[160:163], v165 offset:1024
	ds_read_b128 v[168:171], v165 offset:2048
	ds_read_b128 v[172:175], v165 offset:3072
	s_add_u32 s10, s10, s16
	s_addc_u32 s11, s11, s15
	s_mov_b32 m0, s30
	ds_read_b128 v[180:183], v139 offset:32768
	ds_read_b128 v[184:187], v139 offset:33792
	ds_read_b128 v[188:191], v139 offset:34816
	ds_read_b128 v[192:195], v139 offset:35840
	ds_read_b128 v[196:199], v139 offset:36864
	ds_read_b128 v[212:215], v139 offset:37888
	ds_read_b128 v[216:219], v139 offset:38912
	ds_read_b128 v[220:223], v139 offset:39936
	global_load_lds_dwordx4 v134, s[10:11]
	s_mov_b32 m0, s31
	s_nop 0
	global_load_lds_dwordx4 v136, s[10:11]
	s_waitcnt vmcnt(8)
	s_waitcnt lgkmcnt(0)
	s_barrier
	s_setprio 1
	s_waitcnt lgkmcnt(0)
	s_nop 0
	v_mfma_f32_16x16x32_bf16 v[126:129], v[140:143], v[180:183], v[126:129]
	v_mfma_f32_16x16x32_bf16 v[122:125], v[148:151], v[180:183], v[122:125]
	v_mfma_f32_16x16x32_bf16 v[110:113], v[140:143], v[188:191], v[110:113]
	v_mfma_f32_16x16x32_bf16 v[106:109], v[148:151], v[188:191], v[106:109]
	v_mfma_f32_16x16x32_bf16 v[94:97], v[140:143], v[196:199], v[94:97]
	v_mfma_f32_16x16x32_bf16 v[90:93], v[148:151], v[196:199], v[90:93]
	v_mfma_f32_16x16x32_bf16 v[78:81], v[140:143], v[216:219], v[78:81]
	v_mfma_f32_16x16x32_bf16 v[74:77], v[148:151], v[216:219], v[74:77]
	v_mfma_f32_16x16x32_bf16 v[126:129], v[144:147], v[184:187], v[126:129]
	v_mfma_f32_16x16x32_bf16 v[122:125], v[152:155], v[184:187], v[122:125]
	v_mfma_f32_16x16x32_bf16 v[110:113], v[144:147], v[192:195], v[110:113]
	v_mfma_f32_16x16x32_bf16 v[106:109], v[152:155], v[192:195], v[106:109]
	v_mfma_f32_16x16x32_bf16 v[94:97], v[144:147], v[212:215], v[94:97]
	v_mfma_f32_16x16x32_bf16 v[90:93], v[152:155], v[212:215], v[90:93]
	v_mfma_f32_16x16x32_bf16 v[78:81], v[144:147], v[220:223], v[78:81]
	v_mfma_f32_16x16x32_bf16 v[74:77], v[152:155], v[220:223], v[74:77]
	s_setprio 0
	s_setprio 1
	v_mfma_f32_16x16x32_bf16 v[118:121], v[156:159], v[180:183], v[118:121]
	v_mfma_f32_16x16x32_bf16 v[114:117], v[168:171], v[180:183], v[114:117]
	v_mfma_f32_16x16x32_bf16 v[102:105], v[156:159], v[188:191], v[102:105]
	v_mfma_f32_16x16x32_bf16 v[98:101], v[168:171], v[188:191], v[98:101]
	v_mfma_f32_16x16x32_bf16 v[86:89], v[156:159], v[196:199], v[86:89]
	v_mfma_f32_16x16x32_bf16 v[82:85], v[168:171], v[196:199], v[82:85]
	v_mfma_f32_16x16x32_bf16 v[70:73], v[156:159], v[216:219], v[70:73]
	v_mfma_f32_16x16x32_bf16 v[66:69], v[168:171], v[216:219], v[66:69]
	v_mfma_f32_16x16x32_bf16 v[118:121], v[160:163], v[184:187], v[118:121]
	v_mfma_f32_16x16x32_bf16 v[114:117], v[172:175], v[184:187], v[114:117]
	v_mfma_f32_16x16x32_bf16 v[102:105], v[160:163], v[192:195], v[102:105]
	v_mfma_f32_16x16x32_bf16 v[98:101], v[172:175], v[192:195], v[98:101]
	v_mfma_f32_16x16x32_bf16 v[86:89], v[160:163], v[212:215], v[86:89]
	v_mfma_f32_16x16x32_bf16 v[82:85], v[172:175], v[212:215], v[82:85]
	v_mfma_f32_16x16x32_bf16 v[70:73], v[160:163], v[220:223], v[70:73]
	s_barrier
	v_mfma_f32_16x16x32_bf16 v[66:69], v[172:175], v[220:223], v[66:69]
	s_setprio 0
	s_add_u32 s8, s8, s47
	s_addc_u32 s9, s9, 0
	s_mov_b32 m0, s34
	ds_read_b128 v[180:183], v139 offset:49152
	ds_read_b128 v[184:187], v139 offset:50176
	ds_read_b128 v[188:191], v139 offset:51200
	ds_read_b128 v[192:195], v139 offset:52224
	ds_read_b128 v[196:199], v139 offset:53248
	ds_read_b128 v[212:215], v139 offset:54272
	ds_read_b128 v[216:219], v139 offset:55296
	ds_read_b128 v[220:223], v139 offset:56320
	global_load_lds_dwordx4 v134, s[8:9]
	v_lshl_add_u64 v[224:225], s[8:9], 0, v[136:137]
	s_add_u32 s8, s8, s16
	s_mov_b32 m0, s35
	s_addc_u32 s9, s9, s15
	global_load_lds_dwordx4 v[224:225], off
	s_mov_b32 m0, s48
	s_nop 0
	global_load_lds_dwordx4 v134, s[8:9]
	s_mov_b32 m0, s50
	s_nop 0
	global_load_lds_dwordx4 v136, s[8:9]
	s_mov_b32 m0, s36
	s_nop 0
	global_load_lds_dwordx4 v134, s[6:7]
	s_mov_b32 m0, s37
	s_nop 0
	global_load_lds_dwordx4 v136, s[6:7]
	s_waitcnt vmcnt(8)
	s_waitcnt lgkmcnt(0)
	s_barrier
	s_setprio 1
	s_waitcnt lgkmcnt(0)
	s_nop 0
	v_mfma_f32_16x16x32_bf16 v[62:65], v[140:143], v[180:183], v[62:65]
	v_mfma_f32_16x16x32_bf16 v[58:61], v[148:151], v[180:183], v[58:61]
	v_mfma_f32_16x16x32_bf16 v[46:49], v[140:143], v[188:191], v[46:49]
	v_mfma_f32_16x16x32_bf16 v[42:45], v[148:151], v[188:191], v[42:45]
	v_mfma_f32_16x16x32_bf16 v[30:33], v[140:143], v[196:199], v[30:33]
	v_mfma_f32_16x16x32_bf16 v[26:29], v[148:151], v[196:199], v[26:29]
	v_mfma_f32_16x16x32_bf16 v[14:17], v[140:143], v[216:219], v[14:17]
	v_mfma_f32_16x16x32_bf16 v[10:13], v[148:151], v[216:219], v[10:13]
	v_mfma_f32_16x16x32_bf16 v[62:65], v[144:147], v[184:187], v[62:65]
	v_mfma_f32_16x16x32_bf16 v[58:61], v[152:155], v[184:187], v[58:61]
	v_mfma_f32_16x16x32_bf16 v[46:49], v[144:147], v[192:195], v[46:49]
	v_mfma_f32_16x16x32_bf16 v[42:45], v[152:155], v[192:195], v[42:45]
	v_mfma_f32_16x16x32_bf16 v[30:33], v[144:147], v[212:215], v[30:33]
	v_mfma_f32_16x16x32_bf16 v[26:29], v[152:155], v[212:215], v[26:29]
	v_mfma_f32_16x16x32_bf16 v[14:17], v[144:147], v[220:223], v[14:17]
	v_mfma_f32_16x16x32_bf16 v[10:13], v[152:155], v[220:223], v[10:13]
	s_setprio 0
	s_setprio 1
	v_mfma_f32_16x16x32_bf16 v[54:57], v[156:159], v[180:183], v[54:57]
	v_mfma_f32_16x16x32_bf16 v[50:53], v[168:171], v[180:183], v[50:53]
	v_mfma_f32_16x16x32_bf16 v[38:41], v[156:159], v[188:191], v[38:41]
	v_mfma_f32_16x16x32_bf16 v[34:37], v[168:171], v[188:191], v[34:37]
	v_mfma_f32_16x16x32_bf16 v[22:25], v[156:159], v[196:199], v[22:25]
	v_mfma_f32_16x16x32_bf16 v[18:21], v[168:171], v[196:199], v[18:21]
	v_mfma_f32_16x16x32_bf16 v[6:9], v[156:159], v[216:219], v[6:9]
	v_mfma_f32_16x16x32_bf16 v[2:5], v[168:171], v[216:219], v[2:5]
	v_mfma_f32_16x16x32_bf16 v[54:57], v[160:163], v[184:187], v[54:57]
	v_mfma_f32_16x16x32_bf16 v[50:53], v[172:175], v[184:187], v[50:53]
	v_mfma_f32_16x16x32_bf16 v[38:41], v[160:163], v[192:195], v[38:41]
	v_mfma_f32_16x16x32_bf16 v[34:37], v[172:175], v[192:195], v[34:37]
	v_mfma_f32_16x16x32_bf16 v[22:25], v[160:163], v[212:215], v[22:25]
	v_mfma_f32_16x16x32_bf16 v[18:21], v[172:175], v[212:215], v[18:21]
	v_mfma_f32_16x16x32_bf16 v[6:9], v[160:163], v[220:223], v[6:9]
	s_barrier
	v_mfma_f32_16x16x32_bf16 v[2:5], v[172:175], v[220:223], v[2:5]
	s_setprio 0
	s_add_i32 s6, s60, 2
	s_cmp_ge_i32 s60, s64
	s_mov_b32 s60, s6
	s_cbranch_scc0 .LBB0_2391

.LBB0_2802:
	s_add_i32 s28, s4, s75
	s_add_i32 s26, s28, 1
	s_cmp_ge_i32 s26, s51
	s_cselect_b32 s27, s51, 0
	s_sub_i32 s26, s26, s27
	s_ashr_i32 s27, s26, 31
	s_lshl_b64 s[76:77], s[26:27], s39
	s_add_i32 s28, s28, 2
	s_cmp_ge_i32 s28, s51
	s_cselect_b32 s26, s51, 0
	s_sub_i32 s26, s28, s26
	s_ashr_i32 s27, s26, 31
	v_add_u32_e32 v136, s5, v141
	s_lshl_b64 s[26:27], s[26:27], s39
	ds_read_b128 v[146:149], v136
	ds_read_b128 v[150:153], v136 offset:1024
	ds_read_b128 v[154:157], v136 offset:2048
	ds_read_b128 v[158:161], v136 offset:3072
	v_add_u32_e32 v136, s43, v141
	s_add_u32 s28, s22, s26
	ds_read_b128 v[172:175], v136
	ds_read_b128 v[176:179], v136 offset:1024
	ds_read_b128 v[180:183], v136 offset:2048
	ds_read_b128 v[184:187], v136 offset:3072
	s_addc_u32 s29, s23, s27
	s_add_u32 s26, s24, s26
	s_addc_u32 s27, s25, s27
	s_cmp_eq_u32 s52, s75
	s_cselect_b32 s30, s71, s28
	s_cselect_b32 s31, s72, s29
	s_cselect_b32 s29, s74, s27
	s_cselect_b32 s28, s73, s26
	s_add_u32 s26, s30, s53
	s_addc_u32 s27, s31, 0
	s_add_u32 s76, s69, s76
	s_addc_u32 s77, s70, s77
	s_add_i32 m0, s46, 0xc000
	ds_read_b128 v[188:191], v145
	ds_read_b128 v[192:195], v145 offset:1024
	ds_read_b128 v[196:199], v145 offset:2048
	ds_read_b128 v[212:215], v145 offset:3072
	ds_read_b128 v[216:219], v145 offset:4096
	ds_read_b128 v[220:223], v145 offset:5120
	ds_read_b128 v[224:227], v145 offset:6144
	ds_read_b128 v[228:231], v145 offset:7168
	global_load_lds_dwordx4 v134, s[76:77]
	s_add_i32 m0, s46, 0xe000
	s_nop 0
	global_load_lds_dwordx4 v132, s[76:77]
	s_waitcnt vmcnt(8)
	s_waitcnt lgkmcnt(0)
	s_barrier
	s_setprio 1
	s_waitcnt lgkmcnt(0)
	s_nop 0
	v_mfma_f32_16x16x32_bf16 v[122:125], v[146:149], v[188:191], v[122:125]
	v_mfma_f32_16x16x32_bf16 v[114:117], v[154:157], v[188:191], v[114:117]
	v_mfma_f32_16x16x32_bf16 v[106:109], v[146:149], v[196:199], v[106:109]
	v_mfma_f32_16x16x32_bf16 v[98:101], v[154:157], v[196:199], v[98:101]
	v_mfma_f32_16x16x32_bf16 v[90:93], v[146:149], v[216:219], v[90:93]
	v_mfma_f32_16x16x32_bf16 v[82:85], v[154:157], v[216:219], v[82:85]
	v_mfma_f32_16x16x32_bf16 v[74:77], v[146:149], v[224:227], v[74:77]
	v_mfma_f32_16x16x32_bf16 v[66:69], v[154:157], v[224:227], v[66:69]
	v_mfma_f32_16x16x32_bf16 v[122:125], v[150:153], v[192:195], v[122:125]
	v_mfma_f32_16x16x32_bf16 v[114:117], v[158:161], v[192:195], v[114:117]
	v_mfma_f32_16x16x32_bf16 v[106:109], v[150:153], v[212:215], v[106:109]
	v_mfma_f32_16x16x32_bf16 v[98:101], v[158:161], v[212:215], v[98:101]
	v_mfma_f32_16x16x32_bf16 v[90:93], v[150:153], v[220:223], v[90:93]
	v_mfma_f32_16x16x32_bf16 v[82:85], v[158:161], v[220:223], v[82:85]
	v_mfma_f32_16x16x32_bf16 v[74:77], v[150:153], v[228:231], v[74:77]
	v_mfma_f32_16x16x32_bf16 v[66:69], v[158:161], v[228:231], v[66:69]
	s_setprio 0
	s_setprio 1
	v_mfma_f32_16x16x32_bf16 v[126:129], v[172:175], v[188:191], v[126:129]
	v_mfma_f32_16x16x32_bf16 v[118:121], v[180:183], v[188:191], v[118:121]
	v_mfma_f32_16x16x32_bf16 v[110:113], v[172:175], v[196:199], v[110:113]
	v_mfma_f32_16x16x32_bf16 v[102:105], v[180:183], v[196:199], v[102:105]
	v_mfma_f32_16x16x32_bf16 v[94:97], v[172:175], v[216:219], v[94:97]
	v_mfma_f32_16x16x32_bf16 v[86:89], v[180:183], v[216:219], v[86:89]
	v_mfma_f32_16x16x32_bf16 v[78:81], v[172:175], v[224:227], v[78:81]
	v_mfma_f32_16x16x32_bf16 v[70:73], v[180:183], v[224:227], v[70:73]
	v_mfma_f32_16x16x32_bf16 v[126:129], v[176:179], v[192:195], v[126:129]
	v_mfma_f32_16x16x32_bf16 v[118:121], v[184:187], v[192:195], v[118:121]
	v_mfma_f32_16x16x32_bf16 v[110:113], v[176:179], v[212:215], v[110:113]
	v_mfma_f32_16x16x32_bf16 v[102:105], v[184:187], v[212:215], v[102:105]
	v_mfma_f32_16x16x32_bf16 v[94:97], v[176:179], v[220:223], v[94:97]
	v_mfma_f32_16x16x32_bf16 v[86:89], v[184:187], v[220:223], v[86:89]
	v_mfma_f32_16x16x32_bf16 v[78:81], v[176:179], v[228:231], v[78:81]
	s_barrier
	v_mfma_f32_16x16x32_bf16 v[70:73], v[184:187], v[228:231], v[70:73]
	s_setprio 0
	s_mov_b32 m0, s41
	s_add_u32 s76, s28, s38
	ds_read_b128 v[188:191], v145 offset:16384
	ds_read_b128 v[192:195], v145 offset:17408
	ds_read_b128 v[196:199], v145 offset:18432
	ds_read_b128 v[212:215], v145 offset:19456
	ds_read_b128 v[216:219], v145 offset:20480
	ds_read_b128 v[220:223], v145 offset:21504
	ds_read_b128 v[224:227], v145 offset:22528
	ds_read_b128 v[228:231], v145 offset:23552
	global_load_lds_dwordx4 v0, s[28:29]
	s_mov_b32 m0, s42
	s_addc_u32 s77, s29, 0
	global_load_lds_dwordx4 v130, s[28:29]
	s_mov_b32 m0, s44
	s_nop 0
	global_load_lds_dwordx4 v0, s[76:77]
	s_mov_b32 m0, s45
	s_nop 0
	global_load_lds_dwordx4 v130, s[76:77]
	s_mov_b32 m0, s46
	s_nop 0
	global_load_lds_dwordx4 v134, s[30:31]
	s_mov_b32 m0, s47
	s_nop 0
	global_load_lds_dwordx4 v132, s[30:31]
	s_waitcnt vmcnt(8)
	s_waitcnt lgkmcnt(0)
	s_barrier
	s_setprio 1
	s_waitcnt lgkmcnt(0)
	s_nop 0
	v_mfma_f32_16x16x32_bf16 v[58:61], v[146:149], v[188:191], v[58:61]
	v_mfma_f32_16x16x32_bf16 v[50:53], v[154:157], v[188:191], v[50:53]
	v_mfma_f32_16x16x32_bf16 v[42:45], v[146:149], v[196:199], v[42:45]
	v_mfma_f32_16x16x32_bf16 v[38:41], v[154:157], v[196:199], v[38:41]
	v_mfma_f32_16x16x32_bf16 v[26:29], v[146:149], v[216:219], v[26:29]
	v_mfma_f32_16x16x32_bf16 v[18:21], v[154:157], v[216:219], v[18:21]
	v_mfma_f32_16x16x32_bf16 v[10:13], v[146:149], v[224:227], v[10:13]
	v_mfma_f32_16x16x32_bf16 v[6:9], v[154:157], v[224:227], v[6:9]
	v_mfma_f32_16x16x32_bf16 v[58:61], v[150:153], v[192:195], v[58:61]
	v_mfma_f32_16x16x32_bf16 v[50:53], v[158:161], v[192:195], v[50:53]
	v_mfma_f32_16x16x32_bf16 v[42:45], v[150:153], v[212:215], v[42:45]
	v_mfma_f32_16x16x32_bf16 v[38:41], v[158:161], v[212:215], v[38:41]
	v_mfma_f32_16x16x32_bf16 v[26:29], v[150:153], v[220:223], v[26:29]
	v_mfma_f32_16x16x32_bf16 v[18:21], v[158:161], v[220:223], v[18:21]
	v_mfma_f32_16x16x32_bf16 v[10:13], v[150:153], v[228:231], v[10:13]
	v_mfma_f32_16x16x32_bf16 v[6:9], v[158:161], v[228:231], v[6:9]
	s_setprio 0
	s_setprio 1
	v_mfma_f32_16x16x32_bf16 v[62:65], v[172:175], v[188:191], v[62:65]
	v_mfma_f32_16x16x32_bf16 v[54:57], v[180:183], v[188:191], v[54:57]
	v_mfma_f32_16x16x32_bf16 v[46:49], v[172:175], v[196:199], v[46:49]
	v_mfma_f32_16x16x32_bf16 v[34:37], v[180:183], v[196:199], v[34:37]
	v_mfma_f32_16x16x32_bf16 v[30:33], v[172:175], v[216:219], v[30:33]
	v_mfma_f32_16x16x32_bf16 v[22:25], v[180:183], v[216:219], v[22:25]
	v_mfma_f32_16x16x32_bf16 v[14:17], v[172:175], v[224:227], v[14:17]
	v_mfma_f32_16x16x32_bf16 v[2:5], v[180:183], v[224:227], v[2:5]
	v_mfma_f32_16x16x32_bf16 v[62:65], v[176:179], v[192:195], v[62:65]
	v_mfma_f32_16x16x32_bf16 v[54:57], v[184:187], v[192:195], v[54:57]
	v_mfma_f32_16x16x32_bf16 v[46:49], v[176:179], v[212:215], v[46:49]
	v_mfma_f32_16x16x32_bf16 v[34:37], v[184:187], v[212:215], v[34:37]
	v_mfma_f32_16x16x32_bf16 v[30:33], v[176:179], v[220:223], v[30:33]
	v_mfma_f32_16x16x32_bf16 v[22:25], v[184:187], v[220:223], v[22:25]
	v_mfma_f32_16x16x32_bf16 v[14:17], v[176:179], v[228:231], v[14:17]
	s_barrier
	v_mfma_f32_16x16x32_bf16 v[2:5], v[184:187], v[228:231], v[2:5]
	s_setprio 0
	v_add_u32_e32 v136, s55, v141
	ds_read_b128 v[146:149], v136
	ds_read_b128 v[150:153], v136 offset:1024
	ds_read_b128 v[154:157], v136 offset:2048
	ds_read_b128 v[158:161], v136 offset:3072
	v_add_u32_e32 v136, s60, v141
	ds_read_b128 v[172:175], v136
	ds_read_b128 v[176:179], v136 offset:1024
	ds_read_b128 v[180:183], v136 offset:2048
	ds_read_b128 v[184:187], v136 offset:3072
	s_add_u32 s30, s30, s38
	s_addc_u32 s31, s31, 0
	s_mov_b32 m0, s48
	ds_read_b128 v[188:191], v145 offset:32768
	ds_read_b128 v[192:195], v145 offset:33792
	ds_read_b128 v[196:199], v145 offset:34816
	ds_read_b128 v[212:215], v145 offset:35840
	ds_read_b128 v[216:219], v145 offset:36864
	ds_read_b128 v[220:223], v145 offset:37888
	ds_read_b128 v[224:227], v145 offset:38912
	ds_read_b128 v[228:231], v145 offset:39936
	global_load_lds_dwordx4 v134, s[30:31]
	s_mov_b32 m0, s49
	s_nop 0
	global_load_lds_dwordx4 v132, s[30:31]
	s_waitcnt vmcnt(8)
	s_waitcnt lgkmcnt(0)
	s_barrier
	s_setprio 1
	s_waitcnt lgkmcnt(0)
	s_nop 0
	v_mfma_f32_16x16x32_bf16 v[122:125], v[146:149], v[188:191], v[122:125]
	v_mfma_f32_16x16x32_bf16 v[114:117], v[154:157], v[188:191], v[114:117]
	v_mfma_f32_16x16x32_bf16 v[106:109], v[146:149], v[196:199], v[106:109]
	v_mfma_f32_16x16x32_bf16 v[98:101], v[154:157], v[196:199], v[98:101]
	v_mfma_f32_16x16x32_bf16 v[90:93], v[146:149], v[216:219], v[90:93]
	v_mfma_f32_16x16x32_bf16 v[82:85], v[154:157], v[216:219], v[82:85]
	v_mfma_f32_16x16x32_bf16 v[74:77], v[146:149], v[224:227], v[74:77]
	v_mfma_f32_16x16x32_bf16 v[66:69], v[154:157], v[224:227], v[66:69]
	v_mfma_f32_16x16x32_bf16 v[122:125], v[150:153], v[192:195], v[122:125]
	v_mfma_f32_16x16x32_bf16 v[114:117], v[158:161], v[192:195], v[114:117]
	v_mfma_f32_16x16x32_bf16 v[106:109], v[150:153], v[212:215], v[106:109]
	v_mfma_f32_16x16x32_bf16 v[98:101], v[158:161], v[212:215], v[98:101]
	v_mfma_f32_16x16x32_bf16 v[90:93], v[150:153], v[220:223], v[90:93]
	v_mfma_f32_16x16x32_bf16 v[82:85], v[158:161], v[220:223], v[82:85]
	v_mfma_f32_16x16x32_bf16 v[74:77], v[150:153], v[228:231], v[74:77]
	v_mfma_f32_16x16x32_bf16 v[66:69], v[158:161], v[228:231], v[66:69]
	s_setprio 0
	s_setprio 1
	v_mfma_f32_16x16x32_bf16 v[126:129], v[172:175], v[188:191], v[126:129]
	v_mfma_f32_16x16x32_bf16 v[118:121], v[180:183], v[188:191], v[118:121]
	v_mfma_f32_16x16x32_bf16 v[110:113], v[172:175], v[196:199], v[110:113]
	v_mfma_f32_16x16x32_bf16 v[102:105], v[180:183], v[196:199], v[102:105]
	v_mfma_f32_16x16x32_bf16 v[94:97], v[172:175], v[216:219], v[94:97]
	v_mfma_f32_16x16x32_bf16 v[86:89], v[180:183], v[216:219], v[86:89]
	v_mfma_f32_16x16x32_bf16 v[78:81], v[172:175], v[224:227], v[78:81]
	v_mfma_f32_16x16x32_bf16 v[70:73], v[180:183], v[224:227], v[70:73]
	v_mfma_f32_16x16x32_bf16 v[126:129], v[176:179], v[192:195], v[126:129]
	v_mfma_f32_16x16x32_bf16 v[118:121], v[184:187], v[192:195], v[118:121]
	v_mfma_f32_16x16x32_bf16 v[110:113], v[176:179], v[212:215], v[110:113]
	v_mfma_f32_16x16x32_bf16 v[102:105], v[184:187], v[212:215], v[102:105]
	v_mfma_f32_16x16x32_bf16 v[94:97], v[176:179], v[220:223], v[94:97]
	v_mfma_f32_16x16x32_bf16 v[86:89], v[184:187], v[220:223], v[86:89]
	v_mfma_f32_16x16x32_bf16 v[78:81], v[176:179], v[228:231], v[78:81]
	s_barrier
	v_mfma_f32_16x16x32_bf16 v[70:73], v[184:187], v[228:231], v[70:73]
	s_setprio 0
	s_add_u32 s28, s28, s53
	s_addc_u32 s29, s29, 0
	s_mov_b32 m0, s56
	ds_read_b128 v[188:191], v145 offset:49152
	ds_read_b128 v[192:195], v145 offset:50176
	ds_read_b128 v[196:199], v145 offset:51200
	ds_read_b128 v[212:215], v145 offset:52224
	ds_read_b128 v[216:219], v145 offset:53248
	ds_read_b128 v[220:223], v145 offset:54272
	ds_read_b128 v[224:227], v145 offset:55296
	ds_read_b128 v[228:231], v145 offset:56320
	global_load_lds_dwordx4 v0, s[28:29]
	v_lshl_add_u64 v[136:137], s[28:29], 0, v[130:131]
	s_add_u32 s28, s28, s38
	s_mov_b32 m0, s57
	s_addc_u32 s29, s29, 0
	global_load_lds_dwordx4 v[136:137], off
	s_mov_b32 m0, s62
	s_nop 0
	global_load_lds_dwordx4 v0, s[28:29]
	s_mov_b32 m0, s63
	s_nop 0
	global_load_lds_dwordx4 v130, s[28:29]
	s_mov_b32 m0, s58
	s_nop 0
	global_load_lds_dwordx4 v134, s[26:27]
	s_mov_b32 m0, s59
	s_nop 0
	global_load_lds_dwordx4 v132, s[26:27]
	s_waitcnt vmcnt(8)
	s_waitcnt lgkmcnt(0)
	s_barrier
	s_setprio 1
	s_waitcnt lgkmcnt(0)
	s_nop 0
	v_mfma_f32_16x16x32_bf16 v[58:61], v[146:149], v[188:191], v[58:61]
	v_mfma_f32_16x16x32_bf16 v[50:53], v[154:157], v[188:191], v[50:53]
	v_mfma_f32_16x16x32_bf16 v[42:45], v[146:149], v[196:199], v[42:45]
	v_mfma_f32_16x16x32_bf16 v[38:41], v[154:157], v[196:199], v[38:41]
	v_mfma_f32_16x16x32_bf16 v[26:29], v[146:149], v[216:219], v[26:29]
	v_mfma_f32_16x16x32_bf16 v[18:21], v[154:157], v[216:219], v[18:21]
	v_mfma_f32_16x16x32_bf16 v[10:13], v[146:149], v[224:227], v[10:13]
	v_mfma_f32_16x16x32_bf16 v[6:9], v[154:157], v[224:227], v[6:9]
	v_mfma_f32_16x16x32_bf16 v[58:61], v[150:153], v[192:195], v[58:61]
	v_mfma_f32_16x16x32_bf16 v[50:53], v[158:161], v[192:195], v[50:53]
	v_mfma_f32_16x16x32_bf16 v[42:45], v[150:153], v[212:215], v[42:45]
	v_mfma_f32_16x16x32_bf16 v[38:41], v[158:161], v[212:215], v[38:41]
	v_mfma_f32_16x16x32_bf16 v[26:29], v[150:153], v[220:223], v[26:29]
	v_mfma_f32_16x16x32_bf16 v[18:21], v[158:161], v[220:223], v[18:21]
	v_mfma_f32_16x16x32_bf16 v[10:13], v[150:153], v[228:231], v[10:13]
	v_mfma_f32_16x16x32_bf16 v[6:9], v[158:161], v[228:231], v[6:9]
	s_setprio 0
	s_setprio 1
	v_mfma_f32_16x16x32_bf16 v[62:65], v[172:175], v[188:191], v[62:65]
	v_mfma_f32_16x16x32_bf16 v[54:57], v[180:183], v[188:191], v[54:57]
	v_mfma_f32_16x16x32_bf16 v[46:49], v[172:175], v[196:199], v[46:49]
	v_mfma_f32_16x16x32_bf16 v[34:37], v[180:183], v[196:199], v[34:37]
	v_mfma_f32_16x16x32_bf16 v[30:33], v[172:175], v[216:219], v[30:33]
	v_mfma_f32_16x16x32_bf16 v[22:25], v[180:183], v[216:219], v[22:25]
	v_mfma_f32_16x16x32_bf16 v[14:17], v[172:175], v[224:227], v[14:17]
	v_mfma_f32_16x16x32_bf16 v[2:5], v[180:183], v[224:227], v[2:5]
	v_mfma_f32_16x16x32_bf16 v[62:65], v[176:179], v[192:195], v[62:65]
	v_mfma_f32_16x16x32_bf16 v[54:57], v[184:187], v[192:195], v[54:57]
	v_mfma_f32_16x16x32_bf16 v[46:49], v[176:179], v[212:215], v[46:49]
	v_mfma_f32_16x16x32_bf16 v[34:37], v[184:187], v[212:215], v[34:37]
	v_mfma_f32_16x16x32_bf16 v[30:33], v[176:179], v[220:223], v[30:33]
	v_mfma_f32_16x16x32_bf16 v[22:25], v[184:187], v[220:223], v[22:25]
	v_mfma_f32_16x16x32_bf16 v[14:17], v[176:179], v[228:231], v[14:17]
	s_barrier
	v_mfma_f32_16x16x32_bf16 v[2:5], v[184:187], v[228:231], v[2:5]
	s_setprio 0
	s_add_i32 s75, s75, 2
	s_cmp_ge_i32 s75, s51
	s_cbranch_scc0 .LBB0_2802

.LBB0_2886:
	s_add_i32 s26, s4, s73
	s_add_i32 s24, s26, 1
	s_cmp_ge_i32 s24, s49
	s_cselect_b32 s25, s49, 0
	s_sub_i32 s24, s24, s25
	s_ashr_i32 s25, s24, 31
	s_lshl_b64 s[74:75], s[24:25], s38
	s_add_i32 s26, s26, 2
	s_cmp_ge_i32 s26, s49
	s_cselect_b32 s24, s49, 0
	s_sub_i32 s24, s26, s24
	s_ashr_i32 s25, s24, 31
	s_lshl_b64 s[24:25], s[24:25], s38
	v_add_u32_e32 v144, s5, v155
	v_add_u32_e32 v152, s41, v155
	s_add_u32 s26, s20, s24
	ds_read_b128 v[132:135], v144
	ds_read_b128 v[136:139], v144 offset:1024
	ds_read_b128 v[140:143], v144 offset:2048
	ds_read_b128 v[144:147], v144 offset:3072
	ds_read_b128 v[148:151], v152
	ds_read_b128 v[158:161], v152 offset:1024
	ds_read_b128 v[172:175], v152 offset:2048
	ds_read_b128 v[176:179], v152 offset:3072
	s_addc_u32 s27, s21, s25
	s_add_u32 s24, s22, s24
	s_addc_u32 s25, s23, s25
	s_cmp_eq_u32 s50, s73
	s_cselect_b32 s28, s69, s26
	s_cselect_b32 s29, s70, s27
	s_cselect_b32 s27, s72, s25
	s_cselect_b32 s26, s71, s24
	s_add_u32 s24, s28, s51
	s_addc_u32 s25, s29, 0
	s_add_u32 s74, s67, s74
	s_addc_u32 s75, s68, s75
	s_add_i32 m0, s44, 0xc000
	ds_read_b128 v[180:183], v157
	ds_read_b128 v[184:187], v157 offset:1024
	ds_read_b128 v[188:191], v157 offset:2048
	ds_read_b128 v[192:195], v157 offset:3072
	ds_read_b128 v[196:199], v157 offset:4096
	ds_read_b128 v[212:215], v157 offset:5120
	ds_read_b128 v[216:219], v157 offset:6144
	ds_read_b128 v[220:223], v157 offset:7168
	global_load_lds_dwordx4 v0, s[74:75]
	s_add_i32 m0, s44, 0xe000
	s_nop 0
	global_load_lds_dwordx4 v130, s[74:75]
	s_waitcnt vmcnt(8)
	s_waitcnt lgkmcnt(0)
	s_barrier
	s_setprio 1
	s_waitcnt lgkmcnt(0)
	s_nop 0
	v_mfma_f32_16x16x32_bf16 v[126:129], v[132:135], v[180:183], v[126:129]
	v_mfma_f32_16x16x32_bf16 v[122:125], v[140:143], v[180:183], v[122:125]
	v_mfma_f32_16x16x32_bf16 v[110:113], v[132:135], v[188:191], v[110:113]
	v_mfma_f32_16x16x32_bf16 v[106:109], v[140:143], v[188:191], v[106:109]
	v_mfma_f32_16x16x32_bf16 v[94:97], v[132:135], v[196:199], v[94:97]
	v_mfma_f32_16x16x32_bf16 v[90:93], v[140:143], v[196:199], v[90:93]
	v_mfma_f32_16x16x32_bf16 v[78:81], v[132:135], v[216:219], v[78:81]
	v_mfma_f32_16x16x32_bf16 v[74:77], v[140:143], v[216:219], v[74:77]
	v_mfma_f32_16x16x32_bf16 v[126:129], v[136:139], v[184:187], v[126:129]
	v_mfma_f32_16x16x32_bf16 v[122:125], v[144:147], v[184:187], v[122:125]
	v_mfma_f32_16x16x32_bf16 v[110:113], v[136:139], v[192:195], v[110:113]
	v_mfma_f32_16x16x32_bf16 v[106:109], v[144:147], v[192:195], v[106:109]
	v_mfma_f32_16x16x32_bf16 v[94:97], v[136:139], v[212:215], v[94:97]
	v_mfma_f32_16x16x32_bf16 v[90:93], v[144:147], v[212:215], v[90:93]
	v_mfma_f32_16x16x32_bf16 v[78:81], v[136:139], v[220:223], v[78:81]
	v_mfma_f32_16x16x32_bf16 v[74:77], v[144:147], v[220:223], v[74:77]
	s_setprio 0
	s_setprio 1
	v_mfma_f32_16x16x32_bf16 v[118:121], v[148:151], v[180:183], v[118:121]
	v_mfma_f32_16x16x32_bf16 v[114:117], v[172:175], v[180:183], v[114:117]
	v_mfma_f32_16x16x32_bf16 v[102:105], v[148:151], v[188:191], v[102:105]
	v_mfma_f32_16x16x32_bf16 v[98:101], v[172:175], v[188:191], v[98:101]
	v_mfma_f32_16x16x32_bf16 v[86:89], v[148:151], v[196:199], v[86:89]
	v_mfma_f32_16x16x32_bf16 v[82:85], v[172:175], v[196:199], v[82:85]
	v_mfma_f32_16x16x32_bf16 v[70:73], v[148:151], v[216:219], v[70:73]
	v_mfma_f32_16x16x32_bf16 v[66:69], v[172:175], v[216:219], v[66:69]
	v_mfma_f32_16x16x32_bf16 v[118:121], v[158:161], v[184:187], v[118:121]
	v_mfma_f32_16x16x32_bf16 v[114:117], v[176:179], v[184:187], v[114:117]
	v_mfma_f32_16x16x32_bf16 v[102:105], v[158:161], v[192:195], v[102:105]
	v_mfma_f32_16x16x32_bf16 v[98:101], v[176:179], v[192:195], v[98:101]
	v_mfma_f32_16x16x32_bf16 v[86:89], v[158:161], v[212:215], v[86:89]
	v_mfma_f32_16x16x32_bf16 v[82:85], v[176:179], v[212:215], v[82:85]
	v_mfma_f32_16x16x32_bf16 v[70:73], v[158:161], v[220:223], v[70:73]
	s_barrier
	v_mfma_f32_16x16x32_bf16 v[66:69], v[176:179], v[220:223], v[66:69]
	s_setprio 0
	s_mov_b32 m0, s39
	s_add_u32 s74, s26, s37
	ds_read_b128 v[180:183], v157 offset:16384
	ds_read_b128 v[184:187], v157 offset:17408
	ds_read_b128 v[188:191], v157 offset:18432
	ds_read_b128 v[192:195], v157 offset:19456
	ds_read_b128 v[196:199], v157 offset:20480
	ds_read_b128 v[212:215], v157 offset:21504
	ds_read_b128 v[216:219], v157 offset:22528
	ds_read_b128 v[220:223], v157 offset:23552
	global_load_lds_dwordx4 v0, s[26:27]
	s_mov_b32 m0, s40
	s_addc_u32 s75, s27, 0
	global_load_lds_dwordx4 v130, s[26:27]
	s_mov_b32 m0, s42
	s_nop 0
	global_load_lds_dwordx4 v0, s[74:75]
	s_mov_b32 m0, s43
	s_nop 0
	global_load_lds_dwordx4 v130, s[74:75]
	s_mov_b32 m0, s44
	s_nop 0
	global_load_lds_dwordx4 v0, s[28:29]
	s_mov_b32 m0, s45
	s_nop 0
	global_load_lds_dwordx4 v130, s[28:29]
	s_waitcnt vmcnt(8)
	s_waitcnt lgkmcnt(0)
	s_barrier
	s_setprio 1
	s_waitcnt lgkmcnt(0)
	s_nop 0
	v_mfma_f32_16x16x32_bf16 v[62:65], v[132:135], v[180:183], v[62:65]
	v_mfma_f32_16x16x32_bf16 v[58:61], v[140:143], v[180:183], v[58:61]
	v_mfma_f32_16x16x32_bf16 v[46:49], v[132:135], v[188:191], v[46:49]
	v_mfma_f32_16x16x32_bf16 v[42:45], v[140:143], v[188:191], v[42:45]
	v_mfma_f32_16x16x32_bf16 v[30:33], v[132:135], v[196:199], v[30:33]
	v_mfma_f32_16x16x32_bf16 v[26:29], v[140:143], v[196:199], v[26:29]
	v_mfma_f32_16x16x32_bf16 v[14:17], v[132:135], v[216:219], v[14:17]
	v_mfma_f32_16x16x32_bf16 v[10:13], v[140:143], v[216:219], v[10:13]
	v_mfma_f32_16x16x32_bf16 v[62:65], v[136:139], v[184:187], v[62:65]
	v_mfma_f32_16x16x32_bf16 v[58:61], v[144:147], v[184:187], v[58:61]
	v_mfma_f32_16x16x32_bf16 v[46:49], v[136:139], v[192:195], v[46:49]
	v_mfma_f32_16x16x32_bf16 v[42:45], v[144:147], v[192:195], v[42:45]
	v_mfma_f32_16x16x32_bf16 v[30:33], v[136:139], v[212:215], v[30:33]
	v_mfma_f32_16x16x32_bf16 v[26:29], v[144:147], v[212:215], v[26:29]
	v_mfma_f32_16x16x32_bf16 v[14:17], v[136:139], v[220:223], v[14:17]
	v_mfma_f32_16x16x32_bf16 v[10:13], v[144:147], v[220:223], v[10:13]
	s_setprio 0
	s_setprio 1
	v_mfma_f32_16x16x32_bf16 v[54:57], v[148:151], v[180:183], v[54:57]
	v_mfma_f32_16x16x32_bf16 v[50:53], v[172:175], v[180:183], v[50:53]
	v_mfma_f32_16x16x32_bf16 v[38:41], v[148:151], v[188:191], v[38:41]
	v_mfma_f32_16x16x32_bf16 v[34:37], v[172:175], v[188:191], v[34:37]
	v_mfma_f32_16x16x32_bf16 v[22:25], v[148:151], v[196:199], v[22:25]
	v_mfma_f32_16x16x32_bf16 v[18:21], v[172:175], v[196:199], v[18:21]
	v_mfma_f32_16x16x32_bf16 v[6:9], v[148:151], v[216:219], v[6:9]
	v_mfma_f32_16x16x32_bf16 v[2:5], v[172:175], v[216:219], v[2:5]
	v_mfma_f32_16x16x32_bf16 v[54:57], v[158:161], v[184:187], v[54:57]
	v_mfma_f32_16x16x32_bf16 v[50:53], v[176:179], v[184:187], v[50:53]
	v_mfma_f32_16x16x32_bf16 v[38:41], v[158:161], v[192:195], v[38:41]
	v_mfma_f32_16x16x32_bf16 v[34:37], v[176:179], v[192:195], v[34:37]
	v_mfma_f32_16x16x32_bf16 v[22:25], v[158:161], v[212:215], v[22:25]
	v_mfma_f32_16x16x32_bf16 v[18:21], v[176:179], v[212:215], v[18:21]
	v_mfma_f32_16x16x32_bf16 v[6:9], v[158:161], v[220:223], v[6:9]
	s_barrier
	v_mfma_f32_16x16x32_bf16 v[2:5], v[176:179], v[220:223], v[2:5]
	s_setprio 0
	v_add_u32_e32 v144, s53, v155
	v_add_u32_e32 v152, s58, v155
	ds_read_b128 v[132:135], v144
	ds_read_b128 v[136:139], v144 offset:1024
	ds_read_b128 v[140:143], v144 offset:2048
	ds_read_b128 v[144:147], v144 offset:3072
	ds_read_b128 v[148:151], v152
	ds_read_b128 v[158:161], v152 offset:1024
	ds_read_b128 v[172:175], v152 offset:2048
	ds_read_b128 v[176:179], v152 offset:3072
	s_add_u32 s28, s28, s37
	s_addc_u32 s29, s29, 0
	s_mov_b32 m0, s46
	ds_read_b128 v[180:183], v157 offset:32768
	ds_read_b128 v[184:187], v157 offset:33792
	ds_read_b128 v[188:191], v157 offset:34816
	ds_read_b128 v[192:195], v157 offset:35840
	ds_read_b128 v[196:199], v157 offset:36864
	ds_read_b128 v[212:215], v157 offset:37888
	ds_read_b128 v[216:219], v157 offset:38912
	ds_read_b128 v[220:223], v157 offset:39936
	global_load_lds_dwordx4 v0, s[28:29]
	s_mov_b32 m0, s47
	s_nop 0
	global_load_lds_dwordx4 v130, s[28:29]
	s_waitcnt vmcnt(8)
	s_waitcnt lgkmcnt(0)
	s_barrier
	s_setprio 1
	s_waitcnt lgkmcnt(0)
	s_nop 0
	v_mfma_f32_16x16x32_bf16 v[126:129], v[132:135], v[180:183], v[126:129]
	v_mfma_f32_16x16x32_bf16 v[122:125], v[140:143], v[180:183], v[122:125]
	v_mfma_f32_16x16x32_bf16 v[110:113], v[132:135], v[188:191], v[110:113]
	v_mfma_f32_16x16x32_bf16 v[106:109], v[140:143], v[188:191], v[106:109]
	v_mfma_f32_16x16x32_bf16 v[94:97], v[132:135], v[196:199], v[94:97]
	v_mfma_f32_16x16x32_bf16 v[90:93], v[140:143], v[196:199], v[90:93]
	v_mfma_f32_16x16x32_bf16 v[78:81], v[132:135], v[216:219], v[78:81]
	v_mfma_f32_16x16x32_bf16 v[74:77], v[140:143], v[216:219], v[74:77]
	v_mfma_f32_16x16x32_bf16 v[126:129], v[136:139], v[184:187], v[126:129]
	v_mfma_f32_16x16x32_bf16 v[122:125], v[144:147], v[184:187], v[122:125]
	v_mfma_f32_16x16x32_bf16 v[110:113], v[136:139], v[192:195], v[110:113]
	v_mfma_f32_16x16x32_bf16 v[106:109], v[144:147], v[192:195], v[106:109]
	v_mfma_f32_16x16x32_bf16 v[94:97], v[136:139], v[212:215], v[94:97]
	v_mfma_f32_16x16x32_bf16 v[90:93], v[144:147], v[212:215], v[90:93]
	v_mfma_f32_16x16x32_bf16 v[78:81], v[136:139], v[220:223], v[78:81]
	v_mfma_f32_16x16x32_bf16 v[74:77], v[144:147], v[220:223], v[74:77]
	s_setprio 0
	s_setprio 1
	v_mfma_f32_16x16x32_bf16 v[118:121], v[148:151], v[180:183], v[118:121]
	v_mfma_f32_16x16x32_bf16 v[114:117], v[172:175], v[180:183], v[114:117]
	v_mfma_f32_16x16x32_bf16 v[102:105], v[148:151], v[188:191], v[102:105]
	v_mfma_f32_16x16x32_bf16 v[98:101], v[172:175], v[188:191], v[98:101]
	v_mfma_f32_16x16x32_bf16 v[86:89], v[148:151], v[196:199], v[86:89]
	v_mfma_f32_16x16x32_bf16 v[82:85], v[172:175], v[196:199], v[82:85]
	v_mfma_f32_16x16x32_bf16 v[70:73], v[148:151], v[216:219], v[70:73]
	v_mfma_f32_16x16x32_bf16 v[66:69], v[172:175], v[216:219], v[66:69]
	v_mfma_f32_16x16x32_bf16 v[118:121], v[158:161], v[184:187], v[118:121]
	v_mfma_f32_16x16x32_bf16 v[114:117], v[176:179], v[184:187], v[114:117]
	v_mfma_f32_16x16x32_bf16 v[102:105], v[158:161], v[192:195], v[102:105]
	v_mfma_f32_16x16x32_bf16 v[98:101], v[176:179], v[192:195], v[98:101]
	v_mfma_f32_16x16x32_bf16 v[86:89], v[158:161], v[212:215], v[86:89]
	v_mfma_f32_16x16x32_bf16 v[82:85], v[176:179], v[212:215], v[82:85]
	v_mfma_f32_16x16x32_bf16 v[70:73], v[158:161], v[220:223], v[70:73]
	s_barrier
	v_mfma_f32_16x16x32_bf16 v[66:69], v[176:179], v[220:223], v[66:69]
	s_setprio 0
	s_add_u32 s26, s26, s51
	s_addc_u32 s27, s27, 0
	s_mov_b32 m0, s54
	ds_read_b128 v[180:183], v157 offset:49152
	ds_read_b128 v[184:187], v157 offset:50176
	ds_read_b128 v[188:191], v157 offset:51200
	ds_read_b128 v[192:195], v157 offset:52224
	ds_read_b128 v[196:199], v157 offset:53248
	ds_read_b128 v[212:215], v157 offset:54272
	ds_read_b128 v[216:219], v157 offset:55296
	ds_read_b128 v[220:223], v157 offset:56320
	global_load_lds_dwordx4 v0, s[26:27]
	v_lshl_add_u64 v[152:153], s[26:27], 0, v[130:131]
	s_add_u32 s26, s26, s37
	s_mov_b32 m0, s55
	s_addc_u32 s27, s27, 0
	global_load_lds_dwordx4 v[152:153], off
	s_mov_b32 m0, s59
	s_nop 0
	global_load_lds_dwordx4 v0, s[26:27]
	s_mov_b32 m0, s60
	s_nop 0
	global_load_lds_dwordx4 v130, s[26:27]
	s_mov_b32 m0, s56
	s_nop 0
	global_load_lds_dwordx4 v0, s[24:25]
	s_mov_b32 m0, s57
	s_nop 0
	global_load_lds_dwordx4 v130, s[24:25]
	s_waitcnt vmcnt(8)
	s_waitcnt lgkmcnt(0)
	s_barrier
	s_setprio 1
	s_waitcnt lgkmcnt(0)
	s_nop 0
	v_mfma_f32_16x16x32_bf16 v[62:65], v[132:135], v[180:183], v[62:65]
	v_mfma_f32_16x16x32_bf16 v[58:61], v[140:143], v[180:183], v[58:61]
	v_mfma_f32_16x16x32_bf16 v[46:49], v[132:135], v[188:191], v[46:49]
	v_mfma_f32_16x16x32_bf16 v[42:45], v[140:143], v[188:191], v[42:45]
	v_mfma_f32_16x16x32_bf16 v[30:33], v[132:135], v[196:199], v[30:33]
	v_mfma_f32_16x16x32_bf16 v[26:29], v[140:143], v[196:199], v[26:29]
	v_mfma_f32_16x16x32_bf16 v[14:17], v[132:135], v[216:219], v[14:17]
	v_mfma_f32_16x16x32_bf16 v[10:13], v[140:143], v[216:219], v[10:13]
	v_mfma_f32_16x16x32_bf16 v[62:65], v[136:139], v[184:187], v[62:65]
	v_mfma_f32_16x16x32_bf16 v[58:61], v[144:147], v[184:187], v[58:61]
	v_mfma_f32_16x16x32_bf16 v[46:49], v[136:139], v[192:195], v[46:49]
	v_mfma_f32_16x16x32_bf16 v[42:45], v[144:147], v[192:195], v[42:45]
	v_mfma_f32_16x16x32_bf16 v[30:33], v[136:139], v[212:215], v[30:33]
	v_mfma_f32_16x16x32_bf16 v[26:29], v[144:147], v[212:215], v[26:29]
	v_mfma_f32_16x16x32_bf16 v[14:17], v[136:139], v[220:223], v[14:17]
	v_mfma_f32_16x16x32_bf16 v[10:13], v[144:147], v[220:223], v[10:13]
	s_setprio 0
	s_setprio 1
	v_mfma_f32_16x16x32_bf16 v[54:57], v[148:151], v[180:183], v[54:57]
	v_mfma_f32_16x16x32_bf16 v[50:53], v[172:175], v[180:183], v[50:53]
	v_mfma_f32_16x16x32_bf16 v[38:41], v[148:151], v[188:191], v[38:41]
	v_mfma_f32_16x16x32_bf16 v[34:37], v[172:175], v[188:191], v[34:37]
	v_mfma_f32_16x16x32_bf16 v[22:25], v[148:151], v[196:199], v[22:25]
	v_mfma_f32_16x16x32_bf16 v[18:21], v[172:175], v[196:199], v[18:21]
	v_mfma_f32_16x16x32_bf16 v[6:9], v[148:151], v[216:219], v[6:9]
	v_mfma_f32_16x16x32_bf16 v[2:5], v[172:175], v[216:219], v[2:5]
	v_mfma_f32_16x16x32_bf16 v[54:57], v[158:161], v[184:187], v[54:57]
	v_mfma_f32_16x16x32_bf16 v[50:53], v[176:179], v[184:187], v[50:53]
	v_mfma_f32_16x16x32_bf16 v[38:41], v[158:161], v[192:195], v[38:41]
	v_mfma_f32_16x16x32_bf16 v[34:37], v[176:179], v[192:195], v[34:37]
	v_mfma_f32_16x16x32_bf16 v[22:25], v[158:161], v[212:215], v[22:25]
	v_mfma_f32_16x16x32_bf16 v[18:21], v[176:179], v[212:215], v[18:21]
	v_mfma_f32_16x16x32_bf16 v[6:9], v[158:161], v[220:223], v[6:9]
	s_barrier
	v_mfma_f32_16x16x32_bf16 v[2:5], v[176:179], v[220:223], v[2:5]
	s_setprio 0
	s_add_i32 s73, s73, 2
	s_cmp_ge_i32 s73, s49
	s_cbranch_scc0 .LBB0_2886
